# baseline (speedup 1.0000x reference)
.LBB7_27:
	ds_read_b128 v[128:131], v170
	ds_read_b128 v[132:135], v170 offset:1024
	ds_read_b128 v[136:139], v170 offset:2048
	ds_read_b128 v[140:143], v170 offset:3072
	s_add_u32 s30, s28, 0xfffd0080
	s_addc_u32 s31, s29, -1
	s_cmp_eq_u32 s73, 8
	s_cselect_b32 s35, s9, s31
	s_cselect_b32 s34, s8, s30
	s_cselect_b32 s31, s1, s72
	s_cselect_b32 s30, s0, s71
	v_lshl_add_u64 v[162:163], s[28:29], 0, v[152:153]
	s_add_i32 m0, s43, 0xc000
	ds_read_b128 v[158:161], v171
	ds_read_b128 v[176:179], v171 offset:1024
	ds_read_b128 v[180:183], v171 offset:2048
	ds_read_b128 v[184:187], v171 offset:3072
	ds_read_b128 v[188:191], v171 offset:4096
	ds_read_b128 v[192:195], v171 offset:5120
	ds_read_b128 v[196:199], v171 offset:6144
	ds_read_b128 v[200:203], v171 offset:7168
	global_load_lds_dwordx4 v[162:163], off
	v_lshl_add_u64 v[162:163], s[28:29], 0, v[154:155]
	s_add_i32 m0, s43, 0xe000
	s_nop 0
	global_load_lds_dwordx4 v[162:163], off
	s_waitcnt lgkmcnt(8)
	s_barrier
	s_waitcnt lgkmcnt(0)
	v_mfma_f32_16x16x32_f16 v[124:127], v[128:131], v[158:161], v[124:127]
	v_mfma_f32_16x16x32_f16 v[120:123], v[136:139], v[158:161], v[120:123]
	v_mfma_f32_16x16x32_f16 v[108:111], v[128:131], v[180:183], v[108:111]
	v_mfma_f32_16x16x32_f16 v[104:107], v[136:139], v[180:183], v[104:107]
	v_mfma_f32_16x16x32_f16 v[96:99], v[128:131], v[188:191], v[96:99]
	v_mfma_f32_16x16x32_f16 v[88:91], v[136:139], v[188:191], v[88:91]
	v_mfma_f32_16x16x32_f16 v[80:83], v[128:131], v[196:199], v[80:83]
	v_mfma_f32_16x16x32_f16 v[72:75], v[136:139], v[196:199], v[72:75]
	v_mfma_f32_16x16x32_f16 v[124:127], v[132:135], v[176:179], v[124:127]
	v_mfma_f32_16x16x32_f16 v[120:123], v[140:143], v[176:179], v[120:123]
	v_mfma_f32_16x16x32_f16 v[108:111], v[132:135], v[184:187], v[108:111]
	v_mfma_f32_16x16x32_f16 v[104:107], v[140:143], v[184:187], v[104:107]
	v_mfma_f32_16x16x32_f16 v[96:99], v[132:135], v[192:195], v[96:99]
	v_mfma_f32_16x16x32_f16 v[88:91], v[140:143], v[192:195], v[88:91]
	v_mfma_f32_16x16x32_f16 v[80:83], v[132:135], v[200:203], v[80:83]
	v_mfma_f32_16x16x32_f16 v[72:75], v[140:143], v[200:203], v[72:75]
	s_barrier
	s_add_i32 s74, s65, s42
	v_lshl_add_u64 v[162:163], s[30:31], 0, v[146:147]
	s_mov_b32 m0, s74
	ds_read_b128 v[204:207], v172
	ds_read_b128 v[208:211], v172 offset:1024
	ds_read_b128 v[212:215], v172 offset:2048
	ds_read_b128 v[216:219], v172 offset:3072
	global_load_lds_dwordx4 v[162:163], off
	v_lshl_add_u64 v[220:221], s[30:31], 0, v[150:151]
	s_add_i32 m0, s74, 0x2000
	s_nop 0
	global_load_lds_dwordx4 v[220:221], off
	s_barrier
	s_waitcnt lgkmcnt(0)
	v_mfma_f32_16x16x32_f16 v[116:119], v[204:207], v[158:161], v[116:119]
	v_mfma_f32_16x16x32_f16 v[112:115], v[212:215], v[158:161], v[112:115]
	v_mfma_f32_16x16x32_f16 v[100:103], v[204:207], v[180:183], v[100:103]
	v_mfma_f32_16x16x32_f16 v[92:95], v[212:215], v[180:183], v[92:95]
	v_mfma_f32_16x16x32_f16 v[84:87], v[204:207], v[188:191], v[84:87]
	v_mfma_f32_16x16x32_f16 v[76:79], v[212:215], v[188:191], v[76:79]
	v_mfma_f32_16x16x32_f16 v[68:71], v[204:207], v[196:199], v[68:71]
	v_mfma_f32_16x16x32_f16 v[64:67], v[212:215], v[196:199], v[64:67]
	v_mfma_f32_16x16x32_f16 v[116:119], v[208:211], v[176:179], v[116:119]
	v_mfma_f32_16x16x32_f16 v[112:115], v[216:219], v[176:179], v[112:115]
	v_mfma_f32_16x16x32_f16 v[100:103], v[208:211], v[184:187], v[100:103]
	v_mfma_f32_16x16x32_f16 v[92:95], v[216:219], v[184:187], v[92:95]
	v_mfma_f32_16x16x32_f16 v[84:87], v[208:211], v[192:195], v[84:87]
	v_mfma_f32_16x16x32_f16 v[76:79], v[216:219], v[192:195], v[76:79]
	v_mfma_f32_16x16x32_f16 v[68:71], v[208:211], v[200:203], v[68:71]
	v_mfma_f32_16x16x32_f16 v[64:67], v[216:219], v[200:203], v[64:67]
	s_barrier
	s_mov_b32 m0, s43
	v_lshl_add_u64 v[222:223], s[34:35], 0, v[144:145]
	ds_read_b128 v[158:161], v171 offset:16384
	ds_read_b128 v[176:179], v171 offset:17408
	ds_read_b128 v[180:183], v171 offset:18432
	ds_read_b128 v[184:187], v171 offset:19456
	ds_read_b128 v[188:191], v171 offset:20480
	ds_read_b128 v[192:195], v171 offset:21504
	ds_read_b128 v[196:199], v171 offset:22528
	ds_read_b128 v[200:203], v171 offset:23552
	global_load_lds_dwordx4 v[222:223], off
	v_lshl_add_u64 v[224:225], s[34:35], 0, v[148:149]
	s_mov_b32 m0, s44
	s_nop 0
	global_load_lds_dwordx4 v[224:225], off
	s_barrier
	s_waitcnt lgkmcnt(0)
	v_mfma_f32_16x16x32_f16 v[60:63], v[128:131], v[158:161], v[60:63]
	v_mfma_f32_16x16x32_f16 v[56:59], v[136:139], v[158:161], v[56:59]
	v_mfma_f32_16x16x32_f16 v[48:51], v[128:131], v[180:183], v[48:51]
	v_mfma_f32_16x16x32_f16 v[40:43], v[136:139], v[180:183], v[40:43]
	v_mfma_f32_16x16x32_f16 v[32:35], v[128:131], v[188:191], v[32:35]
	v_mfma_f32_16x16x32_f16 v[24:27], v[136:139], v[188:191], v[24:27]
	v_mfma_f32_16x16x32_f16 v[16:19], v[128:131], v[196:199], v[16:19]
	v_mfma_f32_16x16x32_f16 v[8:11], v[136:139], v[196:199], v[8:11]
	v_mfma_f32_16x16x32_f16 v[60:63], v[132:135], v[176:179], v[60:63]
	v_mfma_f32_16x16x32_f16 v[56:59], v[140:143], v[176:179], v[56:59]
	v_mfma_f32_16x16x32_f16 v[48:51], v[132:135], v[184:187], v[48:51]
	v_mfma_f32_16x16x32_f16 v[40:43], v[140:143], v[184:187], v[40:43]
	v_mfma_f32_16x16x32_f16 v[32:35], v[132:135], v[192:195], v[32:35]
	v_mfma_f32_16x16x32_f16 v[24:27], v[140:143], v[192:195], v[24:27]
	v_mfma_f32_16x16x32_f16 v[16:19], v[132:135], v[200:203], v[16:19]
	v_mfma_f32_16x16x32_f16 v[8:11], v[140:143], v[200:203], v[8:11]
	s_barrier
	s_add_u32 s74, s30, 0xc000
	s_addc_u32 s75, s31, 0
	s_add_i32 s76, s66, s42
	v_lshl_add_u64 v[128:129], s[74:75], 0, v[146:147]
	s_mov_b32 m0, s76
	s_nop 0
	global_load_lds_dwordx4 v[128:129], off
	v_lshl_add_u64 v[128:129], s[74:75], 0, v[150:151]
	s_add_i32 m0, s76, 0x2000
	s_nop 0
	global_load_lds_dwordx4 v[128:129], off
	s_waitcnt vmcnt(6)
	s_barrier
	v_mfma_f32_16x16x32_f16 v[52:55], v[204:207], v[158:161], v[52:55]
	v_mfma_f32_16x16x32_f16 v[44:47], v[212:215], v[158:161], v[44:47]
	v_mfma_f32_16x16x32_f16 v[36:39], v[204:207], v[180:183], v[36:39]
	v_mfma_f32_16x16x32_f16 v[28:31], v[212:215], v[180:183], v[28:31]
	v_mfma_f32_16x16x32_f16 v[20:23], v[204:207], v[188:191], v[20:23]
	v_mfma_f32_16x16x32_f16 v[12:15], v[212:215], v[188:191], v[12:15]
	v_mfma_f32_16x16x32_f16 v[4:7], v[204:207], v[196:199], v[4:7]
	v_mfma_f32_16x16x32_f16 v[0:3], v[212:215], v[196:199], v[0:3]
	v_mfma_f32_16x16x32_f16 v[52:55], v[208:211], v[176:179], v[52:55]
	v_mfma_f32_16x16x32_f16 v[44:47], v[216:219], v[176:179], v[44:47]
	v_mfma_f32_16x16x32_f16 v[36:39], v[208:211], v[184:187], v[36:39]
	v_mfma_f32_16x16x32_f16 v[28:31], v[216:219], v[184:187], v[28:31]
	v_mfma_f32_16x16x32_f16 v[20:23], v[208:211], v[192:195], v[20:23]
	v_mfma_f32_16x16x32_f16 v[12:15], v[216:219], v[192:195], v[12:15]
	v_mfma_f32_16x16x32_f16 v[4:7], v[208:211], v[200:203], v[4:7]
	v_mfma_f32_16x16x32_f16 v[0:3], v[216:219], v[200:203], v[0:3]
	s_barrier
	s_add_i32 s74, 0, 0x18000
	v_add_u32_e32 v140, s74, v166
	ds_read_b128 v[128:131], v140
	ds_read_b128 v[132:135], v140 offset:1024
	ds_read_b128 v[136:139], v140 offset:2048
	ds_read_b128 v[140:143], v140 offset:3072
	s_add_u32 s34, s34, 0x30000
	s_addc_u32 s35, s35, 0
	s_mov_b32 m0, s45
	v_lshl_add_u64 v[204:205], s[34:35], 0, v[144:145]
	ds_read_b128 v[158:161], v171 offset:32768
	ds_read_b128 v[176:179], v171 offset:33792
	ds_read_b128 v[180:183], v171 offset:34816
	ds_read_b128 v[184:187], v171 offset:35840
	ds_read_b128 v[188:191], v171 offset:36864
	ds_read_b128 v[192:195], v171 offset:37888
	ds_read_b128 v[196:199], v171 offset:38912
	ds_read_b128 v[200:203], v171 offset:39936
	global_load_lds_dwordx4 v[204:205], off
	v_lshl_add_u64 v[204:205], s[34:35], 0, v[148:149]
	s_mov_b32 m0, s46
	s_nop 0
	global_load_lds_dwordx4 v[204:205], off
	s_waitcnt lgkmcnt(8)
	s_barrier
	s_waitcnt lgkmcnt(0)
	v_mfma_f32_16x16x32_f16 v[124:127], v[128:131], v[158:161], v[124:127]
	v_mfma_f32_16x16x32_f16 v[120:123], v[136:139], v[158:161], v[120:123]
	v_mfma_f32_16x16x32_f16 v[108:111], v[128:131], v[180:183], v[108:111]
	v_mfma_f32_16x16x32_f16 v[104:107], v[136:139], v[180:183], v[104:107]
	v_mfma_f32_16x16x32_f16 v[96:99], v[128:131], v[188:191], v[96:99]
	v_mfma_f32_16x16x32_f16 v[88:91], v[136:139], v[188:191], v[88:91]
	v_mfma_f32_16x16x32_f16 v[80:83], v[128:131], v[196:199], v[80:83]
	v_mfma_f32_16x16x32_f16 v[72:75], v[136:139], v[196:199], v[72:75]
	v_mfma_f32_16x16x32_f16 v[124:127], v[132:135], v[176:179], v[124:127]
	v_mfma_f32_16x16x32_f16 v[120:123], v[140:143], v[176:179], v[120:123]
	v_mfma_f32_16x16x32_f16 v[108:111], v[132:135], v[184:187], v[108:111]
	v_mfma_f32_16x16x32_f16 v[104:107], v[140:143], v[184:187], v[104:107]
	v_mfma_f32_16x16x32_f16 v[96:99], v[132:135], v[192:195], v[96:99]
	v_mfma_f32_16x16x32_f16 v[88:91], v[140:143], v[192:195], v[88:91]
	v_mfma_f32_16x16x32_f16 v[80:83], v[132:135], v[200:203], v[80:83]
	v_mfma_f32_16x16x32_f16 v[72:75], v[140:143], v[200:203], v[72:75]
	s_barrier
	s_add_i32 s34, 0, 0x1c000
	s_add_i32 s35, s74, s42
	v_add_u32_e32 v175, s34, v166
	v_lshl_add_u64 v[162:163], v[162:163], 0, s[26:27]
	s_mov_b32 m0, s35
	ds_read_b128 v[204:207], v175
	ds_read_b128 v[208:211], v175 offset:1024
	ds_read_b128 v[212:215], v175 offset:2048
	ds_read_b128 v[216:219], v175 offset:3072
	global_load_lds_dwordx4 v[162:163], off
	v_lshl_add_u64 v[162:163], v[220:221], 0, s[26:27]
	s_add_i32 m0, s35, 0x2000
	s_nop 0
	global_load_lds_dwordx4 v[162:163], off
	s_barrier
	s_waitcnt lgkmcnt(0)
	v_mfma_f32_16x16x32_f16 v[116:119], v[204:207], v[158:161], v[116:119]
	v_mfma_f32_16x16x32_f16 v[112:115], v[212:215], v[158:161], v[112:115]
	v_mfma_f32_16x16x32_f16 v[100:103], v[204:207], v[180:183], v[100:103]
	v_mfma_f32_16x16x32_f16 v[92:95], v[212:215], v[180:183], v[92:95]
	v_mfma_f32_16x16x32_f16 v[84:87], v[204:207], v[188:191], v[84:87]
	v_mfma_f32_16x16x32_f16 v[76:79], v[212:215], v[188:191], v[76:79]
	v_mfma_f32_16x16x32_f16 v[68:71], v[204:207], v[196:199], v[68:71]
	v_mfma_f32_16x16x32_f16 v[64:67], v[212:215], v[196:199], v[64:67]
	v_mfma_f32_16x16x32_f16 v[116:119], v[208:211], v[176:179], v[116:119]
	v_mfma_f32_16x16x32_f16 v[112:115], v[216:219], v[176:179], v[112:115]
	v_mfma_f32_16x16x32_f16 v[100:103], v[208:211], v[184:187], v[100:103]
	v_mfma_f32_16x16x32_f16 v[92:95], v[216:219], v[184:187], v[92:95]
	v_mfma_f32_16x16x32_f16 v[84:87], v[208:211], v[192:195], v[84:87]
	v_mfma_f32_16x16x32_f16 v[76:79], v[216:219], v[192:195], v[76:79]
	v_mfma_f32_16x16x32_f16 v[68:71], v[208:211], v[200:203], v[68:71]
	v_mfma_f32_16x16x32_f16 v[64:67], v[216:219], v[200:203], v[64:67]
	s_barrier
	s_mov_b32 m0, s49
	v_lshl_add_u64 v[162:163], v[222:223], 0, s[26:27]
	ds_read_b128 v[158:161], v171 offset:49152
	ds_read_b128 v[176:179], v171 offset:50176
	ds_read_b128 v[180:183], v171 offset:51200
	ds_read_b128 v[184:187], v171 offset:52224
	ds_read_b128 v[188:191], v171 offset:53248
	ds_read_b128 v[192:195], v171 offset:54272
	ds_read_b128 v[196:199], v171 offset:55296
	ds_read_b128 v[200:203], v171 offset:56320
	global_load_lds_dwordx4 v[162:163], off
	v_lshl_add_u64 v[162:163], v[224:225], 0, s[26:27]
	s_mov_b32 m0, s50
	s_nop 0
	global_load_lds_dwordx4 v[162:163], off
	s_barrier
	s_waitcnt lgkmcnt(0)
	v_mfma_f32_16x16x32_f16 v[60:63], v[128:131], v[158:161], v[60:63]
	v_mfma_f32_16x16x32_f16 v[56:59], v[136:139], v[158:161], v[56:59]
	v_mfma_f32_16x16x32_f16 v[48:51], v[128:131], v[180:183], v[48:51]
	v_mfma_f32_16x16x32_f16 v[40:43], v[136:139], v[180:183], v[40:43]
	v_mfma_f32_16x16x32_f16 v[32:35], v[128:131], v[188:191], v[32:35]
	v_mfma_f32_16x16x32_f16 v[24:27], v[136:139], v[188:191], v[24:27]
	v_mfma_f32_16x16x32_f16 v[16:19], v[128:131], v[196:199], v[16:19]
	v_mfma_f32_16x16x32_f16 v[8:11], v[136:139], v[196:199], v[8:11]
	v_mfma_f32_16x16x32_f16 v[60:63], v[132:135], v[176:179], v[60:63]
	v_mfma_f32_16x16x32_f16 v[56:59], v[140:143], v[176:179], v[56:59]
	v_mfma_f32_16x16x32_f16 v[48:51], v[132:135], v[184:187], v[48:51]
	v_mfma_f32_16x16x32_f16 v[40:43], v[140:143], v[184:187], v[40:43]
	v_mfma_f32_16x16x32_f16 v[32:35], v[132:135], v[192:195], v[32:35]
	v_mfma_f32_16x16x32_f16 v[24:27], v[140:143], v[192:195], v[24:27]
	v_mfma_f32_16x16x32_f16 v[16:19], v[132:135], v[200:203], v[16:19]
	v_mfma_f32_16x16x32_f16 v[8:11], v[140:143], v[200:203], v[8:11]
	s_barrier
	s_add_u32 s30, s30, 0xc080
	s_addc_u32 s31, s31, 0
	s_add_i32 s34, s34, s42
	v_lshl_add_u64 v[128:129], s[30:31], 0, v[146:147]
	s_mov_b32 m0, s34
	s_nop 0
	global_load_lds_dwordx4 v[128:129], off
	v_lshl_add_u64 v[128:129], s[30:31], 0, v[150:151]
	s_add_i32 m0, s34, 0x2000
	s_nop 0
	global_load_lds_dwordx4 v[128:129], off
	s_waitcnt vmcnt(6)
	s_barrier
	v_mfma_f32_16x16x32_f16 v[52:55], v[204:207], v[158:161], v[52:55]
	v_mfma_f32_16x16x32_f16 v[44:47], v[212:215], v[158:161], v[44:47]
	v_mfma_f32_16x16x32_f16 v[36:39], v[204:207], v[180:183], v[36:39]
	v_mfma_f32_16x16x32_f16 v[28:31], v[212:215], v[180:183], v[28:31]
	v_mfma_f32_16x16x32_f16 v[20:23], v[204:207], v[188:191], v[20:23]
	v_mfma_f32_16x16x32_f16 v[12:15], v[212:215], v[188:191], v[12:15]
	v_mfma_f32_16x16x32_f16 v[4:7], v[204:207], v[196:199], v[4:7]
	v_mfma_f32_16x16x32_f16 v[0:3], v[212:215], v[196:199], v[0:3]
	v_mfma_f32_16x16x32_f16 v[52:55], v[208:211], v[176:179], v[52:55]
	v_mfma_f32_16x16x32_f16 v[44:47], v[216:219], v[176:179], v[44:47]
	v_mfma_f32_16x16x32_f16 v[36:39], v[208:211], v[184:187], v[36:39]
	v_mfma_f32_16x16x32_f16 v[28:31], v[216:219], v[184:187], v[28:31]
	v_mfma_f32_16x16x32_f16 v[20:23], v[208:211], v[192:195], v[20:23]
	v_mfma_f32_16x16x32_f16 v[12:15], v[216:219], v[192:195], v[12:15]
	v_mfma_f32_16x16x32_f16 v[4:7], v[208:211], v[200:203], v[4:7]
	v_mfma_f32_16x16x32_f16 v[0:3], v[216:219], v[200:203], v[0:3]
	s_barrier
	s_add_i32 s73, s73, 2
	s_add_u32 s28, s28, 0x100
	s_addc_u32 s29, s29, 0
	s_add_u32 s71, s71, 0x100
	s_addc_u32 s72, s72, 0
	s_cmp_gt_u32 s73, 9
	s_cbranch_scc0 .LBB7_27
	s_lshl_b32 s28, s70, 8
	s_add_i32 s28, s28, s48
	s_lshl_b32 s29, s67, 8
	s_or_b32 s29, s29, s51
	s_waitcnt vmcnt(6)
	v_pk_fma_f32 v[126:127], v[126:127], v[226:227], v[236:237] op_sel_hi:[1,0,1]
	v_pk_fma_f32 v[124:125], v[124:125], v[226:227], v[234:235] op_sel_hi:[1,0,1]
	v_pk_fma_f32 v[186:187], v[122:123], v[226:227], v[240:241] op_sel_hi:[1,0,1]
	v_pk_fma_f32 v[122:123], v[120:121], v[226:227], v[238:239] op_sel_hi:[1,0,1]
	v_cvt_pk_f16_f32 v120, v124, v125
	v_cvt_pk_f16_f32 v121, v126, v127
	v_cvt_pk_f16_f32 v122, v122, v123
	v_cvt_pk_f16_f32 v123, v186, v187
	ds_write_b128 v173, v[120:123]
	v_pk_fma_f32 v[118:119], v[118:119], v[226:227], v[244:245] op_sel_hi:[1,0,1]
	v_pk_fma_f32 v[116:117], v[116:117], v[226:227], v[242:243] op_sel_hi:[1,0,1]
	v_pk_fma_f32 v[120:121], v[114:115], v[226:227], v[248:249] op_sel_hi:[1,0,1]
	v_pk_fma_f32 v[114:115], v[112:113], v[226:227], v[246:247] op_sel_hi:[1,0,1]
	v_cvt_pk_f16_f32 v112, v116, v117
	v_cvt_pk_f16_f32 v113, v118, v119
	v_cvt_pk_f16_f32 v114, v114, v115
	v_cvt_pk_f16_f32 v115, v120, v121
	ds_write_b128 v173, v[112:115] offset:64
	v_or_b32_e32 v116, s28, v167
	ds_read_b128 v[112:115], v174
	v_mul_lo_u32 v116, v116, s10
	v_add_u32_e32 v120, s29, v116
	v_lshlrev_b32_e32 v121, 1, v120
	v_add_u32_e32 v122, v121, v168
	ds_read_b128 v[116:119], v174 offset:1152
	s_waitcnt lgkmcnt(0)
	buffer_store_dwordx4 v[112:115], v122, s[20:23], 0 offen nt
	v_pk_fma_f32 v[110:111], v[110:111], v[226:227], v[236:237] op_sel:[0,1,0]
	v_pk_fma_f32 v[108:109], v[108:109], v[226:227], v[234:235] op_sel:[0,1,0]
	v_pk_fma_f32 v[112:113], v[106:107], v[226:227], v[240:241] op_sel:[0,1,0]
	v_pk_fma_f32 v[106:107], v[104:105], v[226:227], v[238:239] op_sel:[0,1,0]
	v_cvt_pk_f16_f32 v104, v108, v109
	v_cvt_pk_f16_f32 v105, v110, v111
	v_cvt_pk_f16_f32 v106, v106, v107
	v_cvt_pk_f16_f32 v107, v112, v113
	ds_write_b128 v173, v[104:107]
	v_pk_fma_f32 v[102:103], v[102:103], v[226:227], v[244:245] op_sel:[0,1,0]
	v_pk_fma_f32 v[100:101], v[100:101], v[226:227], v[242:243] op_sel:[0,1,0]
	v_pk_fma_f32 v[104:105], v[94:95], v[226:227], v[248:249] op_sel:[0,1,0]
	v_pk_fma_f32 v[94:95], v[92:93], v[226:227], v[246:247] op_sel:[0,1,0]
	v_cvt_pk_f16_f32 v92, v100, v101
	v_cvt_pk_f16_f32 v93, v102, v103
	v_cvt_pk_f16_f32 v94, v94, v95
	v_cvt_pk_f16_f32 v95, v104, v105
	ds_write_b128 v173, v[92:95] offset:64
	ds_read_b128 v[92:95], v174
	ds_read_b128 v[100:103], v174 offset:1152
	v_add_u32_e32 v104, s55, v121
	v_add_u32_e32 v114, v121, v169
	v_add_u32_e32 v105, v104, v168
	buffer_store_dwordx4 v[116:119], v114, s[20:23], 0 offen nt
	s_waitcnt lgkmcnt(1)
	buffer_store_dwordx4 v[92:95], v105, s[20:23], 0 offen nt
	v_pk_fma_f32 v[86:87], v[86:87], v[228:229], v[244:245] op_sel_hi:[1,0,1]
	v_pk_fma_f32 v[84:85], v[84:85], v[228:229], v[242:243] op_sel_hi:[1,0,1]
	v_pk_fma_f32 v[92:93], v[98:99], v[228:229], v[236:237] op_sel_hi:[1,0,1]
	v_pk_fma_f32 v[94:95], v[96:97], v[228:229], v[234:235] op_sel_hi:[1,0,1]
	v_pk_fma_f32 v[96:97], v[90:91], v[228:229], v[240:241] op_sel_hi:[1,0,1]
	v_pk_fma_f32 v[90:91], v[88:89], v[228:229], v[238:239] op_sel_hi:[1,0,1]
	v_cvt_pk_f16_f32 v88, v94, v95
	v_cvt_pk_f16_f32 v89, v92, v93
	v_cvt_pk_f16_f32 v90, v90, v91
	v_cvt_pk_f16_f32 v91, v96, v97
	ds_write_b128 v173, v[88:91]
	v_pk_fma_f32 v[88:89], v[78:79], v[228:229], v[248:249] op_sel_hi:[1,0,1]
	v_pk_fma_f32 v[78:79], v[76:77], v[228:229], v[246:247] op_sel_hi:[1,0,1]
	v_cvt_pk_f16_f32 v76, v84, v85
	v_cvt_pk_f16_f32 v77, v86, v87
	v_cvt_pk_f16_f32 v78, v78, v79
	v_cvt_pk_f16_f32 v79, v88, v89
	ds_write_b128 v173, v[76:79] offset:64
	ds_read_b128 v[76:79], v174
	ds_read_b128 v[84:87], v174 offset:1152
	v_add_u32_e32 v88, s55, v104
	v_add_u32_e32 v105, v104, v169
	v_add_u32_e32 v89, v88, v168
	s_waitcnt lgkmcnt(4)
	buffer_store_dwordx4 v[100:103], v105, s[20:23], 0 offen nt
	s_waitcnt lgkmcnt(1)
	buffer_store_dwordx4 v[76:79], v89, s[20:23], 0 offen nt
	v_pk_fma_f32 v[70:71], v[70:71], v[228:229], v[244:245] op_sel:[0,1,0]
	v_pk_fma_f32 v[68:69], v[68:69], v[228:229], v[242:243] op_sel:[0,1,0]
	v_add_u32_e32 v76, v88, v169
	s_waitcnt lgkmcnt(0)
	buffer_store_dwordx4 v[84:87], v76, s[20:23], 0 offen nt
	v_pk_fma_f32 v[76:77], v[82:83], v[228:229], v[236:237] op_sel:[0,1,0]
	v_pk_fma_f32 v[78:79], v[80:81], v[228:229], v[234:235] op_sel:[0,1,0]
	v_pk_fma_f32 v[80:81], v[74:75], v[228:229], v[240:241] op_sel:[0,1,0]
	v_pk_fma_f32 v[74:75], v[72:73], v[228:229], v[238:239] op_sel:[0,1,0]
	v_cvt_pk_f16_f32 v72, v78, v79
	v_cvt_pk_f16_f32 v73, v76, v77
	v_cvt_pk_f16_f32 v74, v74, v75
	v_cvt_pk_f16_f32 v75, v80, v81
	ds_write_b128 v173, v[72:75]
	v_pk_fma_f32 v[72:73], v[66:67], v[228:229], v[248:249] op_sel:[0,1,0]
	v_pk_fma_f32 v[66:67], v[64:65], v[228:229], v[246:247] op_sel:[0,1,0]
	v_cvt_pk_f16_f32 v64, v68, v69
	v_cvt_pk_f16_f32 v65, v70, v71
	v_cvt_pk_f16_f32 v66, v66, v67
	v_cvt_pk_f16_f32 v67, v72, v73
	ds_write_b128 v173, v[64:67] offset:64
	ds_read_b128 v[64:67], v174
	ds_read_b128 v[68:71], v174 offset:1152
	v_add_u32_e32 v72, s56, v120
	v_lshlrev_b32_e32 v73, 1, v72
	v_add_u32_e32 v74, v73, v168
	s_waitcnt lgkmcnt(1)
	buffer_store_dwordx4 v[64:67], v74, s[20:23], 0 offen nt
	v_pk_fma_f32 v[62:63], v[62:63], v[230:231], v[236:237] op_sel_hi:[1,0,1]
	v_pk_fma_f32 v[60:61], v[60:61], v[230:231], v[234:235] op_sel_hi:[1,0,1]
	v_pk_fma_f32 v[64:65], v[58:59], v[230:231], v[240:241] op_sel_hi:[1,0,1]
	v_pk_fma_f32 v[58:59], v[56:57], v[230:231], v[238:239] op_sel_hi:[1,0,1]
	v_cvt_pk_f16_f32 v56, v60, v61
	v_cvt_pk_f16_f32 v57, v62, v63
	v_cvt_pk_f16_f32 v58, v58, v59
	v_cvt_pk_f16_f32 v59, v64, v65
	ds_write_b128 v173, v[56:59]
	v_pk_fma_f32 v[54:55], v[54:55], v[230:231], v[244:245] op_sel_hi:[1,0,1]
	v_pk_fma_f32 v[52:53], v[52:53], v[230:231], v[242:243] op_sel_hi:[1,0,1]
	v_pk_fma_f32 v[56:57], v[46:47], v[230:231], v[248:249] op_sel_hi:[1,0,1]
	v_pk_fma_f32 v[46:47], v[44:45], v[230:231], v[246:247] op_sel_hi:[1,0,1]
	v_cvt_pk_f16_f32 v44, v52, v53
	v_cvt_pk_f16_f32 v45, v54, v55
	v_cvt_pk_f16_f32 v46, v46, v47
	v_cvt_pk_f16_f32 v47, v56, v57
	ds_write_b128 v173, v[44:47] offset:64
	ds_read_b128 v[44:47], v174
	ds_read_b128 v[52:55], v174 offset:1152
	v_add_u32_e32 v56, s62, v88
	v_add_u32_e32 v66, v73, v169
	v_add_u32_e32 v57, v56, v168
	s_waitcnt lgkmcnt(4)
	buffer_store_dwordx4 v[68:71], v66, s[20:23], 0 offen nt
	s_waitcnt lgkmcnt(1)
	buffer_store_dwordx4 v[44:47], v57, s[20:23], 0 offen nt
	v_pk_fma_f32 v[38:39], v[38:39], v[230:231], v[244:245] op_sel:[0,1,0]
	v_pk_fma_f32 v[36:37], v[36:37], v[230:231], v[242:243] op_sel:[0,1,0]
	v_add_u32_e32 v44, v56, v169
	s_waitcnt lgkmcnt(0)
	buffer_store_dwordx4 v[52:55], v44, s[20:23], 0 offen nt
	v_pk_fma_f32 v[44:45], v[50:51], v[230:231], v[236:237] op_sel:[0,1,0]
	v_pk_fma_f32 v[46:47], v[48:49], v[230:231], v[234:235] op_sel:[0,1,0]
	v_pk_fma_f32 v[48:49], v[42:43], v[230:231], v[240:241] op_sel:[0,1,0]
	v_pk_fma_f32 v[42:43], v[40:41], v[230:231], v[238:239] op_sel:[0,1,0]
	v_cvt_pk_f16_f32 v40, v46, v47
	v_cvt_pk_f16_f32 v41, v44, v45
	v_cvt_pk_f16_f32 v42, v42, v43
	v_cvt_pk_f16_f32 v43, v48, v49
	ds_write_b128 v173, v[40:43]
	v_pk_fma_f32 v[40:41], v[30:31], v[230:231], v[248:249] op_sel:[0,1,0]
	v_pk_fma_f32 v[30:31], v[28:29], v[230:231], v[246:247] op_sel:[0,1,0]
	v_cvt_pk_f16_f32 v28, v36, v37
	v_cvt_pk_f16_f32 v29, v38, v39
	v_cvt_pk_f16_f32 v30, v30, v31
	v_cvt_pk_f16_f32 v31, v40, v41
	ds_write_b128 v173, v[28:31] offset:64
	ds_read_b128 v[28:31], v174
	ds_read_b128 v[36:39], v174 offset:1152
	v_add_u32_e32 v40, s63, v72
	v_lshlrev_b32_e32 v41, 1, v40
	v_add_u32_e32 v42, v41, v168
	s_waitcnt lgkmcnt(1)
	buffer_store_dwordx4 v[28:31], v42, s[20:23], 0 offen nt
	v_pk_fma_f32 v[22:23], v[22:23], v[232:233], v[244:245] op_sel_hi:[1,0,1]
	v_pk_fma_f32 v[20:21], v[20:21], v[232:233], v[242:243] op_sel_hi:[1,0,1]
	v_add_u32_e32 v28, v41, v169
	s_waitcnt lgkmcnt(0)
	buffer_store_dwordx4 v[36:39], v28, s[20:23], 0 offen nt
	v_pk_fma_f32 v[28:29], v[34:35], v[232:233], v[236:237] op_sel_hi:[1,0,1]
	v_pk_fma_f32 v[30:31], v[32:33], v[232:233], v[234:235] op_sel_hi:[1,0,1]
	v_pk_fma_f32 v[32:33], v[26:27], v[232:233], v[240:241] op_sel_hi:[1,0,1]
	v_pk_fma_f32 v[26:27], v[24:25], v[232:233], v[238:239] op_sel_hi:[1,0,1]
	v_cvt_pk_f16_f32 v24, v30, v31
	v_cvt_pk_f16_f32 v25, v28, v29
	v_cvt_pk_f16_f32 v26, v26, v27
	v_cvt_pk_f16_f32 v27, v32, v33
	ds_write_b128 v173, v[24:27]
	v_pk_fma_f32 v[24:25], v[14:15], v[232:233], v[248:249] op_sel_hi:[1,0,1]
	v_pk_fma_f32 v[14:15], v[12:13], v[232:233], v[246:247] op_sel_hi:[1,0,1]
	v_cvt_pk_f16_f32 v12, v20, v21
	v_cvt_pk_f16_f32 v13, v22, v23
	v_cvt_pk_f16_f32 v14, v14, v15
	v_cvt_pk_f16_f32 v15, v24, v25
	ds_write_b128 v173, v[12:15] offset:64
	ds_read_b128 v[12:15], v174
	ds_read_b128 v[20:23], v174 offset:1152
	v_add_u32_e32 v24, s64, v40
	v_lshlrev_b32_e32 v25, 1, v24
	v_add_u32_e32 v26, v25, v168
	s_waitcnt lgkmcnt(1)
	buffer_store_dwordx4 v[12:15], v26, s[20:23], 0 offen nt
	v_pk_fma_f32 v[6:7], v[6:7], v[232:233], v[244:245] op_sel:[0,1,0]
	v_pk_fma_f32 v[4:5], v[4:5], v[232:233], v[242:243] op_sel:[0,1,0]
	v_pk_fma_f32 v[12:13], v[18:19], v[232:233], v[236:237] op_sel:[0,1,0]
	v_pk_fma_f32 v[14:15], v[16:17], v[232:233], v[234:235] op_sel:[0,1,0]
	v_pk_fma_f32 v[16:17], v[10:11], v[232:233], v[240:241] op_sel:[0,1,0]
	v_pk_fma_f32 v[10:11], v[8:9], v[232:233], v[238:239] op_sel:[0,1,0]
	v_cvt_pk_f16_f32 v8, v14, v15
	v_cvt_pk_f16_f32 v9, v12, v13
	v_cvt_pk_f16_f32 v10, v10, v11
	v_cvt_pk_f16_f32 v11, v16, v17
	ds_write_b128 v173, v[8:11]
	v_pk_fma_f32 v[8:9], v[2:3], v[232:233], v[248:249] op_sel:[0,1,0]
	v_pk_fma_f32 v[2:3], v[0:1], v[232:233], v[246:247] op_sel:[0,1,0]
	v_cvt_pk_f16_f32 v0, v4, v5
	v_cvt_pk_f16_f32 v1, v6, v7
	v_cvt_pk_f16_f32 v2, v2, v3
	v_cvt_pk_f16_f32 v3, v8, v9
	ds_write_b128 v173, v[0:3] offset:64
	ds_read_b128 v[0:3], v174
	ds_read_b128 v[4:7], v174 offset:1152
	v_add_lshl_u32 v8, v24, s64, 1
	v_add_u32_e32 v25, v25, v169
	v_add_u32_e32 v9, v8, v168
	s_waitcnt lgkmcnt(4)
	buffer_store_dwordx4 v[20:23], v25, s[20:23], 0 offen nt
	s_waitcnt lgkmcnt(1)
	buffer_store_dwordx4 v[0:3], v9, s[20:23], 0 offen nt
	s_mov_b32 s67, s68
	s_mov_b32 s70, s69
	v_add_u32_e32 v0, v8, v169
	s_mov_b64 s[30:31], s[0:1]
	s_mov_b64 s[28:29], s[8:9]
	s_mov_b64 vcc, s[6:7]
	s_waitcnt lgkmcnt(0)
	buffer_store_dwordx4 v[4:7], v0, s[20:23], 0 offen nt
	s_cbranch_vccz .LBB7_12
	s_waitcnt vmcnt(0)
	s_cmpk_gt_u32 s36, 0xff
	s_cbranch_scc1 .LBB7_31
	s_barrier

.LBB7_32:
	s_endpgm
	s_endpgm
	s_endpgm
	s_endpgm
	s_endpgm
	s_endpgm
	s_endpgm
	s_endpgm
	s_endpgm
	s_endpgm
	s_endpgm
	.section	.rodata,"a",@progbits
	.p2align	6, 0x0

.LBB8_27:
	ds_read_b128 v[72:75], v231
	ds_read_b128 v[80:83], v231 offset:1024
	ds_read_b128 v[88:91], v231 offset:2048
	ds_read_b128 v[92:95], v231 offset:3072
	s_add_u32 s40, s38, 0xfffd0080
	s_addc_u32 s41, s39, -1
	s_cmp_eq_u32 s87, 8
	s_cselect_b32 s43, s9, s41
	s_cselect_b32 s42, s8, s40
	s_cselect_b32 s41, s1, s86
	s_cselect_b32 s40, s0, s85
	v_lshl_add_u64 v[190:191], s[38:39], 0, v[184:185]
	s_add_i32 m0, s51, 0xc000
	ds_read_b128 v[136:139], v232
	ds_read_b128 v[148:151], v232 offset:1024
	ds_read_b128 v[152:155], v232 offset:2048
	ds_read_b128 v[156:159], v232 offset:3072
	ds_read_b128 v[160:163], v232 offset:4096
	ds_read_b128 v[164:167], v232 offset:5120
	ds_read_b128 v[168:171], v232 offset:6144
	ds_read_b128 v[172:175], v232 offset:7168
	global_load_lds_dwordx4 v[190:191], off
	v_lshl_add_u64 v[190:191], s[38:39], 0, v[186:187]
	s_add_i32 m0, s51, 0xe000
	s_nop 0
	global_load_lds_dwordx4 v[190:191], off
	s_waitcnt lgkmcnt(8)
	s_barrier
	s_waitcnt lgkmcnt(0)
	v_mfma_f32_16x16x32_f16 v[144:147], v[72:75], v[136:139], v[144:147]
	v_mfma_f32_16x16x32_f16 v[140:143], v[88:91], v[136:139], v[140:143]
	v_mfma_f32_16x16x32_f16 v[124:127], v[72:75], v[152:155], v[124:127]
	v_mfma_f32_16x16x32_f16 v[120:123], v[88:91], v[152:155], v[120:123]
	v_mfma_f32_16x16x32_f16 v[108:111], v[72:75], v[160:163], v[108:111]
	v_mfma_f32_16x16x32_f16 v[104:107], v[88:91], v[160:163], v[104:107]
	v_mfma_f32_16x16x32_f16 v[84:87], v[72:75], v[168:171], v[84:87]
	v_mfma_f32_16x16x32_f16 v[76:79], v[88:91], v[168:171], v[76:79]
	v_mfma_f32_16x16x32_f16 v[144:147], v[80:83], v[148:151], v[144:147]
	v_mfma_f32_16x16x32_f16 v[140:143], v[92:95], v[148:151], v[140:143]
	v_mfma_f32_16x16x32_f16 v[124:127], v[80:83], v[156:159], v[124:127]
	v_mfma_f32_16x16x32_f16 v[120:123], v[92:95], v[156:159], v[120:123]
	v_mfma_f32_16x16x32_f16 v[108:111], v[80:83], v[164:167], v[108:111]
	v_mfma_f32_16x16x32_f16 v[104:107], v[92:95], v[164:167], v[104:107]
	v_mfma_f32_16x16x32_f16 v[84:87], v[80:83], v[172:175], v[84:87]
	v_mfma_f32_16x16x32_f16 v[76:79], v[92:95], v[172:175], v[76:79]
	s_barrier
	s_add_i32 s88, s70, s50
	v_lshl_add_u64 v[206:207], s[40:41], 0, v[178:179]
	s_mov_b32 m0, s88
	ds_read_b128 v[190:193], v233
	ds_read_b128 v[194:197], v233 offset:1024
	ds_read_b128 v[198:201], v233 offset:2048
	ds_read_b128 v[202:205], v233 offset:3072
	global_load_lds_dwordx4 v[206:207], off
	v_lshl_add_u64 v[208:209], s[40:41], 0, v[182:183]
	s_add_i32 m0, s88, 0x2000
	s_nop 0
	global_load_lds_dwordx4 v[208:209], off
	s_barrier
	s_waitcnt lgkmcnt(0)
	v_mfma_f32_16x16x32_f16 v[132:135], v[190:193], v[136:139], v[132:135]
	v_mfma_f32_16x16x32_f16 v[128:131], v[198:201], v[136:139], v[128:131]
	v_mfma_f32_16x16x32_f16 v[116:119], v[190:193], v[152:155], v[116:119]
	v_mfma_f32_16x16x32_f16 v[112:115], v[198:201], v[152:155], v[112:115]
	v_mfma_f32_16x16x32_f16 v[100:103], v[190:193], v[160:163], v[100:103]
	v_mfma_f32_16x16x32_f16 v[96:99], v[198:201], v[160:163], v[96:99]
	v_mfma_f32_16x16x32_f16 v[68:71], v[190:193], v[168:171], v[68:71]
	v_mfma_f32_16x16x32_f16 v[64:67], v[198:201], v[168:171], v[64:67]
	v_mfma_f32_16x16x32_f16 v[132:135], v[194:197], v[148:151], v[132:135]
	v_mfma_f32_16x16x32_f16 v[128:131], v[202:205], v[148:151], v[128:131]
	v_mfma_f32_16x16x32_f16 v[116:119], v[194:197], v[156:159], v[116:119]
	v_mfma_f32_16x16x32_f16 v[112:115], v[202:205], v[156:159], v[112:115]
	v_mfma_f32_16x16x32_f16 v[100:103], v[194:197], v[164:167], v[100:103]
	v_mfma_f32_16x16x32_f16 v[96:99], v[202:205], v[164:167], v[96:99]
	v_mfma_f32_16x16x32_f16 v[68:71], v[194:197], v[172:175], v[68:71]
	v_mfma_f32_16x16x32_f16 v[64:67], v[202:205], v[172:175], v[64:67]
	s_barrier
	s_mov_b32 m0, s51
	v_lshl_add_u64 v[210:211], s[42:43], 0, v[176:177]
	ds_read_b128 v[136:139], v232 offset:16384
	ds_read_b128 v[148:151], v232 offset:17408
	ds_read_b128 v[152:155], v232 offset:18432
	ds_read_b128 v[156:159], v232 offset:19456
	ds_read_b128 v[160:163], v232 offset:20480
	ds_read_b128 v[164:167], v232 offset:21504
	ds_read_b128 v[168:171], v232 offset:22528
	ds_read_b128 v[172:175], v232 offset:23552
	global_load_lds_dwordx4 v[210:211], off
	v_lshl_add_u64 v[212:213], s[42:43], 0, v[180:181]
	s_mov_b32 m0, s52
	s_nop 0
	global_load_lds_dwordx4 v[212:213], off
	s_barrier
	s_waitcnt lgkmcnt(0)
	v_mfma_f32_16x16x32_f16 v[60:63], v[72:75], v[136:139], v[60:63]
	v_mfma_f32_16x16x32_f16 v[56:59], v[88:91], v[136:139], v[56:59]
	v_mfma_f32_16x16x32_f16 v[44:47], v[72:75], v[152:155], v[44:47]
	v_mfma_f32_16x16x32_f16 v[40:43], v[88:91], v[152:155], v[40:43]
	v_mfma_f32_16x16x32_f16 v[28:31], v[72:75], v[160:163], v[28:31]
	v_mfma_f32_16x16x32_f16 v[24:27], v[88:91], v[160:163], v[24:27]
	v_mfma_f32_16x16x32_f16 v[12:15], v[72:75], v[168:171], v[12:15]
	v_mfma_f32_16x16x32_f16 v[8:11], v[88:91], v[168:171], v[8:11]
	v_mfma_f32_16x16x32_f16 v[60:63], v[80:83], v[148:151], v[60:63]
	v_mfma_f32_16x16x32_f16 v[56:59], v[92:95], v[148:151], v[56:59]
	v_mfma_f32_16x16x32_f16 v[44:47], v[80:83], v[156:159], v[44:47]
	v_mfma_f32_16x16x32_f16 v[40:43], v[92:95], v[156:159], v[40:43]
	v_mfma_f32_16x16x32_f16 v[28:31], v[80:83], v[164:167], v[28:31]
	v_mfma_f32_16x16x32_f16 v[24:27], v[92:95], v[164:167], v[24:27]
	v_mfma_f32_16x16x32_f16 v[12:15], v[80:83], v[172:175], v[12:15]
	v_mfma_f32_16x16x32_f16 v[8:11], v[92:95], v[172:175], v[8:11]
	s_barrier
	s_add_u32 s88, s40, 0xc000
	s_addc_u32 s89, s41, 0
	s_add_i32 s90, s71, s50
	v_lshl_add_u64 v[72:73], s[88:89], 0, v[178:179]
	s_mov_b32 m0, s90
	s_nop 0
	global_load_lds_dwordx4 v[72:73], off
	v_lshl_add_u64 v[72:73], s[88:89], 0, v[182:183]
	s_add_i32 m0, s90, 0x2000
	s_nop 0
	global_load_lds_dwordx4 v[72:73], off
	s_waitcnt vmcnt(6)
	s_barrier
	v_mfma_f32_16x16x32_f16 v[52:55], v[190:193], v[136:139], v[52:55]
	v_mfma_f32_16x16x32_f16 v[48:51], v[198:201], v[136:139], v[48:51]
	v_mfma_f32_16x16x32_f16 v[36:39], v[190:193], v[152:155], v[36:39]
	v_mfma_f32_16x16x32_f16 v[32:35], v[198:201], v[152:155], v[32:35]
	v_mfma_f32_16x16x32_f16 v[20:23], v[190:193], v[160:163], v[20:23]
	v_mfma_f32_16x16x32_f16 v[16:19], v[198:201], v[160:163], v[16:19]
	v_mfma_f32_16x16x32_f16 v[4:7], v[190:193], v[168:171], v[4:7]
	v_mfma_f32_16x16x32_f16 v[0:3], v[198:201], v[168:171], v[0:3]
	v_mfma_f32_16x16x32_f16 v[52:55], v[194:197], v[148:151], v[52:55]
	v_mfma_f32_16x16x32_f16 v[48:51], v[202:205], v[148:151], v[48:51]
	v_mfma_f32_16x16x32_f16 v[36:39], v[194:197], v[156:159], v[36:39]
	v_mfma_f32_16x16x32_f16 v[32:35], v[202:205], v[156:159], v[32:35]
	v_mfma_f32_16x16x32_f16 v[20:23], v[194:197], v[164:167], v[20:23]
	v_mfma_f32_16x16x32_f16 v[16:19], v[202:205], v[164:167], v[16:19]
	v_mfma_f32_16x16x32_f16 v[4:7], v[194:197], v[172:175], v[4:7]
	v_mfma_f32_16x16x32_f16 v[0:3], v[202:205], v[172:175], v[0:3]
	s_barrier
	s_add_i32 s88, 0, 0x18000
	v_add_u32_e32 v92, s88, v228
	ds_read_b128 v[72:75], v92
	ds_read_b128 v[80:83], v92 offset:1024
	ds_read_b128 v[88:91], v92 offset:2048
	ds_read_b128 v[92:95], v92 offset:3072
	s_add_u32 s42, s42, 0x30000
	s_addc_u32 s43, s43, 0
	s_mov_b32 m0, s53
	v_lshl_add_u64 v[190:191], s[42:43], 0, v[176:177]
	ds_read_b128 v[136:139], v232 offset:32768
	ds_read_b128 v[148:151], v232 offset:33792
	ds_read_b128 v[152:155], v232 offset:34816
	ds_read_b128 v[156:159], v232 offset:35840
	ds_read_b128 v[160:163], v232 offset:36864
	ds_read_b128 v[164:167], v232 offset:37888
	ds_read_b128 v[168:171], v232 offset:38912
	ds_read_b128 v[172:175], v232 offset:39936
	global_load_lds_dwordx4 v[190:191], off
	v_lshl_add_u64 v[190:191], s[42:43], 0, v[180:181]
	s_mov_b32 m0, s54
	s_nop 0
	global_load_lds_dwordx4 v[190:191], off
	s_waitcnt lgkmcnt(8)
	s_barrier
	s_waitcnt lgkmcnt(0)
	v_mfma_f32_16x16x32_f16 v[144:147], v[72:75], v[136:139], v[144:147]
	v_mfma_f32_16x16x32_f16 v[140:143], v[88:91], v[136:139], v[140:143]
	v_mfma_f32_16x16x32_f16 v[124:127], v[72:75], v[152:155], v[124:127]
	v_mfma_f32_16x16x32_f16 v[120:123], v[88:91], v[152:155], v[120:123]
	v_mfma_f32_16x16x32_f16 v[108:111], v[72:75], v[160:163], v[108:111]
	v_mfma_f32_16x16x32_f16 v[104:107], v[88:91], v[160:163], v[104:107]
	v_mfma_f32_16x16x32_f16 v[84:87], v[72:75], v[168:171], v[84:87]
	v_mfma_f32_16x16x32_f16 v[76:79], v[88:91], v[168:171], v[76:79]
	v_mfma_f32_16x16x32_f16 v[144:147], v[80:83], v[148:151], v[144:147]
	v_mfma_f32_16x16x32_f16 v[140:143], v[92:95], v[148:151], v[140:143]
	v_mfma_f32_16x16x32_f16 v[124:127], v[80:83], v[156:159], v[124:127]
	v_mfma_f32_16x16x32_f16 v[120:123], v[92:95], v[156:159], v[120:123]
	v_mfma_f32_16x16x32_f16 v[108:111], v[80:83], v[164:167], v[108:111]
	v_mfma_f32_16x16x32_f16 v[104:107], v[92:95], v[164:167], v[104:107]
	v_mfma_f32_16x16x32_f16 v[84:87], v[80:83], v[172:175], v[84:87]
	v_mfma_f32_16x16x32_f16 v[76:79], v[92:95], v[172:175], v[76:79]
	s_barrier
	s_add_i32 s42, 0, 0x1c000
	s_add_i32 s43, s88, s50
	v_add_u32_e32 v202, s42, v228
	v_lshl_add_u64 v[206:207], v[206:207], 0, s[36:37]
	s_mov_b32 m0, s43
	ds_read_b128 v[190:193], v202
	ds_read_b128 v[194:197], v202 offset:1024
	ds_read_b128 v[198:201], v202 offset:2048
	ds_read_b128 v[202:205], v202 offset:3072
	global_load_lds_dwordx4 v[206:207], off
	v_lshl_add_u64 v[206:207], v[208:209], 0, s[36:37]
	s_add_i32 m0, s43, 0x2000
	s_nop 0
	global_load_lds_dwordx4 v[206:207], off
	s_barrier
	s_waitcnt lgkmcnt(0)
	v_mfma_f32_16x16x32_f16 v[132:135], v[190:193], v[136:139], v[132:135]
	v_mfma_f32_16x16x32_f16 v[128:131], v[198:201], v[136:139], v[128:131]
	v_mfma_f32_16x16x32_f16 v[116:119], v[190:193], v[152:155], v[116:119]
	v_mfma_f32_16x16x32_f16 v[112:115], v[198:201], v[152:155], v[112:115]
	v_mfma_f32_16x16x32_f16 v[100:103], v[190:193], v[160:163], v[100:103]
	v_mfma_f32_16x16x32_f16 v[96:99], v[198:201], v[160:163], v[96:99]
	v_mfma_f32_16x16x32_f16 v[68:71], v[190:193], v[168:171], v[68:71]
	v_mfma_f32_16x16x32_f16 v[64:67], v[198:201], v[168:171], v[64:67]
	v_mfma_f32_16x16x32_f16 v[132:135], v[194:197], v[148:151], v[132:135]
	v_mfma_f32_16x16x32_f16 v[128:131], v[202:205], v[148:151], v[128:131]
	v_mfma_f32_16x16x32_f16 v[116:119], v[194:197], v[156:159], v[116:119]
	v_mfma_f32_16x16x32_f16 v[112:115], v[202:205], v[156:159], v[112:115]
	v_mfma_f32_16x16x32_f16 v[100:103], v[194:197], v[164:167], v[100:103]
	v_mfma_f32_16x16x32_f16 v[96:99], v[202:205], v[164:167], v[96:99]
	v_mfma_f32_16x16x32_f16 v[68:71], v[194:197], v[172:175], v[68:71]
	v_mfma_f32_16x16x32_f16 v[64:67], v[202:205], v[172:175], v[64:67]
	s_barrier
	s_mov_b32 m0, s59
	v_lshl_add_u64 v[206:207], v[210:211], 0, s[36:37]
	ds_read_b128 v[136:139], v232 offset:49152
	ds_read_b128 v[148:151], v232 offset:50176
	ds_read_b128 v[152:155], v232 offset:51200
	ds_read_b128 v[156:159], v232 offset:52224
	ds_read_b128 v[160:163], v232 offset:53248
	ds_read_b128 v[164:167], v232 offset:54272
	ds_read_b128 v[168:171], v232 offset:55296
	ds_read_b128 v[172:175], v232 offset:56320
	global_load_lds_dwordx4 v[206:207], off
	v_lshl_add_u64 v[206:207], v[212:213], 0, s[36:37]
	s_mov_b32 m0, s60
	s_nop 0
	global_load_lds_dwordx4 v[206:207], off
	s_barrier
	s_waitcnt lgkmcnt(0)
	v_mfma_f32_16x16x32_f16 v[60:63], v[72:75], v[136:139], v[60:63]
	v_mfma_f32_16x16x32_f16 v[56:59], v[88:91], v[136:139], v[56:59]
	v_mfma_f32_16x16x32_f16 v[44:47], v[72:75], v[152:155], v[44:47]
	v_mfma_f32_16x16x32_f16 v[40:43], v[88:91], v[152:155], v[40:43]
	v_mfma_f32_16x16x32_f16 v[28:31], v[72:75], v[160:163], v[28:31]
	v_mfma_f32_16x16x32_f16 v[24:27], v[88:91], v[160:163], v[24:27]
	v_mfma_f32_16x16x32_f16 v[12:15], v[72:75], v[168:171], v[12:15]
	v_mfma_f32_16x16x32_f16 v[8:11], v[88:91], v[168:171], v[8:11]
	v_mfma_f32_16x16x32_f16 v[60:63], v[80:83], v[148:151], v[60:63]
	v_mfma_f32_16x16x32_f16 v[56:59], v[92:95], v[148:151], v[56:59]
	v_mfma_f32_16x16x32_f16 v[44:47], v[80:83], v[156:159], v[44:47]
	v_mfma_f32_16x16x32_f16 v[40:43], v[92:95], v[156:159], v[40:43]
	v_mfma_f32_16x16x32_f16 v[28:31], v[80:83], v[164:167], v[28:31]
	v_mfma_f32_16x16x32_f16 v[24:27], v[92:95], v[164:167], v[24:27]
	v_mfma_f32_16x16x32_f16 v[12:15], v[80:83], v[172:175], v[12:15]
	v_mfma_f32_16x16x32_f16 v[8:11], v[92:95], v[172:175], v[8:11]
	s_barrier
	s_add_u32 s40, s40, 0xc080
	s_addc_u32 s41, s41, 0
	s_add_i32 s42, s42, s50
	v_lshl_add_u64 v[72:73], s[40:41], 0, v[178:179]
	s_mov_b32 m0, s42
	s_nop 0
	global_load_lds_dwordx4 v[72:73], off
	v_lshl_add_u64 v[72:73], s[40:41], 0, v[182:183]
	s_add_i32 m0, s42, 0x2000
	s_nop 0
	global_load_lds_dwordx4 v[72:73], off
	s_waitcnt vmcnt(6)
	s_barrier
	v_mfma_f32_16x16x32_f16 v[52:55], v[190:193], v[136:139], v[52:55]
	v_mfma_f32_16x16x32_f16 v[48:51], v[198:201], v[136:139], v[48:51]
	v_mfma_f32_16x16x32_f16 v[36:39], v[190:193], v[152:155], v[36:39]
	v_mfma_f32_16x16x32_f16 v[32:35], v[198:201], v[152:155], v[32:35]
	v_mfma_f32_16x16x32_f16 v[20:23], v[190:193], v[160:163], v[20:23]
	v_mfma_f32_16x16x32_f16 v[16:19], v[198:201], v[160:163], v[16:19]
	v_mfma_f32_16x16x32_f16 v[4:7], v[190:193], v[168:171], v[4:7]
	v_mfma_f32_16x16x32_f16 v[0:3], v[198:201], v[168:171], v[0:3]
	v_mfma_f32_16x16x32_f16 v[52:55], v[194:197], v[148:151], v[52:55]
	v_mfma_f32_16x16x32_f16 v[48:51], v[202:205], v[148:151], v[48:51]
	v_mfma_f32_16x16x32_f16 v[36:39], v[194:197], v[156:159], v[36:39]
	v_mfma_f32_16x16x32_f16 v[32:35], v[202:205], v[156:159], v[32:35]
	v_mfma_f32_16x16x32_f16 v[20:23], v[194:197], v[164:167], v[20:23]
	v_mfma_f32_16x16x32_f16 v[16:19], v[202:205], v[164:167], v[16:19]
	v_mfma_f32_16x16x32_f16 v[4:7], v[194:197], v[172:175], v[4:7]
	v_mfma_f32_16x16x32_f16 v[0:3], v[202:205], v[172:175], v[0:3]
	s_barrier
	s_add_i32 s87, s87, 2
	s_add_u32 s38, s38, 0x100
	s_addc_u32 s39, s39, 0
	s_add_u32 s85, s85, 0x100
	s_addc_u32 s86, s86, 0
	s_cmp_gt_u32 s87, 9
	s_cbranch_scc0 .LBB8_27
	s_lshl_b32 s92, s84, 8
	s_add_i32 s92, s92, s58
	s_lshl_b32 s93, s83, 8
	s_or_b32 s93, s93, s61
	v_lshlrev_b32_e32 v237, 2, v226
	s_lshl_b32 s96, s93, 2
	s_add_u32 s94, s16, s96
	s_addc_u32 s95, s17, 0
	global_load_dwordx4 v[72:75], v237, s[94:95] offset:0
	global_load_dwordx4 v[80:83], v237, s[94:95] offset:16
	global_load_dwordx4 v[88:91], v237, s[94:95] offset:128
	global_load_dwordx4 v[92:95], v237, s[94:95] offset:144
	s_add_u32 s94, s18, s96
	s_addc_u32 s95, s19, 0
	global_load_dwordx4 v[136:139], v237, s[94:95] offset:0
	global_load_dwordx4 v[148:151], v237, s[94:95] offset:16
	global_load_dwordx4 v[152:155], v237, s[94:95] offset:128
	global_load_dwordx4 v[156:159], v237, s[94:95] offset:144
	s_add_u32 s94, s14, s96
	s_addc_u32 s95, s15, 0
	global_load_dwordx4 v[160:163], v237, s[94:95] offset:0
	global_load_dwordx4 v[164:167], v237, s[94:95] offset:16
	global_load_dwordx4 v[168:171], v237, s[94:95] offset:128
	global_load_dwordx4 v[172:175], v237, s[94:95] offset:144
	v_lshlrev_b32_e32 v190, 3, v227
	s_lshl_b32 s96, s92, 3
	s_add_u32 s94, s12, s96
	s_addc_u32 s95, s13, 0
	global_load_dwordx2 v[238:239], v190, s[94:95] offset:0
	global_load_dwordx2 v[192:193], v190, s[94:95] offset:128
	global_load_dwordx2 v[194:195], v190, s[94:95] offset:256
	global_load_dwordx2 v[196:197], v190, s[94:95] offset:384
	global_load_dwordx2 v[198:199], v190, s[94:95] offset:1024
	global_load_dwordx2 v[200:201], v190, s[94:95] offset:1152
	global_load_dwordx2 v[202:203], v190, s[94:95] offset:1280
	global_load_dwordx2 v[204:205], v190, s[94:95] offset:1408
	v_mul_u32_u24_e32 v191, 0x600, v227
	v_lshl_add_u32 v191, v226, 1, v191
	s_mul_i32 s96, s92, 0x600
	s_lshl_b32 s97, s93, 1
	s_add_u32 s96, s96, s97
	s_add_u32 s98, s10, s96
	s_addc_u32 s99, s11, 0
	s_add_u32 s94, s98, 0x0
	s_addc_u32 s95, s99, 0
	global_load_dwordx4 v[208:211], v191, s[94:95] offset:0 nt
	global_load_dwordx4 v[212:215], v191, s[94:95] offset:64 nt
	s_add_u32 s94, s98, 0x6000
	s_addc_u32 s95, s99, 0
	global_load_dwordx4 v[216:219], v191, s[94:95] offset:0 nt
	global_load_dwordx4 v[220:223], v191, s[94:95] offset:64 nt
	v_add_u32_e32 v224, s92, v229
	v_mul_u32_u24_e32 v224, 0x600, v224
	s_lshl_b32 s97, s93, 1
	v_add3_u32 v224, v224, v230, s97
	s_lshl_b32 s96, s83, 2
	s_lshr_b32 s97, s61, 6
	s_add_u32 s96, s96, s97
	s_lshl_b32 s96, s96, 19
	s_lshl_b32 s97, s92, 3
	s_add_u32 s96, s96, s97
	s_add_u32 s100, s28, s96
	s_addc_u32 s101, s29, 0
	s_waitcnt vmcnt(19)
	v_pk_add_f32 v[72:73], v[72:73], v[136:137]
	v_pk_add_f32 v[74:75], v[74:75], v[138:139]
	s_waitcnt vmcnt(18)
	v_pk_add_f32 v[80:81], v[80:81], v[148:149]
	v_pk_add_f32 v[82:83], v[82:83], v[150:151]
	s_waitcnt vmcnt(17)
	v_pk_add_f32 v[88:89], v[88:89], v[152:153]
	v_pk_add_f32 v[90:91], v[90:91], v[154:155]
	s_waitcnt vmcnt(16)
	v_pk_add_f32 v[92:93], v[92:93], v[156:157]
	v_pk_add_f32 v[94:95], v[94:95], v[158:159]
	v_pk_add_f32 v[144:145], v[144:145], v[72:73]
	v_pk_add_f32 v[146:147], v[146:147], v[74:75]
	v_pk_add_f32 v[124:125], v[124:125], v[72:73]
	v_pk_add_f32 v[126:127], v[126:127], v[74:75]
	v_pk_add_f32 v[108:109], v[108:109], v[72:73]
	v_pk_add_f32 v[110:111], v[110:111], v[74:75]
	v_pk_add_f32 v[84:85], v[84:85], v[72:73]
	v_pk_add_f32 v[86:87], v[86:87], v[74:75]
	v_pk_add_f32 v[60:61], v[60:61], v[72:73]
	v_pk_add_f32 v[62:63], v[62:63], v[74:75]
	v_pk_add_f32 v[44:45], v[44:45], v[72:73]
	v_pk_add_f32 v[46:47], v[46:47], v[74:75]
	v_pk_add_f32 v[28:29], v[28:29], v[72:73]
	v_pk_add_f32 v[30:31], v[30:31], v[74:75]
	v_pk_add_f32 v[12:13], v[12:13], v[72:73]
	v_pk_add_f32 v[14:15], v[14:15], v[74:75]
	v_pk_add_f32 v[140:141], v[140:141], v[80:81]
	v_pk_add_f32 v[142:143], v[142:143], v[82:83]
	v_pk_add_f32 v[120:121], v[120:121], v[80:81]
	v_pk_add_f32 v[122:123], v[122:123], v[82:83]
	v_pk_add_f32 v[104:105], v[104:105], v[80:81]
	v_pk_add_f32 v[106:107], v[106:107], v[82:83]
	v_pk_add_f32 v[76:77], v[76:77], v[80:81]
	v_pk_add_f32 v[78:79], v[78:79], v[82:83]
	v_pk_add_f32 v[56:57], v[56:57], v[80:81]
	v_pk_add_f32 v[58:59], v[58:59], v[82:83]
	v_pk_add_f32 v[40:41], v[40:41], v[80:81]
	v_pk_add_f32 v[42:43], v[42:43], v[82:83]
	v_pk_add_f32 v[24:25], v[24:25], v[80:81]
	v_pk_add_f32 v[26:27], v[26:27], v[82:83]
	v_pk_add_f32 v[8:9], v[8:9], v[80:81]
	v_pk_add_f32 v[10:11], v[10:11], v[82:83]
	v_pk_add_f32 v[132:133], v[132:133], v[88:89]
	v_pk_add_f32 v[134:135], v[134:135], v[90:91]
	v_pk_add_f32 v[116:117], v[116:117], v[88:89]
	v_pk_add_f32 v[118:119], v[118:119], v[90:91]
	v_pk_add_f32 v[100:101], v[100:101], v[88:89]
	v_pk_add_f32 v[102:103], v[102:103], v[90:91]
	v_pk_add_f32 v[68:69], v[68:69], v[88:89]
	v_pk_add_f32 v[70:71], v[70:71], v[90:91]
	v_pk_add_f32 v[52:53], v[52:53], v[88:89]
	v_pk_add_f32 v[54:55], v[54:55], v[90:91]
	v_pk_add_f32 v[36:37], v[36:37], v[88:89]
	v_pk_add_f32 v[38:39], v[38:39], v[90:91]
	v_pk_add_f32 v[20:21], v[20:21], v[88:89]
	v_pk_add_f32 v[22:23], v[22:23], v[90:91]
	v_pk_add_f32 v[4:5], v[4:5], v[88:89]
	v_pk_add_f32 v[6:7], v[6:7], v[90:91]
	v_pk_add_f32 v[128:129], v[128:129], v[92:93]
	v_pk_add_f32 v[130:131], v[130:131], v[94:95]
	v_pk_add_f32 v[112:113], v[112:113], v[92:93]
	v_pk_add_f32 v[114:115], v[114:115], v[94:95]
	v_pk_add_f32 v[96:97], v[96:97], v[92:93]
	v_pk_add_f32 v[98:99], v[98:99], v[94:95]
	v_pk_add_f32 v[64:65], v[64:65], v[92:93]
	v_pk_add_f32 v[66:67], v[66:67], v[94:95]
	v_pk_add_f32 v[48:49], v[48:49], v[92:93]
	v_pk_add_f32 v[50:51], v[50:51], v[94:95]
	v_pk_add_f32 v[32:33], v[32:33], v[92:93]
	v_pk_add_f32 v[34:35], v[34:35], v[94:95]
	v_pk_add_f32 v[16:17], v[16:17], v[92:93]
	v_pk_add_f32 v[18:19], v[18:19], v[94:95]
	v_pk_add_f32 v[0:1], v[0:1], v[92:93]
	v_pk_add_f32 v[2:3], v[2:3], v[94:95]
	s_add_u32 s94, s98, 0xc000
	s_addc_u32 s95, s99, 0
	global_load_dwordx4 v[240:243], v191, s[94:95] offset:0 nt
	global_load_dwordx4 v[244:247], v191, s[94:95] offset:64 nt
	s_add_u32 s94, s98, 0x12000
	s_addc_u32 s95, s99, 0
	global_load_dwordx4 v[248:251], v191, s[94:95] offset:0 nt
	global_load_dwordx4 v[252:255], v191, s[94:95] offset:64 nt
	s_add_u32 s94, s98, 0x30000
	s_addc_u32 s95, s99, 0
	global_load_dwordx4 v[136:139], v191, s[94:95] offset:0 nt
	global_load_dwordx4 v[148:151], v191, s[94:95] offset:64 nt
	s_add_u32 s94, s98, 0x36000
	s_addc_u32 s95, s99, 0
	global_load_dwordx4 v[152:155], v191, s[94:95] offset:0 nt
	global_load_dwordx4 v[156:159], v191, s[94:95] offset:64 nt
	s_waitcnt vmcnt(19)
	s_waitcnt vmcnt(11)
	v_cvt_f32_f16_e32 v72, v208
	v_cvt_f32_f16_sdwa v73, v208 dst_sel:DWORD dst_unused:UNUSED_PAD src0_sel:WORD_1
	v_cvt_f32_f16_e32 v74, v209
	v_cvt_f32_f16_sdwa v75, v209 dst_sel:DWORD dst_unused:UNUSED_PAD src0_sel:WORD_1
	v_cvt_f32_f16_e32 v80, v210
	v_cvt_f32_f16_sdwa v81, v210 dst_sel:DWORD dst_unused:UNUSED_PAD src0_sel:WORD_1
	v_cvt_f32_f16_e32 v82, v211
	v_cvt_f32_f16_sdwa v83, v211 dst_sel:DWORD dst_unused:UNUSED_PAD src0_sel:WORD_1
	v_sub_f32_e32 v72, v72, v238
	v_sub_f32_e32 v73, v73, v238
	v_sub_f32_e32 v74, v74, v238
	v_sub_f32_e32 v75, v75, v238
	v_sub_f32_e32 v80, v80, v238
	v_sub_f32_e32 v81, v81, v238
	v_sub_f32_e32 v82, v82, v238
	v_sub_f32_e32 v83, v83, v238
	v_pk_mul_f32 v[72:73], v[238:239], v[72:73] op_sel:[1,0]
	v_pk_mul_f32 v[74:75], v[238:239], v[74:75] op_sel:[1,0]
	v_pk_mul_f32 v[80:81], v[238:239], v[80:81] op_sel:[1,0]
	v_pk_mul_f32 v[82:83], v[238:239], v[82:83] op_sel:[1,0]
	v_pk_fma_f32 v[144:145], v[72:73], v[160:161], v[144:145]
	v_pk_fma_f32 v[146:147], v[74:75], v[162:163], v[146:147]
	v_pk_fma_f32 v[140:141], v[80:81], v[164:165], v[140:141]
	v_pk_fma_f32 v[142:143], v[82:83], v[166:167], v[142:143]
	v_cvt_pk_f16_f32 v144, v144, v145
	v_cvt_pk_f16_f32 v145, v146, v147
	v_cvt_pk_f16_f32 v146, v140, v141
	v_cvt_pk_f16_f32 v147, v142, v143
	ds_write_b128 v235, v[144:147]
	v_fma_mix_f32 v206, v144, 1.0, 0 op_sel_hi:[1,0,0]
	v_fma_mix_f32 v207, v144, v144, 0 op_sel_hi:[1,1,0]
	v_fma_mix_f32 v206, v144, 1.0, v206 op_sel:[1,0,0] op_sel_hi:[1,0,0]
	v_fma_mix_f32 v207, v144, v144, v207 op_sel:[1,1,0] op_sel_hi:[1,1,0]
	v_fma_mix_f32 v206, v145, 1.0, v206 op_sel_hi:[1,0,0]
	v_fma_mix_f32 v207, v145, v145, v207 op_sel_hi:[1,1,0]
	v_fma_mix_f32 v206, v145, 1.0, v206 op_sel:[1,0,0] op_sel_hi:[1,0,0]
	v_fma_mix_f32 v207, v145, v145, v207 op_sel:[1,1,0] op_sel_hi:[1,1,0]
	v_fma_mix_f32 v206, v146, 1.0, v206 op_sel_hi:[1,0,0]
	v_fma_mix_f32 v207, v146, v146, v207 op_sel_hi:[1,1,0]
	v_fma_mix_f32 v206, v146, 1.0, v206 op_sel:[1,0,0] op_sel_hi:[1,0,0]
	v_fma_mix_f32 v207, v146, v146, v207 op_sel:[1,1,0] op_sel_hi:[1,1,0]
	v_fma_mix_f32 v206, v147, 1.0, v206 op_sel_hi:[1,0,0]
	v_fma_mix_f32 v207, v147, v147, v207 op_sel_hi:[1,1,0]
	v_fma_mix_f32 v206, v147, 1.0, v206 op_sel:[1,0,0] op_sel_hi:[1,0,0]
	v_fma_mix_f32 v207, v147, v147, v207 op_sel:[1,1,0] op_sel_hi:[1,1,0]
	s_waitcnt vmcnt(10)
	v_cvt_f32_f16_e32 v72, v212
	v_cvt_f32_f16_sdwa v73, v212 dst_sel:DWORD dst_unused:UNUSED_PAD src0_sel:WORD_1
	v_cvt_f32_f16_e32 v74, v213
	v_cvt_f32_f16_sdwa v75, v213 dst_sel:DWORD dst_unused:UNUSED_PAD src0_sel:WORD_1
	v_cvt_f32_f16_e32 v80, v214
	v_cvt_f32_f16_sdwa v81, v214 dst_sel:DWORD dst_unused:UNUSED_PAD src0_sel:WORD_1
	v_cvt_f32_f16_e32 v82, v215
	v_cvt_f32_f16_sdwa v83, v215 dst_sel:DWORD dst_unused:UNUSED_PAD src0_sel:WORD_1
	v_sub_f32_e32 v72, v72, v238
	v_sub_f32_e32 v73, v73, v238
	v_sub_f32_e32 v74, v74, v238
	v_sub_f32_e32 v75, v75, v238
	v_sub_f32_e32 v80, v80, v238
	v_sub_f32_e32 v81, v81, v238
	v_sub_f32_e32 v82, v82, v238
	v_sub_f32_e32 v83, v83, v238
	v_pk_mul_f32 v[72:73], v[238:239], v[72:73] op_sel:[1,0]
	v_pk_mul_f32 v[74:75], v[238:239], v[74:75] op_sel:[1,0]
	v_pk_mul_f32 v[80:81], v[238:239], v[80:81] op_sel:[1,0]
	v_pk_mul_f32 v[82:83], v[238:239], v[82:83] op_sel:[1,0]
	v_pk_fma_f32 v[132:133], v[72:73], v[168:169], v[132:133]
	v_pk_fma_f32 v[134:135], v[74:75], v[170:171], v[134:135]
	v_pk_fma_f32 v[128:129], v[80:81], v[172:173], v[128:129]
	v_pk_fma_f32 v[130:131], v[82:83], v[174:175], v[130:131]
	v_cvt_pk_f16_f32 v132, v132, v133
	v_cvt_pk_f16_f32 v133, v134, v135
	v_cvt_pk_f16_f32 v134, v128, v129
	v_cvt_pk_f16_f32 v135, v130, v131
	ds_write_b128 v235, v[132:135] offset:64
	v_fma_mix_f32 v206, v132, 1.0, v206 op_sel_hi:[1,0,0]
	v_fma_mix_f32 v207, v132, v132, v207 op_sel_hi:[1,1,0]
	v_fma_mix_f32 v206, v132, 1.0, v206 op_sel:[1,0,0] op_sel_hi:[1,0,0]
	v_fma_mix_f32 v207, v132, v132, v207 op_sel:[1,1,0] op_sel_hi:[1,1,0]
	v_fma_mix_f32 v206, v133, 1.0, v206 op_sel_hi:[1,0,0]
	v_fma_mix_f32 v207, v133, v133, v207 op_sel_hi:[1,1,0]
	v_fma_mix_f32 v206, v133, 1.0, v206 op_sel:[1,0,0] op_sel_hi:[1,0,0]
	v_fma_mix_f32 v207, v133, v133, v207 op_sel:[1,1,0] op_sel_hi:[1,1,0]
	v_fma_mix_f32 v206, v134, 1.0, v206 op_sel_hi:[1,0,0]
	v_fma_mix_f32 v207, v134, v134, v207 op_sel_hi:[1,1,0]
	v_fma_mix_f32 v206, v134, 1.0, v206 op_sel:[1,0,0] op_sel_hi:[1,0,0]
	v_fma_mix_f32 v207, v134, v134, v207 op_sel:[1,1,0] op_sel_hi:[1,1,0]
	v_fma_mix_f32 v206, v135, 1.0, v206 op_sel_hi:[1,0,0]
	v_fma_mix_f32 v207, v135, v135, v207 op_sel_hi:[1,1,0]
	v_fma_mix_f32 v206, v135, 1.0, v206 op_sel:[1,0,0] op_sel_hi:[1,0,0]
	v_fma_mix_f32 v207, v135, v135, v207 op_sel:[1,1,0] op_sel_hi:[1,1,0]
	ds_read_b128 v[88:91], v236
	ds_read_b128 v[92:95], v236 offset:1152
	s_waitcnt vmcnt(9)
	v_cvt_f32_f16_e32 v72, v216
	v_cvt_f32_f16_sdwa v73, v216 dst_sel:DWORD dst_unused:UNUSED_PAD src0_sel:WORD_1
	v_cvt_f32_f16_e32 v74, v217
	v_cvt_f32_f16_sdwa v75, v217 dst_sel:DWORD dst_unused:UNUSED_PAD src0_sel:WORD_1
	v_cvt_f32_f16_e32 v80, v218
	v_cvt_f32_f16_sdwa v81, v218 dst_sel:DWORD dst_unused:UNUSED_PAD src0_sel:WORD_1
	v_cvt_f32_f16_e32 v82, v219
	v_cvt_f32_f16_sdwa v83, v219 dst_sel:DWORD dst_unused:UNUSED_PAD src0_sel:WORD_1
	v_sub_f32_e32 v72, v72, v192
	v_sub_f32_e32 v73, v73, v192
	v_sub_f32_e32 v74, v74, v192
	v_sub_f32_e32 v75, v75, v192
	v_sub_f32_e32 v80, v80, v192
	v_sub_f32_e32 v81, v81, v192
	v_sub_f32_e32 v82, v82, v192
	v_sub_f32_e32 v83, v83, v192
	v_pk_mul_f32 v[72:73], v[192:193], v[72:73] op_sel:[1,0]
	v_pk_mul_f32 v[74:75], v[192:193], v[74:75] op_sel:[1,0]
	v_pk_mul_f32 v[80:81], v[192:193], v[80:81] op_sel:[1,0]
	v_pk_mul_f32 v[82:83], v[192:193], v[82:83] op_sel:[1,0]
	v_pk_fma_f32 v[124:125], v[72:73], v[160:161], v[124:125]
	v_pk_fma_f32 v[126:127], v[74:75], v[162:163], v[126:127]
	v_pk_fma_f32 v[120:121], v[80:81], v[164:165], v[120:121]
	v_pk_fma_f32 v[122:123], v[82:83], v[166:167], v[122:123]
	v_cvt_pk_f16_f32 v124, v124, v125
	v_cvt_pk_f16_f32 v125, v126, v127
	v_cvt_pk_f16_f32 v126, v120, v121
	v_cvt_pk_f16_f32 v127, v122, v123
	s_waitcnt lgkmcnt(0)
	buffer_store_dwordx4 v[88:91], v224, s[24:27], 0 offen nt
	v_add_u32_e32 v82, 0x3000, v224
	buffer_store_dwordx4 v[92:95], v82, s[24:27], 0 offen nt
	ds_write_b128 v235, v[124:127]
	v_fma_mix_f32 v140, v124, 1.0, 0 op_sel_hi:[1,0,0]
	v_fma_mix_f32 v141, v124, v124, 0 op_sel_hi:[1,1,0]
	v_fma_mix_f32 v140, v124, 1.0, v140 op_sel:[1,0,0] op_sel_hi:[1,0,0]
	v_fma_mix_f32 v141, v124, v124, v141 op_sel:[1,1,0] op_sel_hi:[1,1,0]
	v_fma_mix_f32 v140, v125, 1.0, v140 op_sel_hi:[1,0,0]
	v_fma_mix_f32 v141, v125, v125, v141 op_sel_hi:[1,1,0]
	v_fma_mix_f32 v140, v125, 1.0, v140 op_sel:[1,0,0] op_sel_hi:[1,0,0]
	v_fma_mix_f32 v141, v125, v125, v141 op_sel:[1,1,0] op_sel_hi:[1,1,0]
	v_fma_mix_f32 v140, v126, 1.0, v140 op_sel_hi:[1,0,0]
	v_fma_mix_f32 v141, v126, v126, v141 op_sel_hi:[1,1,0]
	v_fma_mix_f32 v140, v126, 1.0, v140 op_sel:[1,0,0] op_sel_hi:[1,0,0]
	v_fma_mix_f32 v141, v126, v126, v141 op_sel:[1,1,0] op_sel_hi:[1,1,0]
	v_fma_mix_f32 v140, v127, 1.0, v140 op_sel_hi:[1,0,0]
	v_fma_mix_f32 v141, v127, v127, v141 op_sel_hi:[1,1,0]
	v_fma_mix_f32 v140, v127, 1.0, v140 op_sel:[1,0,0] op_sel_hi:[1,0,0]
	v_fma_mix_f32 v141, v127, v127, v141 op_sel:[1,1,0] op_sel_hi:[1,1,0]
	s_waitcnt vmcnt(10)
	v_cvt_f32_f16_e32 v72, v220
	v_cvt_f32_f16_sdwa v73, v220 dst_sel:DWORD dst_unused:UNUSED_PAD src0_sel:WORD_1
	v_cvt_f32_f16_e32 v74, v221
	v_cvt_f32_f16_sdwa v75, v221 dst_sel:DWORD dst_unused:UNUSED_PAD src0_sel:WORD_1
	v_cvt_f32_f16_e32 v80, v222
	v_cvt_f32_f16_sdwa v81, v222 dst_sel:DWORD dst_unused:UNUSED_PAD src0_sel:WORD_1
	v_cvt_f32_f16_e32 v82, v223
	v_cvt_f32_f16_sdwa v83, v223 dst_sel:DWORD dst_unused:UNUSED_PAD src0_sel:WORD_1
	v_sub_f32_e32 v72, v72, v192
	v_sub_f32_e32 v73, v73, v192
	v_sub_f32_e32 v74, v74, v192
	v_sub_f32_e32 v75, v75, v192
	v_sub_f32_e32 v80, v80, v192
	v_sub_f32_e32 v81, v81, v192
	v_sub_f32_e32 v82, v82, v192
	v_sub_f32_e32 v83, v83, v192
	v_pk_mul_f32 v[72:73], v[192:193], v[72:73] op_sel:[1,0]
	v_pk_mul_f32 v[74:75], v[192:193], v[74:75] op_sel:[1,0]
	v_pk_mul_f32 v[80:81], v[192:193], v[80:81] op_sel:[1,0]
	v_pk_mul_f32 v[82:83], v[192:193], v[82:83] op_sel:[1,0]
	v_pk_fma_f32 v[116:117], v[72:73], v[168:169], v[116:117]
	v_pk_fma_f32 v[118:119], v[74:75], v[170:171], v[118:119]
	v_pk_fma_f32 v[112:113], v[80:81], v[172:173], v[112:113]
	v_pk_fma_f32 v[114:115], v[82:83], v[174:175], v[114:115]
	v_cvt_pk_f16_f32 v116, v116, v117
	v_cvt_pk_f16_f32 v117, v118, v119
	v_cvt_pk_f16_f32 v118, v112, v113
	v_cvt_pk_f16_f32 v119, v114, v115
	ds_write_b128 v235, v[116:119] offset:64
	v_fma_mix_f32 v140, v116, 1.0, v140 op_sel_hi:[1,0,0]
	v_fma_mix_f32 v141, v116, v116, v141 op_sel_hi:[1,1,0]
	v_fma_mix_f32 v140, v116, 1.0, v140 op_sel:[1,0,0] op_sel_hi:[1,0,0]
	v_fma_mix_f32 v141, v116, v116, v141 op_sel:[1,1,0] op_sel_hi:[1,1,0]
	v_fma_mix_f32 v140, v117, 1.0, v140 op_sel_hi:[1,0,0]
	v_fma_mix_f32 v141, v117, v117, v141 op_sel_hi:[1,1,0]
	v_fma_mix_f32 v140, v117, 1.0, v140 op_sel:[1,0,0] op_sel_hi:[1,0,0]
	v_fma_mix_f32 v141, v117, v117, v141 op_sel:[1,1,0] op_sel_hi:[1,1,0]
	v_fma_mix_f32 v140, v118, 1.0, v140 op_sel_hi:[1,0,0]
	v_fma_mix_f32 v141, v118, v118, v141 op_sel_hi:[1,1,0]
	v_fma_mix_f32 v140, v118, 1.0, v140 op_sel:[1,0,0] op_sel_hi:[1,0,0]
	v_fma_mix_f32 v141, v118, v118, v141 op_sel:[1,1,0] op_sel_hi:[1,1,0]
	v_fma_mix_f32 v140, v119, 1.0, v140 op_sel_hi:[1,0,0]
	v_fma_mix_f32 v141, v119, v119, v141 op_sel_hi:[1,1,0]
	v_fma_mix_f32 v140, v119, 1.0, v140 op_sel:[1,0,0] op_sel_hi:[1,0,0]
	v_fma_mix_f32 v141, v119, v119, v141 op_sel:[1,1,0] op_sel_hi:[1,1,0]
	ds_read_b128 v[208:211], v236
	ds_read_b128 v[128:131], v236 offset:1152
	s_add_u32 s94, s98, 0x3c000
	s_addc_u32 s95, s99, 0
	global_load_dwordx4 v[212:215], v191, s[94:95] offset:0 nt
	global_load_dwordx4 v[144:147], v191, s[94:95] offset:64 nt
	s_add_u32 s94, s98, 0x42000
	s_addc_u32 s95, s99, 0
	global_load_dwordx4 v[132:135], v191, s[94:95] offset:0 nt
	global_load_dwordx4 v[88:91], v191, s[94:95] offset:64 nt
	s_waitcnt vmcnt(13)
	v_cvt_f32_f16_e32 v72, v240
	v_cvt_f32_f16_sdwa v73, v240 dst_sel:DWORD dst_unused:UNUSED_PAD src0_sel:WORD_1
	v_cvt_f32_f16_e32 v74, v241
	v_cvt_f32_f16_sdwa v75, v241 dst_sel:DWORD dst_unused:UNUSED_PAD src0_sel:WORD_1
	v_cvt_f32_f16_e32 v80, v242
	v_cvt_f32_f16_sdwa v81, v242 dst_sel:DWORD dst_unused:UNUSED_PAD src0_sel:WORD_1
	v_cvt_f32_f16_e32 v82, v243
	v_cvt_f32_f16_sdwa v83, v243 dst_sel:DWORD dst_unused:UNUSED_PAD src0_sel:WORD_1
	v_sub_f32_e32 v72, v72, v194
	v_sub_f32_e32 v73, v73, v194
	v_sub_f32_e32 v74, v74, v194
	v_sub_f32_e32 v75, v75, v194
	v_sub_f32_e32 v80, v80, v194
	v_sub_f32_e32 v81, v81, v194
	v_sub_f32_e32 v82, v82, v194
	v_sub_f32_e32 v83, v83, v194
	v_pk_mul_f32 v[72:73], v[194:195], v[72:73] op_sel:[1,0]
	v_pk_mul_f32 v[74:75], v[194:195], v[74:75] op_sel:[1,0]
	v_pk_mul_f32 v[80:81], v[194:195], v[80:81] op_sel:[1,0]
	v_pk_mul_f32 v[82:83], v[194:195], v[82:83] op_sel:[1,0]
	v_pk_fma_f32 v[108:109], v[72:73], v[160:161], v[108:109]
	v_pk_fma_f32 v[110:111], v[74:75], v[162:163], v[110:111]
	v_pk_fma_f32 v[104:105], v[80:81], v[164:165], v[104:105]
	v_pk_fma_f32 v[106:107], v[82:83], v[166:167], v[106:107]
	v_cvt_pk_f16_f32 v108, v108, v109
	v_cvt_pk_f16_f32 v109, v110, v111
	v_cvt_pk_f16_f32 v110, v104, v105
	v_cvt_pk_f16_f32 v111, v106, v107
	s_waitcnt lgkmcnt(0)
	v_add_u32_e32 v83, 0x6000, v224
	buffer_store_dwordx4 v[208:211], v83, s[24:27], 0 offen nt
	v_add_u32_e32 v82, 0x9000, v224
	buffer_store_dwordx4 v[128:131], v82, s[24:27], 0 offen nt
	ds_write_b128 v235, v[108:111]
	v_fma_mix_f32 v142, v108, 1.0, 0 op_sel_hi:[1,0,0]
	v_fma_mix_f32 v143, v108, v108, 0 op_sel_hi:[1,1,0]
	v_fma_mix_f32 v142, v108, 1.0, v142 op_sel:[1,0,0] op_sel_hi:[1,0,0]
	v_fma_mix_f32 v143, v108, v108, v143 op_sel:[1,1,0] op_sel_hi:[1,1,0]
	v_fma_mix_f32 v142, v109, 1.0, v142 op_sel_hi:[1,0,0]
	v_fma_mix_f32 v143, v109, v109, v143 op_sel_hi:[1,1,0]
	v_fma_mix_f32 v142, v109, 1.0, v142 op_sel:[1,0,0] op_sel_hi:[1,0,0]
	v_fma_mix_f32 v143, v109, v109, v143 op_sel:[1,1,0] op_sel_hi:[1,1,0]
	v_fma_mix_f32 v142, v110, 1.0, v142 op_sel_hi:[1,0,0]
	v_fma_mix_f32 v143, v110, v110, v143 op_sel_hi:[1,1,0]
	v_fma_mix_f32 v142, v110, 1.0, v142 op_sel:[1,0,0] op_sel_hi:[1,0,0]
	v_fma_mix_f32 v143, v110, v110, v143 op_sel:[1,1,0] op_sel_hi:[1,1,0]
	v_fma_mix_f32 v142, v111, 1.0, v142 op_sel_hi:[1,0,0]
	v_fma_mix_f32 v143, v111, v111, v143 op_sel_hi:[1,1,0]
	v_fma_mix_f32 v142, v111, 1.0, v142 op_sel:[1,0,0] op_sel_hi:[1,0,0]
	v_fma_mix_f32 v143, v111, v111, v143 op_sel:[1,1,0] op_sel_hi:[1,1,0]
	s_waitcnt vmcnt(14)
	v_cvt_f32_f16_e32 v72, v244
	v_cvt_f32_f16_sdwa v73, v244 dst_sel:DWORD dst_unused:UNUSED_PAD src0_sel:WORD_1
	v_cvt_f32_f16_e32 v74, v245
	v_cvt_f32_f16_sdwa v75, v245 dst_sel:DWORD dst_unused:UNUSED_PAD src0_sel:WORD_1
	v_cvt_f32_f16_e32 v80, v246
	v_cvt_f32_f16_sdwa v81, v246 dst_sel:DWORD dst_unused:UNUSED_PAD src0_sel:WORD_1
	v_cvt_f32_f16_e32 v82, v247
	v_cvt_f32_f16_sdwa v83, v247 dst_sel:DWORD dst_unused:UNUSED_PAD src0_sel:WORD_1
	v_sub_f32_e32 v72, v72, v194
	v_sub_f32_e32 v73, v73, v194
	v_sub_f32_e32 v74, v74, v194
	v_sub_f32_e32 v75, v75, v194
	v_sub_f32_e32 v80, v80, v194
	v_sub_f32_e32 v81, v81, v194
	v_sub_f32_e32 v82, v82, v194
	v_sub_f32_e32 v83, v83, v194
	v_pk_mul_f32 v[72:73], v[194:195], v[72:73] op_sel:[1,0]
	v_pk_mul_f32 v[74:75], v[194:195], v[74:75] op_sel:[1,0]
	v_pk_mul_f32 v[80:81], v[194:195], v[80:81] op_sel:[1,0]
	v_pk_mul_f32 v[82:83], v[194:195], v[82:83] op_sel:[1,0]
	v_pk_fma_f32 v[100:101], v[72:73], v[168:169], v[100:101]
	v_pk_fma_f32 v[102:103], v[74:75], v[170:171], v[102:103]
	v_pk_fma_f32 v[96:97], v[80:81], v[172:173], v[96:97]
	v_pk_fma_f32 v[98:99], v[82:83], v[174:175], v[98:99]
	v_cvt_pk_f16_f32 v100, v100, v101
	v_cvt_pk_f16_f32 v101, v102, v103
	v_cvt_pk_f16_f32 v102, v96, v97
	v_cvt_pk_f16_f32 v103, v98, v99
	ds_write_b128 v235, v[100:103] offset:64
	v_fma_mix_f32 v142, v100, 1.0, v142 op_sel_hi:[1,0,0]
	v_fma_mix_f32 v143, v100, v100, v143 op_sel_hi:[1,1,0]
	v_fma_mix_f32 v142, v100, 1.0, v142 op_sel:[1,0,0] op_sel_hi:[1,0,0]
	v_fma_mix_f32 v143, v100, v100, v143 op_sel:[1,1,0] op_sel_hi:[1,1,0]
	v_fma_mix_f32 v142, v101, 1.0, v142 op_sel_hi:[1,0,0]
	v_fma_mix_f32 v143, v101, v101, v143 op_sel_hi:[1,1,0]
	v_fma_mix_f32 v142, v101, 1.0, v142 op_sel:[1,0,0] op_sel_hi:[1,0,0]
	v_fma_mix_f32 v143, v101, v101, v143 op_sel:[1,1,0] op_sel_hi:[1,1,0]
	v_fma_mix_f32 v142, v102, 1.0, v142 op_sel_hi:[1,0,0]
	v_fma_mix_f32 v143, v102, v102, v143 op_sel_hi:[1,1,0]
	v_fma_mix_f32 v142, v102, 1.0, v142 op_sel:[1,0,0] op_sel_hi:[1,0,0]
	v_fma_mix_f32 v143, v102, v102, v143 op_sel:[1,1,0] op_sel_hi:[1,1,0]
	v_fma_mix_f32 v142, v103, 1.0, v142 op_sel_hi:[1,0,0]
	v_fma_mix_f32 v143, v103, v103, v143 op_sel_hi:[1,1,0]
	v_fma_mix_f32 v142, v103, 1.0, v142 op_sel:[1,0,0] op_sel_hi:[1,0,0]
	v_fma_mix_f32 v143, v103, v103, v143 op_sel:[1,1,0] op_sel_hi:[1,1,0]
	ds_read_b128 v[92:95], v236
	ds_read_b128 v[120:123], v236 offset:1152
	s_waitcnt vmcnt(13)
	v_cvt_f32_f16_e32 v72, v248
	v_cvt_f32_f16_sdwa v73, v248 dst_sel:DWORD dst_unused:UNUSED_PAD src0_sel:WORD_1
	v_cvt_f32_f16_e32 v74, v249
	v_cvt_f32_f16_sdwa v75, v249 dst_sel:DWORD dst_unused:UNUSED_PAD src0_sel:WORD_1
	v_cvt_f32_f16_e32 v80, v250
	v_cvt_f32_f16_sdwa v81, v250 dst_sel:DWORD dst_unused:UNUSED_PAD src0_sel:WORD_1
	v_cvt_f32_f16_e32 v82, v251
	v_cvt_f32_f16_sdwa v83, v251 dst_sel:DWORD dst_unused:UNUSED_PAD src0_sel:WORD_1
	v_sub_f32_e32 v72, v72, v196
	v_sub_f32_e32 v73, v73, v196
	v_sub_f32_e32 v74, v74, v196
	v_sub_f32_e32 v75, v75, v196
	v_sub_f32_e32 v80, v80, v196
	v_sub_f32_e32 v81, v81, v196
	v_sub_f32_e32 v82, v82, v196
	v_sub_f32_e32 v83, v83, v196
	v_pk_mul_f32 v[72:73], v[196:197], v[72:73] op_sel:[1,0]
	v_pk_mul_f32 v[74:75], v[196:197], v[74:75] op_sel:[1,0]
	v_pk_mul_f32 v[80:81], v[196:197], v[80:81] op_sel:[1,0]
	v_pk_mul_f32 v[82:83], v[196:197], v[82:83] op_sel:[1,0]
	v_pk_fma_f32 v[84:85], v[72:73], v[160:161], v[84:85]
	v_pk_fma_f32 v[86:87], v[74:75], v[162:163], v[86:87]
	v_pk_fma_f32 v[76:77], v[80:81], v[164:165], v[76:77]
	v_pk_fma_f32 v[78:79], v[82:83], v[166:167], v[78:79]
	v_cvt_pk_f16_f32 v84, v84, v85
	v_cvt_pk_f16_f32 v85, v86, v87
	v_cvt_pk_f16_f32 v86, v76, v77
	v_cvt_pk_f16_f32 v87, v78, v79
	s_waitcnt lgkmcnt(0)
	v_add_u32_e32 v83, 0xc000, v224
	buffer_store_dwordx4 v[92:95], v83, s[24:27], 0 offen nt
	v_add_u32_e32 v82, 0xf000, v224
	buffer_store_dwordx4 v[120:123], v82, s[24:27], 0 offen nt
	ds_write_b128 v235, v[84:87]
	v_fma_mix_f32 v216, v84, 1.0, 0 op_sel_hi:[1,0,0]
	v_fma_mix_f32 v217, v84, v84, 0 op_sel_hi:[1,1,0]
	v_fma_mix_f32 v216, v84, 1.0, v216 op_sel:[1,0,0] op_sel_hi:[1,0,0]
	v_fma_mix_f32 v217, v84, v84, v217 op_sel:[1,1,0] op_sel_hi:[1,1,0]
	v_fma_mix_f32 v216, v85, 1.0, v216 op_sel_hi:[1,0,0]
	v_fma_mix_f32 v217, v85, v85, v217 op_sel_hi:[1,1,0]
	v_fma_mix_f32 v216, v85, 1.0, v216 op_sel:[1,0,0] op_sel_hi:[1,0,0]
	v_fma_mix_f32 v217, v85, v85, v217 op_sel:[1,1,0] op_sel_hi:[1,1,0]
	v_fma_mix_f32 v216, v86, 1.0, v216 op_sel_hi:[1,0,0]
	v_fma_mix_f32 v217, v86, v86, v217 op_sel_hi:[1,1,0]
	v_fma_mix_f32 v216, v86, 1.0, v216 op_sel:[1,0,0] op_sel_hi:[1,0,0]
	v_fma_mix_f32 v217, v86, v86, v217 op_sel:[1,1,0] op_sel_hi:[1,1,0]
	v_fma_mix_f32 v216, v87, 1.0, v216 op_sel_hi:[1,0,0]
	v_fma_mix_f32 v217, v87, v87, v217 op_sel_hi:[1,1,0]
	v_fma_mix_f32 v216, v87, 1.0, v216 op_sel:[1,0,0] op_sel_hi:[1,0,0]
	v_fma_mix_f32 v217, v87, v87, v217 op_sel:[1,1,0] op_sel_hi:[1,1,0]
	s_waitcnt vmcnt(14)
	v_cvt_f32_f16_e32 v72, v252
	v_cvt_f32_f16_sdwa v73, v252 dst_sel:DWORD dst_unused:UNUSED_PAD src0_sel:WORD_1
	v_cvt_f32_f16_e32 v74, v253
	v_cvt_f32_f16_sdwa v75, v253 dst_sel:DWORD dst_unused:UNUSED_PAD src0_sel:WORD_1
	v_cvt_f32_f16_e32 v80, v254
	v_cvt_f32_f16_sdwa v81, v254 dst_sel:DWORD dst_unused:UNUSED_PAD src0_sel:WORD_1
	v_cvt_f32_f16_e32 v82, v255
	v_cvt_f32_f16_sdwa v83, v255 dst_sel:DWORD dst_unused:UNUSED_PAD src0_sel:WORD_1
	v_sub_f32_e32 v72, v72, v196
	v_sub_f32_e32 v73, v73, v196
	v_sub_f32_e32 v74, v74, v196
	v_sub_f32_e32 v75, v75, v196
	v_sub_f32_e32 v80, v80, v196
	v_sub_f32_e32 v81, v81, v196
	v_sub_f32_e32 v82, v82, v196
	v_sub_f32_e32 v83, v83, v196
	v_pk_mul_f32 v[72:73], v[196:197], v[72:73] op_sel:[1,0]
	v_pk_mul_f32 v[74:75], v[196:197], v[74:75] op_sel:[1,0]
	v_pk_mul_f32 v[80:81], v[196:197], v[80:81] op_sel:[1,0]
	v_pk_mul_f32 v[82:83], v[196:197], v[82:83] op_sel:[1,0]
	v_pk_fma_f32 v[68:69], v[72:73], v[168:169], v[68:69]
	v_pk_fma_f32 v[70:71], v[74:75], v[170:171], v[70:71]
	v_pk_fma_f32 v[64:65], v[80:81], v[172:173], v[64:65]
	v_pk_fma_f32 v[66:67], v[82:83], v[174:175], v[66:67]
	v_cvt_pk_f16_f32 v68, v68, v69
	v_cvt_pk_f16_f32 v69, v70, v71
	v_cvt_pk_f16_f32 v70, v64, v65
	v_cvt_pk_f16_f32 v71, v66, v67
	ds_write_b128 v235, v[68:71] offset:64
	v_fma_mix_f32 v216, v68, 1.0, v216 op_sel_hi:[1,0,0]
	v_fma_mix_f32 v217, v68, v68, v217 op_sel_hi:[1,1,0]
	v_fma_mix_f32 v216, v68, 1.0, v216 op_sel:[1,0,0] op_sel_hi:[1,0,0]
	v_fma_mix_f32 v217, v68, v68, v217 op_sel:[1,1,0] op_sel_hi:[1,1,0]
	v_fma_mix_f32 v216, v69, 1.0, v216 op_sel_hi:[1,0,0]
	v_fma_mix_f32 v217, v69, v69, v217 op_sel_hi:[1,1,0]
	v_fma_mix_f32 v216, v69, 1.0, v216 op_sel:[1,0,0] op_sel_hi:[1,0,0]
	v_fma_mix_f32 v217, v69, v69, v217 op_sel:[1,1,0] op_sel_hi:[1,1,0]
	v_fma_mix_f32 v216, v70, 1.0, v216 op_sel_hi:[1,0,0]
	v_fma_mix_f32 v217, v70, v70, v217 op_sel_hi:[1,1,0]
	v_fma_mix_f32 v216, v70, 1.0, v216 op_sel:[1,0,0] op_sel_hi:[1,0,0]
	v_fma_mix_f32 v217, v70, v70, v217 op_sel:[1,1,0] op_sel_hi:[1,1,0]
	v_fma_mix_f32 v216, v71, 1.0, v216 op_sel_hi:[1,0,0]
	v_fma_mix_f32 v217, v71, v71, v217 op_sel_hi:[1,1,0]
	v_fma_mix_f32 v216, v71, 1.0, v216 op_sel:[1,0,0] op_sel_hi:[1,0,0]
	v_fma_mix_f32 v217, v71, v71, v217 op_sel:[1,1,0] op_sel_hi:[1,1,0]
	ds_read_b128 v[112:115], v236
	ds_read_b128 v[220:223], v236 offset:1152
	s_waitcnt vmcnt(13)
	v_cvt_f32_f16_e32 v72, v136
	v_cvt_f32_f16_sdwa v73, v136 dst_sel:DWORD dst_unused:UNUSED_PAD src0_sel:WORD_1
	v_cvt_f32_f16_e32 v74, v137
	v_cvt_f32_f16_sdwa v75, v137 dst_sel:DWORD dst_unused:UNUSED_PAD src0_sel:WORD_1
	v_cvt_f32_f16_e32 v80, v138
	v_cvt_f32_f16_sdwa v81, v138 dst_sel:DWORD dst_unused:UNUSED_PAD src0_sel:WORD_1
	v_cvt_f32_f16_e32 v82, v139
	v_cvt_f32_f16_sdwa v83, v139 dst_sel:DWORD dst_unused:UNUSED_PAD src0_sel:WORD_1
	v_sub_f32_e32 v72, v72, v198
	v_sub_f32_e32 v73, v73, v198
	v_sub_f32_e32 v74, v74, v198
	v_sub_f32_e32 v75, v75, v198
	v_sub_f32_e32 v80, v80, v198
	v_sub_f32_e32 v81, v81, v198
	v_sub_f32_e32 v82, v82, v198
	v_sub_f32_e32 v83, v83, v198
	v_pk_mul_f32 v[72:73], v[198:199], v[72:73] op_sel:[1,0]
	v_pk_mul_f32 v[74:75], v[198:199], v[74:75] op_sel:[1,0]
	v_pk_mul_f32 v[80:81], v[198:199], v[80:81] op_sel:[1,0]
	v_pk_mul_f32 v[82:83], v[198:199], v[82:83] op_sel:[1,0]
	v_pk_fma_f32 v[60:61], v[72:73], v[160:161], v[60:61]
	v_pk_fma_f32 v[62:63], v[74:75], v[162:163], v[62:63]
	v_pk_fma_f32 v[56:57], v[80:81], v[164:165], v[56:57]
	v_pk_fma_f32 v[58:59], v[82:83], v[166:167], v[58:59]
	v_cvt_pk_f16_f32 v60, v60, v61
	v_cvt_pk_f16_f32 v61, v62, v63
	v_cvt_pk_f16_f32 v62, v56, v57
	v_cvt_pk_f16_f32 v63, v58, v59
	s_waitcnt lgkmcnt(0)
	v_add_u32_e32 v83, 0x12000, v224
	buffer_store_dwordx4 v[112:115], v83, s[24:27], 0 offen nt
	v_add_u32_e32 v82, 0x15000, v224
	buffer_store_dwordx4 v[220:223], v82, s[24:27], 0 offen nt
	ds_write_b128 v235, v[60:63]
	v_fma_mix_f32 v218, v60, 1.0, 0 op_sel_hi:[1,0,0]
	v_fma_mix_f32 v219, v60, v60, 0 op_sel_hi:[1,1,0]
	v_fma_mix_f32 v218, v60, 1.0, v218 op_sel:[1,0,0] op_sel_hi:[1,0,0]
	v_fma_mix_f32 v219, v60, v60, v219 op_sel:[1,1,0] op_sel_hi:[1,1,0]
	v_fma_mix_f32 v218, v61, 1.0, v218 op_sel_hi:[1,0,0]
	v_fma_mix_f32 v219, v61, v61, v219 op_sel_hi:[1,1,0]
	v_fma_mix_f32 v218, v61, 1.0, v218 op_sel:[1,0,0] op_sel_hi:[1,0,0]
	v_fma_mix_f32 v219, v61, v61, v219 op_sel:[1,1,0] op_sel_hi:[1,1,0]
	v_fma_mix_f32 v218, v62, 1.0, v218 op_sel_hi:[1,0,0]
	v_fma_mix_f32 v219, v62, v62, v219 op_sel_hi:[1,1,0]
	v_fma_mix_f32 v218, v62, 1.0, v218 op_sel:[1,0,0] op_sel_hi:[1,0,0]
	v_fma_mix_f32 v219, v62, v62, v219 op_sel:[1,1,0] op_sel_hi:[1,1,0]
	v_fma_mix_f32 v218, v63, 1.0, v218 op_sel_hi:[1,0,0]
	v_fma_mix_f32 v219, v63, v63, v219 op_sel_hi:[1,1,0]
	v_fma_mix_f32 v218, v63, 1.0, v218 op_sel:[1,0,0] op_sel_hi:[1,0,0]
	v_fma_mix_f32 v219, v63, v63, v219 op_sel:[1,1,0] op_sel_hi:[1,1,0]
	s_waitcnt vmcnt(14)
	v_cvt_f32_f16_e32 v72, v148
	v_cvt_f32_f16_sdwa v73, v148 dst_sel:DWORD dst_unused:UNUSED_PAD src0_sel:WORD_1
	v_cvt_f32_f16_e32 v74, v149
	v_cvt_f32_f16_sdwa v75, v149 dst_sel:DWORD dst_unused:UNUSED_PAD src0_sel:WORD_1
	v_cvt_f32_f16_e32 v80, v150
	v_cvt_f32_f16_sdwa v81, v150 dst_sel:DWORD dst_unused:UNUSED_PAD src0_sel:WORD_1
	v_cvt_f32_f16_e32 v82, v151
	v_cvt_f32_f16_sdwa v83, v151 dst_sel:DWORD dst_unused:UNUSED_PAD src0_sel:WORD_1
	v_sub_f32_e32 v72, v72, v198
	v_sub_f32_e32 v73, v73, v198
	v_sub_f32_e32 v74, v74, v198
	v_sub_f32_e32 v75, v75, v198
	v_sub_f32_e32 v80, v80, v198
	v_sub_f32_e32 v81, v81, v198
	v_sub_f32_e32 v82, v82, v198
	v_sub_f32_e32 v83, v83, v198
	v_pk_mul_f32 v[72:73], v[198:199], v[72:73] op_sel:[1,0]
	v_pk_mul_f32 v[74:75], v[198:199], v[74:75] op_sel:[1,0]
	v_pk_mul_f32 v[80:81], v[198:199], v[80:81] op_sel:[1,0]
	v_pk_mul_f32 v[82:83], v[198:199], v[82:83] op_sel:[1,0]
	v_pk_fma_f32 v[52:53], v[72:73], v[168:169], v[52:53]
	v_pk_fma_f32 v[54:55], v[74:75], v[170:171], v[54:55]
	v_pk_fma_f32 v[48:49], v[80:81], v[172:173], v[48:49]
	v_pk_fma_f32 v[50:51], v[82:83], v[174:175], v[50:51]
	v_cvt_pk_f16_f32 v52, v52, v53
	v_cvt_pk_f16_f32 v53, v54, v55
	v_cvt_pk_f16_f32 v54, v48, v49
	v_cvt_pk_f16_f32 v55, v50, v51
	ds_write_b128 v235, v[52:55] offset:64
	v_fma_mix_f32 v218, v52, 1.0, v218 op_sel_hi:[1,0,0]
	v_fma_mix_f32 v219, v52, v52, v219 op_sel_hi:[1,1,0]
	v_fma_mix_f32 v218, v52, 1.0, v218 op_sel:[1,0,0] op_sel_hi:[1,0,0]
	v_fma_mix_f32 v219, v52, v52, v219 op_sel:[1,1,0] op_sel_hi:[1,1,0]
	v_fma_mix_f32 v218, v53, 1.0, v218 op_sel_hi:[1,0,0]
	v_fma_mix_f32 v219, v53, v53, v219 op_sel_hi:[1,1,0]
	v_fma_mix_f32 v218, v53, 1.0, v218 op_sel:[1,0,0] op_sel_hi:[1,0,0]
	v_fma_mix_f32 v219, v53, v53, v219 op_sel:[1,1,0] op_sel_hi:[1,1,0]
	v_fma_mix_f32 v218, v54, 1.0, v218 op_sel_hi:[1,0,0]
	v_fma_mix_f32 v219, v54, v54, v219 op_sel_hi:[1,1,0]
	v_fma_mix_f32 v218, v54, 1.0, v218 op_sel:[1,0,0] op_sel_hi:[1,0,0]
	v_fma_mix_f32 v219, v54, v54, v219 op_sel:[1,1,0] op_sel_hi:[1,1,0]
	v_fma_mix_f32 v218, v55, 1.0, v218 op_sel_hi:[1,0,0]
	v_fma_mix_f32 v219, v55, v55, v219 op_sel_hi:[1,1,0]
	v_fma_mix_f32 v218, v55, 1.0, v218 op_sel:[1,0,0] op_sel_hi:[1,0,0]
	v_fma_mix_f32 v219, v55, v55, v219 op_sel:[1,1,0] op_sel_hi:[1,1,0]
	ds_read_b128 v[124:127], v236
	ds_read_b128 v[116:119], v236 offset:1152
	s_waitcnt vmcnt(13)
	v_cvt_f32_f16_e32 v72, v152
	v_cvt_f32_f16_sdwa v73, v152 dst_sel:DWORD dst_unused:UNUSED_PAD src0_sel:WORD_1
	v_cvt_f32_f16_e32 v74, v153
	v_cvt_f32_f16_sdwa v75, v153 dst_sel:DWORD dst_unused:UNUSED_PAD src0_sel:WORD_1
	v_cvt_f32_f16_e32 v80, v154
	v_cvt_f32_f16_sdwa v81, v154 dst_sel:DWORD dst_unused:UNUSED_PAD src0_sel:WORD_1
	v_cvt_f32_f16_e32 v82, v155
	v_cvt_f32_f16_sdwa v83, v155 dst_sel:DWORD dst_unused:UNUSED_PAD src0_sel:WORD_1
	v_sub_f32_e32 v72, v72, v200
	v_sub_f32_e32 v73, v73, v200
	v_sub_f32_e32 v74, v74, v200
	v_sub_f32_e32 v75, v75, v200
	v_sub_f32_e32 v80, v80, v200
	v_sub_f32_e32 v81, v81, v200
	v_sub_f32_e32 v82, v82, v200
	v_sub_f32_e32 v83, v83, v200
	v_pk_mul_f32 v[72:73], v[200:201], v[72:73] op_sel:[1,0]
	v_pk_mul_f32 v[74:75], v[200:201], v[74:75] op_sel:[1,0]
	v_pk_mul_f32 v[80:81], v[200:201], v[80:81] op_sel:[1,0]
	v_pk_mul_f32 v[82:83], v[200:201], v[82:83] op_sel:[1,0]
	v_pk_fma_f32 v[44:45], v[72:73], v[160:161], v[44:45]
	v_pk_fma_f32 v[46:47], v[74:75], v[162:163], v[46:47]
	v_pk_fma_f32 v[40:41], v[80:81], v[164:165], v[40:41]
	v_pk_fma_f32 v[42:43], v[82:83], v[166:167], v[42:43]
	v_cvt_pk_f16_f32 v44, v44, v45
	v_cvt_pk_f16_f32 v45, v46, v47
	v_cvt_pk_f16_f32 v46, v40, v41
	v_cvt_pk_f16_f32 v47, v42, v43
	s_waitcnt lgkmcnt(0)
	v_add_u32_e32 v83, 0x30000, v224
	buffer_store_dwordx4 v[124:127], v83, s[24:27], 0 offen nt
	v_add_u32_e32 v82, 0x33000, v224
	buffer_store_dwordx4 v[116:119], v82, s[24:27], 0 offen nt
	ds_write_b128 v235, v[44:47]
	v_fma_mix_f32 v208, v44, 1.0, 0 op_sel_hi:[1,0,0]
	v_fma_mix_f32 v209, v44, v44, 0 op_sel_hi:[1,1,0]
	v_fma_mix_f32 v208, v44, 1.0, v208 op_sel:[1,0,0] op_sel_hi:[1,0,0]
	v_fma_mix_f32 v209, v44, v44, v209 op_sel:[1,1,0] op_sel_hi:[1,1,0]
	v_fma_mix_f32 v208, v45, 1.0, v208 op_sel_hi:[1,0,0]
	v_fma_mix_f32 v209, v45, v45, v209 op_sel_hi:[1,1,0]
	v_fma_mix_f32 v208, v45, 1.0, v208 op_sel:[1,0,0] op_sel_hi:[1,0,0]
	v_fma_mix_f32 v209, v45, v45, v209 op_sel:[1,1,0] op_sel_hi:[1,1,0]
	v_fma_mix_f32 v208, v46, 1.0, v208 op_sel_hi:[1,0,0]
	v_fma_mix_f32 v209, v46, v46, v209 op_sel_hi:[1,1,0]
	v_fma_mix_f32 v208, v46, 1.0, v208 op_sel:[1,0,0] op_sel_hi:[1,0,0]
	v_fma_mix_f32 v209, v46, v46, v209 op_sel:[1,1,0] op_sel_hi:[1,1,0]
	v_fma_mix_f32 v208, v47, 1.0, v208 op_sel_hi:[1,0,0]
	v_fma_mix_f32 v209, v47, v47, v209 op_sel_hi:[1,1,0]
	v_fma_mix_f32 v208, v47, 1.0, v208 op_sel:[1,0,0] op_sel_hi:[1,0,0]
	v_fma_mix_f32 v209, v47, v47, v209 op_sel:[1,1,0] op_sel_hi:[1,1,0]
	s_waitcnt vmcnt(14)
	v_cvt_f32_f16_e32 v72, v156
	v_cvt_f32_f16_sdwa v73, v156 dst_sel:DWORD dst_unused:UNUSED_PAD src0_sel:WORD_1
	v_cvt_f32_f16_e32 v74, v157
	v_cvt_f32_f16_sdwa v75, v157 dst_sel:DWORD dst_unused:UNUSED_PAD src0_sel:WORD_1
	v_cvt_f32_f16_e32 v80, v158
	v_cvt_f32_f16_sdwa v81, v158 dst_sel:DWORD dst_unused:UNUSED_PAD src0_sel:WORD_1
	v_cvt_f32_f16_e32 v82, v159
	v_cvt_f32_f16_sdwa v83, v159 dst_sel:DWORD dst_unused:UNUSED_PAD src0_sel:WORD_1
	v_sub_f32_e32 v72, v72, v200
	v_sub_f32_e32 v73, v73, v200
	v_sub_f32_e32 v74, v74, v200
	v_sub_f32_e32 v75, v75, v200
	v_sub_f32_e32 v80, v80, v200
	v_sub_f32_e32 v81, v81, v200
	v_sub_f32_e32 v82, v82, v200
	v_sub_f32_e32 v83, v83, v200
	v_pk_mul_f32 v[72:73], v[200:201], v[72:73] op_sel:[1,0]
	v_pk_mul_f32 v[74:75], v[200:201], v[74:75] op_sel:[1,0]
	v_pk_mul_f32 v[80:81], v[200:201], v[80:81] op_sel:[1,0]
	v_pk_mul_f32 v[82:83], v[200:201], v[82:83] op_sel:[1,0]
	v_pk_fma_f32 v[36:37], v[72:73], v[168:169], v[36:37]
	v_pk_fma_f32 v[38:39], v[74:75], v[170:171], v[38:39]
	v_pk_fma_f32 v[32:33], v[80:81], v[172:173], v[32:33]
	v_pk_fma_f32 v[34:35], v[82:83], v[174:175], v[34:35]
	v_cvt_pk_f16_f32 v36, v36, v37
	v_cvt_pk_f16_f32 v37, v38, v39
	v_cvt_pk_f16_f32 v38, v32, v33
	v_cvt_pk_f16_f32 v39, v34, v35
	ds_write_b128 v235, v[36:39] offset:64
	v_fma_mix_f32 v208, v36, 1.0, v208 op_sel_hi:[1,0,0]
	v_fma_mix_f32 v209, v36, v36, v209 op_sel_hi:[1,1,0]
	v_fma_mix_f32 v208, v36, 1.0, v208 op_sel:[1,0,0] op_sel_hi:[1,0,0]
	v_fma_mix_f32 v209, v36, v36, v209 op_sel:[1,1,0] op_sel_hi:[1,1,0]
	v_fma_mix_f32 v208, v37, 1.0, v208 op_sel_hi:[1,0,0]
	v_fma_mix_f32 v209, v37, v37, v209 op_sel_hi:[1,1,0]
	v_fma_mix_f32 v208, v37, 1.0, v208 op_sel:[1,0,0] op_sel_hi:[1,0,0]
	v_fma_mix_f32 v209, v37, v37, v209 op_sel:[1,1,0] op_sel_hi:[1,1,0]
	v_fma_mix_f32 v208, v38, 1.0, v208 op_sel_hi:[1,0,0]
	v_fma_mix_f32 v209, v38, v38, v209 op_sel_hi:[1,1,0]
	v_fma_mix_f32 v208, v38, 1.0, v208 op_sel:[1,0,0] op_sel_hi:[1,0,0]
	v_fma_mix_f32 v209, v38, v38, v209 op_sel:[1,1,0] op_sel_hi:[1,1,0]
	v_fma_mix_f32 v208, v39, 1.0, v208 op_sel_hi:[1,0,0]
	v_fma_mix_f32 v209, v39, v39, v209 op_sel_hi:[1,1,0]
	v_fma_mix_f32 v208, v39, 1.0, v208 op_sel:[1,0,0] op_sel_hi:[1,0,0]
	v_fma_mix_f32 v209, v39, v39, v209 op_sel:[1,1,0] op_sel_hi:[1,1,0]
	ds_read_b128 v[128:131], v236
	ds_read_b128 v[104:107], v236 offset:1152
	s_waitcnt vmcnt(11)
	v_cvt_f32_f16_e32 v72, v212
	v_cvt_f32_f16_sdwa v73, v212 dst_sel:DWORD dst_unused:UNUSED_PAD src0_sel:WORD_1
	v_cvt_f32_f16_e32 v74, v213
	v_cvt_f32_f16_sdwa v75, v213 dst_sel:DWORD dst_unused:UNUSED_PAD src0_sel:WORD_1
	v_cvt_f32_f16_e32 v80, v214
	v_cvt_f32_f16_sdwa v81, v214 dst_sel:DWORD dst_unused:UNUSED_PAD src0_sel:WORD_1
	v_cvt_f32_f16_e32 v82, v215
	v_cvt_f32_f16_sdwa v83, v215 dst_sel:DWORD dst_unused:UNUSED_PAD src0_sel:WORD_1
	v_sub_f32_e32 v72, v72, v202
	v_sub_f32_e32 v73, v73, v202
	v_sub_f32_e32 v74, v74, v202
	v_sub_f32_e32 v75, v75, v202
	v_sub_f32_e32 v80, v80, v202
	v_sub_f32_e32 v81, v81, v202
	v_sub_f32_e32 v82, v82, v202
	v_sub_f32_e32 v83, v83, v202
	v_pk_mul_f32 v[72:73], v[202:203], v[72:73] op_sel:[1,0]
	v_pk_mul_f32 v[74:75], v[202:203], v[74:75] op_sel:[1,0]
	v_pk_mul_f32 v[80:81], v[202:203], v[80:81] op_sel:[1,0]
	v_pk_mul_f32 v[82:83], v[202:203], v[82:83] op_sel:[1,0]
	v_pk_fma_f32 v[28:29], v[72:73], v[160:161], v[28:29]
	v_pk_fma_f32 v[30:31], v[74:75], v[162:163], v[30:31]
	v_pk_fma_f32 v[24:25], v[80:81], v[164:165], v[24:25]
	v_pk_fma_f32 v[26:27], v[82:83], v[166:167], v[26:27]
	v_cvt_pk_f16_f32 v28, v28, v29
	v_cvt_pk_f16_f32 v29, v30, v31
	v_cvt_pk_f16_f32 v30, v24, v25
	v_cvt_pk_f16_f32 v31, v26, v27
	s_waitcnt lgkmcnt(0)
	v_add_u32_e32 v83, 0x36000, v224
	buffer_store_dwordx4 v[128:131], v83, s[24:27], 0 offen nt
	v_add_u32_e32 v82, 0x39000, v224
	buffer_store_dwordx4 v[104:107], v82, s[24:27], 0 offen nt
	ds_write_b128 v235, v[28:31]
	v_fma_mix_f32 v210, v28, 1.0, 0 op_sel_hi:[1,0,0]
	v_fma_mix_f32 v211, v28, v28, 0 op_sel_hi:[1,1,0]
	v_fma_mix_f32 v210, v28, 1.0, v210 op_sel:[1,0,0] op_sel_hi:[1,0,0]
	v_fma_mix_f32 v211, v28, v28, v211 op_sel:[1,1,0] op_sel_hi:[1,1,0]
	v_fma_mix_f32 v210, v29, 1.0, v210 op_sel_hi:[1,0,0]
	v_fma_mix_f32 v211, v29, v29, v211 op_sel_hi:[1,1,0]
	v_fma_mix_f32 v210, v29, 1.0, v210 op_sel:[1,0,0] op_sel_hi:[1,0,0]
	v_fma_mix_f32 v211, v29, v29, v211 op_sel:[1,1,0] op_sel_hi:[1,1,0]
	v_fma_mix_f32 v210, v30, 1.0, v210 op_sel_hi:[1,0,0]
	v_fma_mix_f32 v211, v30, v30, v211 op_sel_hi:[1,1,0]
	v_fma_mix_f32 v210, v30, 1.0, v210 op_sel:[1,0,0] op_sel_hi:[1,0,0]
	v_fma_mix_f32 v211, v30, v30, v211 op_sel:[1,1,0] op_sel_hi:[1,1,0]
	v_fma_mix_f32 v210, v31, 1.0, v210 op_sel_hi:[1,0,0]
	v_fma_mix_f32 v211, v31, v31, v211 op_sel_hi:[1,1,0]
	v_fma_mix_f32 v210, v31, 1.0, v210 op_sel:[1,0,0] op_sel_hi:[1,0,0]
	v_fma_mix_f32 v211, v31, v31, v211 op_sel:[1,1,0] op_sel_hi:[1,1,0]
	s_waitcnt vmcnt(12)
	v_cvt_f32_f16_e32 v72, v144
	v_cvt_f32_f16_sdwa v73, v144 dst_sel:DWORD dst_unused:UNUSED_PAD src0_sel:WORD_1
	v_cvt_f32_f16_e32 v74, v145
	v_cvt_f32_f16_sdwa v75, v145 dst_sel:DWORD dst_unused:UNUSED_PAD src0_sel:WORD_1
	v_cvt_f32_f16_e32 v80, v146
	v_cvt_f32_f16_sdwa v81, v146 dst_sel:DWORD dst_unused:UNUSED_PAD src0_sel:WORD_1
	v_cvt_f32_f16_e32 v82, v147
	v_cvt_f32_f16_sdwa v83, v147 dst_sel:DWORD dst_unused:UNUSED_PAD src0_sel:WORD_1
	v_sub_f32_e32 v72, v72, v202
	v_sub_f32_e32 v73, v73, v202
	v_sub_f32_e32 v74, v74, v202
	v_sub_f32_e32 v75, v75, v202
	v_sub_f32_e32 v80, v80, v202
	v_sub_f32_e32 v81, v81, v202
	v_sub_f32_e32 v82, v82, v202
	v_sub_f32_e32 v83, v83, v202
	v_pk_mul_f32 v[72:73], v[202:203], v[72:73] op_sel:[1,0]
	v_pk_mul_f32 v[74:75], v[202:203], v[74:75] op_sel:[1,0]
	v_pk_mul_f32 v[80:81], v[202:203], v[80:81] op_sel:[1,0]
	v_pk_mul_f32 v[82:83], v[202:203], v[82:83] op_sel:[1,0]
	v_pk_fma_f32 v[20:21], v[72:73], v[168:169], v[20:21]
	v_pk_fma_f32 v[22:23], v[74:75], v[170:171], v[22:23]
	v_pk_fma_f32 v[16:17], v[80:81], v[172:173], v[16:17]
	v_pk_fma_f32 v[18:19], v[82:83], v[174:175], v[18:19]
	v_cvt_pk_f16_f32 v20, v20, v21
	v_cvt_pk_f16_f32 v21, v22, v23
	v_cvt_pk_f16_f32 v22, v16, v17
	v_cvt_pk_f16_f32 v23, v18, v19
	ds_write_b128 v235, v[20:23] offset:64
	v_fma_mix_f32 v210, v20, 1.0, v210 op_sel_hi:[1,0,0]
	v_fma_mix_f32 v211, v20, v20, v211 op_sel_hi:[1,1,0]
	v_fma_mix_f32 v210, v20, 1.0, v210 op_sel:[1,0,0] op_sel_hi:[1,0,0]
	v_fma_mix_f32 v211, v20, v20, v211 op_sel:[1,1,0] op_sel_hi:[1,1,0]
	v_fma_mix_f32 v210, v21, 1.0, v210 op_sel_hi:[1,0,0]
	v_fma_mix_f32 v211, v21, v21, v211 op_sel_hi:[1,1,0]
	v_fma_mix_f32 v210, v21, 1.0, v210 op_sel:[1,0,0] op_sel_hi:[1,0,0]
	v_fma_mix_f32 v211, v21, v21, v211 op_sel:[1,1,0] op_sel_hi:[1,1,0]
	v_fma_mix_f32 v210, v22, 1.0, v210 op_sel_hi:[1,0,0]
	v_fma_mix_f32 v211, v22, v22, v211 op_sel_hi:[1,1,0]
	v_fma_mix_f32 v210, v22, 1.0, v210 op_sel:[1,0,0] op_sel_hi:[1,0,0]
	v_fma_mix_f32 v211, v22, v22, v211 op_sel:[1,1,0] op_sel_hi:[1,1,0]
	v_fma_mix_f32 v210, v23, 1.0, v210 op_sel_hi:[1,0,0]
	v_fma_mix_f32 v211, v23, v23, v211 op_sel_hi:[1,1,0]
	v_fma_mix_f32 v210, v23, 1.0, v210 op_sel:[1,0,0] op_sel_hi:[1,0,0]
	v_fma_mix_f32 v211, v23, v23, v211 op_sel:[1,1,0] op_sel_hi:[1,1,0]
	ds_read_b128 v[240:243], v236
	ds_read_b128 v[96:99], v236 offset:1152
	s_waitcnt vmcnt(11)
	v_cvt_f32_f16_e32 v72, v132
	v_cvt_f32_f16_sdwa v73, v132 dst_sel:DWORD dst_unused:UNUSED_PAD src0_sel:WORD_1
	v_cvt_f32_f16_e32 v74, v133
	v_cvt_f32_f16_sdwa v75, v133 dst_sel:DWORD dst_unused:UNUSED_PAD src0_sel:WORD_1
	v_cvt_f32_f16_e32 v80, v134
	v_cvt_f32_f16_sdwa v81, v134 dst_sel:DWORD dst_unused:UNUSED_PAD src0_sel:WORD_1
	v_cvt_f32_f16_e32 v82, v135
	v_cvt_f32_f16_sdwa v83, v135 dst_sel:DWORD dst_unused:UNUSED_PAD src0_sel:WORD_1
	v_sub_f32_e32 v72, v72, v204
	v_sub_f32_e32 v73, v73, v204
	v_sub_f32_e32 v74, v74, v204
	v_sub_f32_e32 v75, v75, v204
	v_sub_f32_e32 v80, v80, v204
	v_sub_f32_e32 v81, v81, v204
	v_sub_f32_e32 v82, v82, v204
	v_sub_f32_e32 v83, v83, v204
	v_pk_mul_f32 v[72:73], v[204:205], v[72:73] op_sel:[1,0]
	v_pk_mul_f32 v[74:75], v[204:205], v[74:75] op_sel:[1,0]
	v_pk_mul_f32 v[80:81], v[204:205], v[80:81] op_sel:[1,0]
	v_pk_mul_f32 v[82:83], v[204:205], v[82:83] op_sel:[1,0]
	v_pk_fma_f32 v[12:13], v[72:73], v[160:161], v[12:13]
	v_pk_fma_f32 v[14:15], v[74:75], v[162:163], v[14:15]
	v_pk_fma_f32 v[8:9], v[80:81], v[164:165], v[8:9]
	v_pk_fma_f32 v[10:11], v[82:83], v[166:167], v[10:11]
	v_cvt_pk_f16_f32 v12, v12, v13
	v_cvt_pk_f16_f32 v13, v14, v15
	v_cvt_pk_f16_f32 v14, v8, v9
	v_cvt_pk_f16_f32 v15, v10, v11
	s_waitcnt lgkmcnt(0)
	v_add_u32_e32 v83, 0x3c000, v224
	buffer_store_dwordx4 v[240:243], v83, s[24:27], 0 offen nt
	v_add_u32_e32 v82, 0x3f000, v224
	buffer_store_dwordx4 v[96:99], v82, s[24:27], 0 offen nt
	ds_write_b128 v235, v[12:15]
	v_fma_mix_f32 v244, v12, 1.0, 0 op_sel_hi:[1,0,0]
	v_fma_mix_f32 v245, v12, v12, 0 op_sel_hi:[1,1,0]
	v_fma_mix_f32 v244, v12, 1.0, v244 op_sel:[1,0,0] op_sel_hi:[1,0,0]
	v_fma_mix_f32 v245, v12, v12, v245 op_sel:[1,1,0] op_sel_hi:[1,1,0]
	v_fma_mix_f32 v244, v13, 1.0, v244 op_sel_hi:[1,0,0]
	v_fma_mix_f32 v245, v13, v13, v245 op_sel_hi:[1,1,0]
	v_fma_mix_f32 v244, v13, 1.0, v244 op_sel:[1,0,0] op_sel_hi:[1,0,0]
	v_fma_mix_f32 v245, v13, v13, v245 op_sel:[1,1,0] op_sel_hi:[1,1,0]
	v_fma_mix_f32 v244, v14, 1.0, v244 op_sel_hi:[1,0,0]
	v_fma_mix_f32 v245, v14, v14, v245 op_sel_hi:[1,1,0]
	v_fma_mix_f32 v244, v14, 1.0, v244 op_sel:[1,0,0] op_sel_hi:[1,0,0]
	v_fma_mix_f32 v245, v14, v14, v245 op_sel:[1,1,0] op_sel_hi:[1,1,0]
	v_fma_mix_f32 v244, v15, 1.0, v244 op_sel_hi:[1,0,0]
	v_fma_mix_f32 v245, v15, v15, v245 op_sel_hi:[1,1,0]
	v_fma_mix_f32 v244, v15, 1.0, v244 op_sel:[1,0,0] op_sel_hi:[1,0,0]
	v_fma_mix_f32 v245, v15, v15, v245 op_sel:[1,1,0] op_sel_hi:[1,1,0]
	s_waitcnt vmcnt(12)
	v_cvt_f32_f16_e32 v72, v88
	v_cvt_f32_f16_sdwa v73, v88 dst_sel:DWORD dst_unused:UNUSED_PAD src0_sel:WORD_1
	v_cvt_f32_f16_e32 v74, v89
	v_cvt_f32_f16_sdwa v75, v89 dst_sel:DWORD dst_unused:UNUSED_PAD src0_sel:WORD_1
	v_cvt_f32_f16_e32 v80, v90
	v_cvt_f32_f16_sdwa v81, v90 dst_sel:DWORD dst_unused:UNUSED_PAD src0_sel:WORD_1
	v_cvt_f32_f16_e32 v82, v91
	v_cvt_f32_f16_sdwa v83, v91 dst_sel:DWORD dst_unused:UNUSED_PAD src0_sel:WORD_1
	v_sub_f32_e32 v72, v72, v204
	v_sub_f32_e32 v73, v73, v204
	v_sub_f32_e32 v74, v74, v204
	v_sub_f32_e32 v75, v75, v204
	v_sub_f32_e32 v80, v80, v204
	v_sub_f32_e32 v81, v81, v204
	v_sub_f32_e32 v82, v82, v204
	v_sub_f32_e32 v83, v83, v204
	v_pk_mul_f32 v[72:73], v[204:205], v[72:73] op_sel:[1,0]
	v_pk_mul_f32 v[74:75], v[204:205], v[74:75] op_sel:[1,0]
	v_pk_mul_f32 v[80:81], v[204:205], v[80:81] op_sel:[1,0]
	v_pk_mul_f32 v[82:83], v[204:205], v[82:83] op_sel:[1,0]
	v_pk_fma_f32 v[4:5], v[72:73], v[168:169], v[4:5]
	v_pk_fma_f32 v[6:7], v[74:75], v[170:171], v[6:7]
	v_pk_fma_f32 v[0:1], v[80:81], v[172:173], v[0:1]
	v_pk_fma_f32 v[2:3], v[82:83], v[174:175], v[2:3]
	v_cvt_pk_f16_f32 v4, v4, v5
	v_cvt_pk_f16_f32 v5, v6, v7
	v_cvt_pk_f16_f32 v6, v0, v1
	v_cvt_pk_f16_f32 v7, v2, v3
	ds_write_b128 v235, v[4:7] offset:64
	v_fma_mix_f32 v244, v4, 1.0, v244 op_sel_hi:[1,0,0]
	v_fma_mix_f32 v245, v4, v4, v245 op_sel_hi:[1,1,0]
	v_fma_mix_f32 v244, v4, 1.0, v244 op_sel:[1,0,0] op_sel_hi:[1,0,0]
	v_fma_mix_f32 v245, v4, v4, v245 op_sel:[1,1,0] op_sel_hi:[1,1,0]
	v_fma_mix_f32 v244, v5, 1.0, v244 op_sel_hi:[1,0,0]
	v_fma_mix_f32 v245, v5, v5, v245 op_sel_hi:[1,1,0]
	v_fma_mix_f32 v244, v5, 1.0, v244 op_sel:[1,0,0] op_sel_hi:[1,0,0]
	v_fma_mix_f32 v245, v5, v5, v245 op_sel:[1,1,0] op_sel_hi:[1,1,0]
	v_fma_mix_f32 v244, v6, 1.0, v244 op_sel_hi:[1,0,0]
	v_fma_mix_f32 v245, v6, v6, v245 op_sel_hi:[1,1,0]
	v_fma_mix_f32 v244, v6, 1.0, v244 op_sel:[1,0,0] op_sel_hi:[1,0,0]
	v_fma_mix_f32 v245, v6, v6, v245 op_sel:[1,1,0] op_sel_hi:[1,1,0]
	v_fma_mix_f32 v244, v7, 1.0, v244 op_sel_hi:[1,0,0]
	v_fma_mix_f32 v245, v7, v7, v245 op_sel_hi:[1,1,0]
	v_fma_mix_f32 v244, v7, 1.0, v244 op_sel:[1,0,0] op_sel_hi:[1,0,0]
	v_fma_mix_f32 v245, v7, v7, v245 op_sel:[1,1,0] op_sel_hi:[1,1,0]
	ds_read_b128 v[108:111], v236
	ds_read_b128 v[100:103], v236 offset:1152
	s_waitcnt lgkmcnt(0)
	v_add_u32_e32 v83, 0x42000, v224
	buffer_store_dwordx4 v[108:111], v83, s[24:27], 0 offen nt
	v_add_u32_e32 v82, 0x45000, v224
	buffer_store_dwordx4 v[100:103], v82, s[24:27], 0 offen nt
	v_xor_b32_e32 v225, 16, v234
	v_lshlrev_b32_e32 v225, 2, v225
	v_xor_b32_e32 v246, 32, v234
	v_lshlrev_b32_e32 v246, 2, v246
	ds_bpermute_b32 v92, v225, v206
	ds_bpermute_b32 v93, v225, v207
	ds_bpermute_b32 v94, v225, v140
	ds_bpermute_b32 v95, v225, v141
	ds_bpermute_b32 v120, v225, v142
	ds_bpermute_b32 v121, v225, v143
	ds_bpermute_b32 v122, v225, v216
	ds_bpermute_b32 v123, v225, v217
	s_waitcnt lgkmcnt(0)
	v_pk_add_f32 v[206:207], v[206:207], v[92:93]
	v_pk_add_f32 v[140:141], v[140:141], v[94:95]
	v_pk_add_f32 v[142:143], v[142:143], v[120:121]
	v_pk_add_f32 v[216:217], v[216:217], v[122:123]
	ds_bpermute_b32 v92, v225, v218
	ds_bpermute_b32 v93, v225, v219
	ds_bpermute_b32 v94, v225, v208
	ds_bpermute_b32 v95, v225, v209
	ds_bpermute_b32 v120, v225, v210
	ds_bpermute_b32 v121, v225, v211
	ds_bpermute_b32 v122, v225, v244
	ds_bpermute_b32 v123, v225, v245
	s_waitcnt lgkmcnt(0)
	v_pk_add_f32 v[218:219], v[218:219], v[92:93]
	v_pk_add_f32 v[208:209], v[208:209], v[94:95]
	v_pk_add_f32 v[210:211], v[210:211], v[120:121]
	v_pk_add_f32 v[244:245], v[244:245], v[122:123]
	ds_bpermute_b32 v92, v246, v206
	ds_bpermute_b32 v93, v246, v207
	ds_bpermute_b32 v94, v246, v140
	ds_bpermute_b32 v95, v246, v141
	ds_bpermute_b32 v120, v246, v142
	ds_bpermute_b32 v121, v246, v143
	ds_bpermute_b32 v122, v246, v216
	ds_bpermute_b32 v123, v246, v217
	s_waitcnt lgkmcnt(0)
	v_pk_add_f32 v[206:207], v[206:207], v[92:93]
	v_pk_add_f32 v[140:141], v[140:141], v[94:95]
	v_pk_add_f32 v[142:143], v[142:143], v[120:121]
	v_pk_add_f32 v[216:217], v[216:217], v[122:123]
	ds_bpermute_b32 v92, v246, v218
	ds_bpermute_b32 v93, v246, v219
	ds_bpermute_b32 v94, v246, v208
	ds_bpermute_b32 v95, v246, v209
	ds_bpermute_b32 v120, v246, v210
	ds_bpermute_b32 v121, v246, v211
	ds_bpermute_b32 v122, v246, v244
	ds_bpermute_b32 v123, v246, v245
	s_waitcnt lgkmcnt(0)
	v_pk_add_f32 v[218:219], v[218:219], v[92:93]
	v_pk_add_f32 v[208:209], v[208:209], v[94:95]
	v_pk_add_f32 v[210:211], v[210:211], v[120:121]
	v_pk_add_f32 v[244:245], v[244:245], v[122:123]
	s_mov_b64 exec, 0xffff
	global_store_dwordx2 v190, v[206:207], s[100:101] offset:0
	global_store_dwordx2 v190, v[140:141], s[100:101] offset:128
	global_store_dwordx2 v190, v[142:143], s[100:101] offset:256
	global_store_dwordx2 v190, v[216:217], s[100:101] offset:384
	global_store_dwordx2 v190, v[218:219], s[100:101] offset:1024
	global_store_dwordx2 v190, v[208:209], s[100:101] offset:1152
	global_store_dwordx2 v190, v[210:211], s[100:101] offset:1280
	global_store_dwordx2 v190, v[244:245], s[100:101] offset:1408
	s_mov_b64 exec, -1
	s_mov_b32 s83, s81
	s_mov_b32 s84, s82
	s_mov_b64 s[40:41], s[0:1]
	s_mov_b64 s[38:39], s[8:9]
	s_mov_b64 vcc, s[6:7]
	s_cbranch_vccz .LBB8_12
	s_waitcnt vmcnt(0)
	s_cmpk_gt_u32 s44, 0xff
	s_cbranch_scc1 .LBB8_31
	s_barrier

.LBB9_27:
	ds_read_b128 v[128:131], v172
	ds_read_b128 v[132:135], v172 offset:1024
	ds_read_b128 v[136:139], v172 offset:2048
	ds_read_b128 v[140:143], v172 offset:3072
	s_add_u32 s30, s28, 0xfffd0080
	s_addc_u32 s31, s29, -1
	s_cmp_eq_u32 s73, 8
	s_cselect_b32 s35, s9, s31
	s_cselect_b32 s34, s8, s30
	s_cselect_b32 s31, s1, s72
	s_cselect_b32 s30, s0, s71
	v_lshl_add_u64 v[202:203], s[28:29], 0, v[152:153]
	s_add_i32 m0, s43, 0xc000
	ds_read_b128 v[158:161], v173
	ds_read_b128 v[162:165], v173 offset:1024
	ds_read_b128 v[178:181], v173 offset:2048
	ds_read_b128 v[182:185], v173 offset:3072
	ds_read_b128 v[186:189], v173 offset:4096
	ds_read_b128 v[190:193], v173 offset:5120
	ds_read_b128 v[194:197], v173 offset:6144
	ds_read_b128 v[198:201], v173 offset:7168
	global_load_lds_dwordx4 v[202:203], off
	v_lshl_add_u64 v[202:203], s[28:29], 0, v[154:155]
	s_add_i32 m0, s43, 0xe000
	s_nop 0
	global_load_lds_dwordx4 v[202:203], off
	s_waitcnt lgkmcnt(8)
	s_barrier
	s_waitcnt lgkmcnt(0)
	v_mfma_f32_16x16x32_f16 v[124:127], v[128:131], v[158:161], v[124:127]
	v_mfma_f32_16x16x32_f16 v[120:123], v[136:139], v[158:161], v[120:123]
	v_mfma_f32_16x16x32_f16 v[108:111], v[128:131], v[178:181], v[108:111]
	v_mfma_f32_16x16x32_f16 v[104:107], v[136:139], v[178:181], v[104:107]
	v_mfma_f32_16x16x32_f16 v[96:99], v[128:131], v[186:189], v[96:99]
	v_mfma_f32_16x16x32_f16 v[88:91], v[136:139], v[186:189], v[88:91]
	v_mfma_f32_16x16x32_f16 v[80:83], v[128:131], v[194:197], v[80:83]
	v_mfma_f32_16x16x32_f16 v[72:75], v[136:139], v[194:197], v[72:75]
	v_mfma_f32_16x16x32_f16 v[124:127], v[132:135], v[162:165], v[124:127]
	v_mfma_f32_16x16x32_f16 v[120:123], v[140:143], v[162:165], v[120:123]
	v_mfma_f32_16x16x32_f16 v[108:111], v[132:135], v[182:185], v[108:111]
	v_mfma_f32_16x16x32_f16 v[104:107], v[140:143], v[182:185], v[104:107]
	v_mfma_f32_16x16x32_f16 v[96:99], v[132:135], v[190:193], v[96:99]
	v_mfma_f32_16x16x32_f16 v[88:91], v[140:143], v[190:193], v[88:91]
	v_mfma_f32_16x16x32_f16 v[80:83], v[132:135], v[198:201], v[80:83]
	v_mfma_f32_16x16x32_f16 v[72:75], v[140:143], v[198:201], v[72:75]
	s_barrier
	s_add_i32 s74, s65, s42
	v_lshl_add_u64 v[218:219], s[30:31], 0, v[146:147]
	s_mov_b32 m0, s74
	ds_read_b128 v[202:205], v174
	ds_read_b128 v[206:209], v174 offset:1024
	ds_read_b128 v[210:213], v174 offset:2048
	ds_read_b128 v[214:217], v174 offset:3072
	global_load_lds_dwordx4 v[218:219], off
	v_lshl_add_u64 v[220:221], s[30:31], 0, v[150:151]
	s_add_i32 m0, s74, 0x2000
	s_nop 0
	global_load_lds_dwordx4 v[220:221], off
	s_barrier
	s_waitcnt lgkmcnt(0)
	v_mfma_f32_16x16x32_f16 v[116:119], v[202:205], v[158:161], v[116:119]
	v_mfma_f32_16x16x32_f16 v[112:115], v[210:213], v[158:161], v[112:115]
	v_mfma_f32_16x16x32_f16 v[100:103], v[202:205], v[178:181], v[100:103]
	v_mfma_f32_16x16x32_f16 v[92:95], v[210:213], v[178:181], v[92:95]
	v_mfma_f32_16x16x32_f16 v[84:87], v[202:205], v[186:189], v[84:87]
	v_mfma_f32_16x16x32_f16 v[76:79], v[210:213], v[186:189], v[76:79]
	v_mfma_f32_16x16x32_f16 v[68:71], v[202:205], v[194:197], v[68:71]
	v_mfma_f32_16x16x32_f16 v[64:67], v[210:213], v[194:197], v[64:67]
	v_mfma_f32_16x16x32_f16 v[116:119], v[206:209], v[162:165], v[116:119]
	v_mfma_f32_16x16x32_f16 v[112:115], v[214:217], v[162:165], v[112:115]
	v_mfma_f32_16x16x32_f16 v[100:103], v[206:209], v[182:185], v[100:103]
	v_mfma_f32_16x16x32_f16 v[92:95], v[214:217], v[182:185], v[92:95]
	v_mfma_f32_16x16x32_f16 v[84:87], v[206:209], v[190:193], v[84:87]
	v_mfma_f32_16x16x32_f16 v[76:79], v[214:217], v[190:193], v[76:79]
	v_mfma_f32_16x16x32_f16 v[68:71], v[206:209], v[198:201], v[68:71]
	v_mfma_f32_16x16x32_f16 v[64:67], v[214:217], v[198:201], v[64:67]
	s_barrier
	s_mov_b32 m0, s43
	v_lshl_add_u64 v[222:223], s[34:35], 0, v[144:145]
	ds_read_b128 v[158:161], v173 offset:16384
	ds_read_b128 v[162:165], v173 offset:17408
	ds_read_b128 v[178:181], v173 offset:18432
	ds_read_b128 v[182:185], v173 offset:19456
	ds_read_b128 v[186:189], v173 offset:20480
	ds_read_b128 v[190:193], v173 offset:21504
	ds_read_b128 v[194:197], v173 offset:22528
	ds_read_b128 v[198:201], v173 offset:23552
	global_load_lds_dwordx4 v[222:223], off
	v_lshl_add_u64 v[224:225], s[34:35], 0, v[148:149]
	s_mov_b32 m0, s44
	s_nop 0
	global_load_lds_dwordx4 v[224:225], off
	s_barrier
	s_waitcnt lgkmcnt(0)
	v_mfma_f32_16x16x32_f16 v[60:63], v[128:131], v[158:161], v[60:63]
	v_mfma_f32_16x16x32_f16 v[56:59], v[136:139], v[158:161], v[56:59]
	v_mfma_f32_16x16x32_f16 v[48:51], v[128:131], v[178:181], v[48:51]
	v_mfma_f32_16x16x32_f16 v[40:43], v[136:139], v[178:181], v[40:43]
	v_mfma_f32_16x16x32_f16 v[32:35], v[128:131], v[186:189], v[32:35]
	v_mfma_f32_16x16x32_f16 v[24:27], v[136:139], v[186:189], v[24:27]
	v_mfma_f32_16x16x32_f16 v[16:19], v[128:131], v[194:197], v[16:19]
	v_mfma_f32_16x16x32_f16 v[8:11], v[136:139], v[194:197], v[8:11]
	v_mfma_f32_16x16x32_f16 v[60:63], v[132:135], v[162:165], v[60:63]
	v_mfma_f32_16x16x32_f16 v[56:59], v[140:143], v[162:165], v[56:59]
	v_mfma_f32_16x16x32_f16 v[48:51], v[132:135], v[182:185], v[48:51]
	v_mfma_f32_16x16x32_f16 v[40:43], v[140:143], v[182:185], v[40:43]
	v_mfma_f32_16x16x32_f16 v[32:35], v[132:135], v[190:193], v[32:35]
	v_mfma_f32_16x16x32_f16 v[24:27], v[140:143], v[190:193], v[24:27]
	v_mfma_f32_16x16x32_f16 v[16:19], v[132:135], v[198:201], v[16:19]
	v_mfma_f32_16x16x32_f16 v[8:11], v[140:143], v[198:201], v[8:11]
	s_barrier
	s_add_u32 s74, s30, 0xc000
	s_addc_u32 s75, s31, 0
	s_add_i32 s76, s66, s42
	v_lshl_add_u64 v[128:129], s[74:75], 0, v[146:147]
	s_mov_b32 m0, s76
	s_nop 0
	global_load_lds_dwordx4 v[128:129], off
	v_lshl_add_u64 v[128:129], s[74:75], 0, v[150:151]
	s_add_i32 m0, s76, 0x2000
	s_nop 0
	global_load_lds_dwordx4 v[128:129], off
	s_waitcnt vmcnt(6)
	s_barrier
	v_mfma_f32_16x16x32_f16 v[52:55], v[202:205], v[158:161], v[52:55]
	v_mfma_f32_16x16x32_f16 v[44:47], v[210:213], v[158:161], v[44:47]
	v_mfma_f32_16x16x32_f16 v[36:39], v[202:205], v[178:181], v[36:39]
	v_mfma_f32_16x16x32_f16 v[28:31], v[210:213], v[178:181], v[28:31]
	v_mfma_f32_16x16x32_f16 v[20:23], v[202:205], v[186:189], v[20:23]
	v_mfma_f32_16x16x32_f16 v[12:15], v[210:213], v[186:189], v[12:15]
	v_mfma_f32_16x16x32_f16 v[4:7], v[202:205], v[194:197], v[4:7]
	v_mfma_f32_16x16x32_f16 v[0:3], v[210:213], v[194:197], v[0:3]
	v_mfma_f32_16x16x32_f16 v[52:55], v[206:209], v[162:165], v[52:55]
	v_mfma_f32_16x16x32_f16 v[44:47], v[214:217], v[162:165], v[44:47]
	v_mfma_f32_16x16x32_f16 v[36:39], v[206:209], v[182:185], v[36:39]
	v_mfma_f32_16x16x32_f16 v[28:31], v[214:217], v[182:185], v[28:31]
	v_mfma_f32_16x16x32_f16 v[20:23], v[206:209], v[190:193], v[20:23]
	v_mfma_f32_16x16x32_f16 v[12:15], v[214:217], v[190:193], v[12:15]
	v_mfma_f32_16x16x32_f16 v[4:7], v[206:209], v[198:201], v[4:7]
	v_mfma_f32_16x16x32_f16 v[0:3], v[214:217], v[198:201], v[0:3]
	s_barrier
	s_add_i32 s74, 0, 0x18000
	v_add_u32_e32 v140, s74, v168
	ds_read_b128 v[128:131], v140
	ds_read_b128 v[132:135], v140 offset:1024
	ds_read_b128 v[136:139], v140 offset:2048
	ds_read_b128 v[140:143], v140 offset:3072
	s_add_u32 s34, s34, 0x30000
	s_addc_u32 s35, s35, 0
	s_mov_b32 m0, s45
	v_lshl_add_u64 v[202:203], s[34:35], 0, v[144:145]
	ds_read_b128 v[158:161], v173 offset:32768
	ds_read_b128 v[162:165], v173 offset:33792
	ds_read_b128 v[178:181], v173 offset:34816
	ds_read_b128 v[182:185], v173 offset:35840
	ds_read_b128 v[186:189], v173 offset:36864
	ds_read_b128 v[190:193], v173 offset:37888
	ds_read_b128 v[194:197], v173 offset:38912
	ds_read_b128 v[198:201], v173 offset:39936
	global_load_lds_dwordx4 v[202:203], off
	v_lshl_add_u64 v[202:203], s[34:35], 0, v[148:149]
	s_mov_b32 m0, s46
	s_nop 0
	global_load_lds_dwordx4 v[202:203], off
	s_waitcnt lgkmcnt(8)
	s_barrier
	s_waitcnt lgkmcnt(0)
	v_mfma_f32_16x16x32_f16 v[124:127], v[128:131], v[158:161], v[124:127]
	v_mfma_f32_16x16x32_f16 v[120:123], v[136:139], v[158:161], v[120:123]
	v_mfma_f32_16x16x32_f16 v[108:111], v[128:131], v[178:181], v[108:111]
	v_mfma_f32_16x16x32_f16 v[104:107], v[136:139], v[178:181], v[104:107]
	v_mfma_f32_16x16x32_f16 v[96:99], v[128:131], v[186:189], v[96:99]
	v_mfma_f32_16x16x32_f16 v[88:91], v[136:139], v[186:189], v[88:91]
	v_mfma_f32_16x16x32_f16 v[80:83], v[128:131], v[194:197], v[80:83]
	v_mfma_f32_16x16x32_f16 v[72:75], v[136:139], v[194:197], v[72:75]
	v_mfma_f32_16x16x32_f16 v[124:127], v[132:135], v[162:165], v[124:127]
	v_mfma_f32_16x16x32_f16 v[120:123], v[140:143], v[162:165], v[120:123]
	v_mfma_f32_16x16x32_f16 v[108:111], v[132:135], v[182:185], v[108:111]
	v_mfma_f32_16x16x32_f16 v[104:107], v[140:143], v[182:185], v[104:107]
	v_mfma_f32_16x16x32_f16 v[96:99], v[132:135], v[190:193], v[96:99]
	v_mfma_f32_16x16x32_f16 v[88:91], v[140:143], v[190:193], v[88:91]
	v_mfma_f32_16x16x32_f16 v[80:83], v[132:135], v[198:201], v[80:83]
	v_mfma_f32_16x16x32_f16 v[72:75], v[140:143], v[198:201], v[72:75]
	s_barrier
	s_add_i32 s34, 0, 0x1c000
	s_add_i32 s35, s74, s42
	v_add_u32_e32 v177, s34, v168
	v_lshl_add_u64 v[218:219], v[218:219], 0, s[26:27]
	s_mov_b32 m0, s35
	ds_read_b128 v[202:205], v177
	ds_read_b128 v[206:209], v177 offset:1024
	ds_read_b128 v[210:213], v177 offset:2048
	ds_read_b128 v[214:217], v177 offset:3072
	global_load_lds_dwordx4 v[218:219], off
	v_lshl_add_u64 v[218:219], v[220:221], 0, s[26:27]
	s_add_i32 m0, s35, 0x2000
	s_nop 0
	global_load_lds_dwordx4 v[218:219], off
	s_barrier
	s_waitcnt lgkmcnt(0)
	v_mfma_f32_16x16x32_f16 v[116:119], v[202:205], v[158:161], v[116:119]
	v_mfma_f32_16x16x32_f16 v[112:115], v[210:213], v[158:161], v[112:115]
	v_mfma_f32_16x16x32_f16 v[100:103], v[202:205], v[178:181], v[100:103]
	v_mfma_f32_16x16x32_f16 v[92:95], v[210:213], v[178:181], v[92:95]
	v_mfma_f32_16x16x32_f16 v[84:87], v[202:205], v[186:189], v[84:87]
	v_mfma_f32_16x16x32_f16 v[76:79], v[210:213], v[186:189], v[76:79]
	v_mfma_f32_16x16x32_f16 v[68:71], v[202:205], v[194:197], v[68:71]
	v_mfma_f32_16x16x32_f16 v[64:67], v[210:213], v[194:197], v[64:67]
	v_mfma_f32_16x16x32_f16 v[116:119], v[206:209], v[162:165], v[116:119]
	v_mfma_f32_16x16x32_f16 v[112:115], v[214:217], v[162:165], v[112:115]
	v_mfma_f32_16x16x32_f16 v[100:103], v[206:209], v[182:185], v[100:103]
	v_mfma_f32_16x16x32_f16 v[92:95], v[214:217], v[182:185], v[92:95]
	v_mfma_f32_16x16x32_f16 v[84:87], v[206:209], v[190:193], v[84:87]
	v_mfma_f32_16x16x32_f16 v[76:79], v[214:217], v[190:193], v[76:79]
	v_mfma_f32_16x16x32_f16 v[68:71], v[206:209], v[198:201], v[68:71]
	v_mfma_f32_16x16x32_f16 v[64:67], v[214:217], v[198:201], v[64:67]
	s_barrier
	s_mov_b32 m0, s49
	v_lshl_add_u64 v[218:219], v[222:223], 0, s[26:27]
	ds_read_b128 v[158:161], v173 offset:49152
	ds_read_b128 v[162:165], v173 offset:50176
	ds_read_b128 v[178:181], v173 offset:51200
	ds_read_b128 v[182:185], v173 offset:52224
	ds_read_b128 v[186:189], v173 offset:53248
	ds_read_b128 v[190:193], v173 offset:54272
	ds_read_b128 v[194:197], v173 offset:55296
	ds_read_b128 v[198:201], v173 offset:56320
	global_load_lds_dwordx4 v[218:219], off
	v_lshl_add_u64 v[218:219], v[224:225], 0, s[26:27]
	s_mov_b32 m0, s50
	s_nop 0
	global_load_lds_dwordx4 v[218:219], off
	s_barrier
	s_waitcnt lgkmcnt(0)
	v_mfma_f32_16x16x32_f16 v[60:63], v[128:131], v[158:161], v[60:63]
	v_mfma_f32_16x16x32_f16 v[56:59], v[136:139], v[158:161], v[56:59]
	v_mfma_f32_16x16x32_f16 v[48:51], v[128:131], v[178:181], v[48:51]
	v_mfma_f32_16x16x32_f16 v[40:43], v[136:139], v[178:181], v[40:43]
	v_mfma_f32_16x16x32_f16 v[32:35], v[128:131], v[186:189], v[32:35]
	v_mfma_f32_16x16x32_f16 v[24:27], v[136:139], v[186:189], v[24:27]
	v_mfma_f32_16x16x32_f16 v[16:19], v[128:131], v[194:197], v[16:19]
	v_mfma_f32_16x16x32_f16 v[8:11], v[136:139], v[194:197], v[8:11]
	v_mfma_f32_16x16x32_f16 v[60:63], v[132:135], v[162:165], v[60:63]
	v_mfma_f32_16x16x32_f16 v[56:59], v[140:143], v[162:165], v[56:59]
	v_mfma_f32_16x16x32_f16 v[48:51], v[132:135], v[182:185], v[48:51]
	v_mfma_f32_16x16x32_f16 v[40:43], v[140:143], v[182:185], v[40:43]
	v_mfma_f32_16x16x32_f16 v[32:35], v[132:135], v[190:193], v[32:35]
	v_mfma_f32_16x16x32_f16 v[24:27], v[140:143], v[190:193], v[24:27]
	v_mfma_f32_16x16x32_f16 v[16:19], v[132:135], v[198:201], v[16:19]
	v_mfma_f32_16x16x32_f16 v[8:11], v[140:143], v[198:201], v[8:11]
	s_barrier
	s_add_u32 s30, s30, 0xc080
	s_addc_u32 s31, s31, 0
	s_add_i32 s34, s34, s42
	v_lshl_add_u64 v[128:129], s[30:31], 0, v[146:147]
	s_mov_b32 m0, s34
	s_nop 0
	global_load_lds_dwordx4 v[128:129], off
	v_lshl_add_u64 v[128:129], s[30:31], 0, v[150:151]
	s_add_i32 m0, s34, 0x2000
	s_nop 0
	global_load_lds_dwordx4 v[128:129], off
	s_waitcnt vmcnt(6)
	s_barrier
	v_mfma_f32_16x16x32_f16 v[52:55], v[202:205], v[158:161], v[52:55]
	v_mfma_f32_16x16x32_f16 v[44:47], v[210:213], v[158:161], v[44:47]
	v_mfma_f32_16x16x32_f16 v[36:39], v[202:205], v[178:181], v[36:39]
	v_mfma_f32_16x16x32_f16 v[28:31], v[210:213], v[178:181], v[28:31]
	v_mfma_f32_16x16x32_f16 v[20:23], v[202:205], v[186:189], v[20:23]
	v_mfma_f32_16x16x32_f16 v[12:15], v[210:213], v[186:189], v[12:15]
	v_mfma_f32_16x16x32_f16 v[4:7], v[202:205], v[194:197], v[4:7]
	v_mfma_f32_16x16x32_f16 v[0:3], v[210:213], v[194:197], v[0:3]
	v_mfma_f32_16x16x32_f16 v[52:55], v[206:209], v[162:165], v[52:55]
	v_mfma_f32_16x16x32_f16 v[44:47], v[214:217], v[162:165], v[44:47]
	v_mfma_f32_16x16x32_f16 v[36:39], v[206:209], v[182:185], v[36:39]
	v_mfma_f32_16x16x32_f16 v[28:31], v[214:217], v[182:185], v[28:31]
	v_mfma_f32_16x16x32_f16 v[20:23], v[206:209], v[190:193], v[20:23]
	v_mfma_f32_16x16x32_f16 v[12:15], v[214:217], v[190:193], v[12:15]
	v_mfma_f32_16x16x32_f16 v[4:7], v[206:209], v[198:201], v[4:7]
	v_mfma_f32_16x16x32_f16 v[0:3], v[214:217], v[198:201], v[0:3]
	s_barrier
	s_add_i32 s73, s73, 2
	s_add_u32 s28, s28, 0x100
	s_addc_u32 s29, s29, 0
	s_add_u32 s71, s71, 0x100
	s_addc_u32 s72, s72, 0
	s_cmp_gt_u32 s73, 9
	s_cbranch_scc0 .LBB9_27
	s_lshl_b32 s28, s70, 8
	s_add_i32 s28, s28, s48
	s_lshl_b32 s29, s68, 8
	s_or_b32 s29, s29, s51
	s_waitcnt vmcnt(6)
	v_pk_fma_f32 v[126:127], v[126:127], v[226:227], v[236:237] op_sel_hi:[1,0,1]
	v_pk_fma_f32 v[124:125], v[124:125], v[226:227], v[234:235] op_sel_hi:[1,0,1]
	v_pk_fma_f32 v[122:123], v[122:123], v[226:227], v[240:241] op_sel_hi:[1,0,1]
	v_pk_fma_f32 v[120:121], v[120:121], v[226:227], v[238:239] op_sel_hi:[1,0,1]
	v_cvt_pk_f16_f32 v124, v124, v125
	v_cvt_pk_f16_f32 v125, v126, v127
	v_cvt_pk_f16_f32 v126, v120, v121
	v_cvt_pk_f16_f32 v123, v122, v123
	v_pk_fma_f32 v[118:119], v[118:119], v[226:227], v[244:245] op_sel_hi:[1,0,1]
	v_pk_fma_f32 v[116:117], v[116:117], v[226:227], v[242:243] op_sel_hi:[1,0,1]
	v_pk_fma_f32 v[114:115], v[114:115], v[226:227], v[248:249] op_sel_hi:[1,0,1]
	v_pk_fma_f32 v[112:113], v[112:113], v[226:227], v[246:247] op_sel_hi:[1,0,1]
	v_pk_max_f16 v120, v124, 0
	v_pk_max_f16 v121, v125, 0
	v_pk_max_f16 v122, v126, 0
	v_pk_max_f16 v123, v123, 0
	v_cvt_pk_f16_f32 v116, v116, v117
	v_cvt_pk_f16_f32 v117, v118, v119
	v_cvt_pk_f16_f32 v118, v112, v113
	v_cvt_pk_f16_f32 v115, v114, v115
	v_pk_fma_f32 v[110:111], v[110:111], v[226:227], v[236:237] op_sel:[0,1,0]
	v_pk_fma_f32 v[108:109], v[108:109], v[226:227], v[234:235] op_sel:[0,1,0]
	v_pk_fma_f32 v[106:107], v[106:107], v[226:227], v[240:241] op_sel:[0,1,0]
	v_pk_fma_f32 v[104:105], v[104:105], v[226:227], v[238:239] op_sel:[0,1,0]
	v_pk_fma_f32 v[102:103], v[102:103], v[226:227], v[244:245] op_sel:[0,1,0]
	v_pk_fma_f32 v[100:101], v[100:101], v[226:227], v[242:243] op_sel:[0,1,0]
	v_pk_fma_f32 v[94:95], v[94:95], v[226:227], v[248:249] op_sel:[0,1,0]
	v_pk_fma_f32 v[92:93], v[92:93], v[226:227], v[246:247] op_sel:[0,1,0]
	ds_write_b128 v175, v[120:123]
	v_or_b32_e32 v120, s28, v169
	v_pk_max_f16 v112, v116, 0
	v_pk_max_f16 v113, v117, 0
	v_pk_max_f16 v114, v118, 0
	v_pk_max_f16 v115, v115, 0
	v_cvt_pk_f16_f32 v108, v108, v109
	v_cvt_pk_f16_f32 v109, v110, v111
	v_cvt_pk_f16_f32 v110, v104, v105
	v_cvt_pk_f16_f32 v107, v106, v107
	v_cvt_pk_f16_f32 v100, v100, v101
	v_cvt_pk_f16_f32 v101, v102, v103
	v_cvt_pk_f16_f32 v102, v92, v93
	v_cvt_pk_f16_f32 v95, v94, v95
	ds_write_b128 v175, v[112:115] offset:64
	v_mul_lo_u32 v116, v120, s10
	v_pk_max_f16 v104, v108, 0
	v_pk_max_f16 v105, v109, 0
	v_pk_max_f16 v106, v110, 0
	v_pk_max_f16 v107, v107, 0
	v_pk_max_f16 v92, v100, 0
	v_pk_max_f16 v93, v101, 0
	v_pk_max_f16 v94, v102, 0
	v_pk_max_f16 v95, v95, 0
	ds_read_b128 v[112:115], v176
	v_add_u32_e32 v120, s29, v116
	ds_read_b128 v[116:119], v176 offset:1152
	ds_write_b128 v175, v[104:107]
	ds_write_b128 v175, v[92:95] offset:64
	ds_read_b128 v[92:95], v176
	ds_read_b128 v[100:103], v176 offset:1152
	v_lshlrev_b32_e32 v121, 1, v120
	v_add_u32_e32 v122, v121, v170
	v_add_u32_e32 v104, s55, v121
	s_waitcnt lgkmcnt(0)
	buffer_store_dwordx4 v[112:115], v122, s[20:23], 0 offen nt
	v_add_u32_e32 v105, v104, v170
	v_pk_fma_f32 v[90:91], v[90:91], v[228:229], v[240:241] op_sel_hi:[1,0,1]
	v_add_u32_e32 v112, v121, v171
	buffer_store_dwordx4 v[116:119], v112, s[20:23], 0 offen nt
	buffer_store_dwordx4 v[92:95], v105, s[20:23], 0 offen nt
	v_pk_fma_f32 v[88:89], v[88:89], v[228:229], v[238:239] op_sel_hi:[1,0,1]
	v_pk_fma_f32 v[86:87], v[86:87], v[228:229], v[244:245] op_sel_hi:[1,0,1]
	v_pk_fma_f32 v[92:93], v[98:99], v[228:229], v[236:237] op_sel_hi:[1,0,1]
	v_pk_fma_f32 v[94:95], v[96:97], v[228:229], v[234:235] op_sel_hi:[1,0,1]
	v_pk_fma_f32 v[84:85], v[84:85], v[228:229], v[242:243] op_sel_hi:[1,0,1]
	v_pk_fma_f32 v[78:79], v[78:79], v[228:229], v[248:249] op_sel_hi:[1,0,1]
	v_pk_fma_f32 v[76:77], v[76:77], v[228:229], v[246:247] op_sel_hi:[1,0,1]
	v_cvt_pk_f16_f32 v94, v94, v95
	v_cvt_pk_f16_f32 v92, v92, v93
	v_cvt_pk_f16_f32 v93, v88, v89
	v_cvt_pk_f16_f32 v91, v90, v91
	v_cvt_pk_f16_f32 v84, v84, v85
	v_cvt_pk_f16_f32 v85, v86, v87
	v_cvt_pk_f16_f32 v86, v76, v77
	v_cvt_pk_f16_f32 v79, v78, v79
	v_pk_max_f16 v88, v94, 0
	v_pk_max_f16 v89, v92, 0
	v_pk_max_f16 v90, v93, 0
	v_pk_max_f16 v91, v91, 0
	v_pk_max_f16 v76, v84, 0
	v_pk_max_f16 v77, v85, 0
	v_pk_max_f16 v78, v86, 0
	v_pk_max_f16 v79, v79, 0
	ds_write_b128 v175, v[88:91]
	ds_write_b128 v175, v[76:79] offset:64
	ds_read_b128 v[76:79], v176
	ds_read_b128 v[84:87], v176 offset:1152
	v_add_u32_e32 v88, s55, v104
	v_add_u32_e32 v105, v104, v171
	v_add_u32_e32 v89, v88, v170
	buffer_store_dwordx4 v[100:103], v105, s[20:23], 0 offen nt
	s_waitcnt lgkmcnt(1)
	buffer_store_dwordx4 v[76:79], v89, s[20:23], 0 offen nt
	v_pk_fma_f32 v[74:75], v[74:75], v[228:229], v[240:241] op_sel:[0,1,0]
	v_pk_fma_f32 v[72:73], v[72:73], v[228:229], v[238:239] op_sel:[0,1,0]
	v_add_u32_e32 v76, v88, v171
	s_waitcnt lgkmcnt(0)
	buffer_store_dwordx4 v[84:87], v76, s[20:23], 0 offen nt
	v_pk_fma_f32 v[76:77], v[82:83], v[228:229], v[236:237] op_sel:[0,1,0]
	v_pk_fma_f32 v[78:79], v[80:81], v[228:229], v[234:235] op_sel:[0,1,0]
	v_pk_fma_f32 v[70:71], v[70:71], v[228:229], v[244:245] op_sel:[0,1,0]
	v_pk_fma_f32 v[68:69], v[68:69], v[228:229], v[242:243] op_sel:[0,1,0]
	v_pk_fma_f32 v[66:67], v[66:67], v[228:229], v[248:249] op_sel:[0,1,0]
	v_pk_fma_f32 v[64:65], v[64:65], v[228:229], v[246:247] op_sel:[0,1,0]
	v_cvt_pk_f16_f32 v78, v78, v79
	v_cvt_pk_f16_f32 v76, v76, v77
	v_cvt_pk_f16_f32 v77, v72, v73
	v_cvt_pk_f16_f32 v75, v74, v75
	v_cvt_pk_f16_f32 v68, v68, v69
	v_cvt_pk_f16_f32 v69, v70, v71
	v_cvt_pk_f16_f32 v70, v64, v65
	v_cvt_pk_f16_f32 v67, v66, v67
	v_pk_fma_f32 v[62:63], v[62:63], v[230:231], v[236:237] op_sel_hi:[1,0,1]
	v_pk_fma_f32 v[60:61], v[60:61], v[230:231], v[234:235] op_sel_hi:[1,0,1]
	v_pk_fma_f32 v[58:59], v[58:59], v[230:231], v[240:241] op_sel_hi:[1,0,1]
	v_pk_fma_f32 v[56:57], v[56:57], v[230:231], v[238:239] op_sel_hi:[1,0,1]
	v_pk_fma_f32 v[54:55], v[54:55], v[230:231], v[244:245] op_sel_hi:[1,0,1]
	v_pk_fma_f32 v[52:53], v[52:53], v[230:231], v[242:243] op_sel_hi:[1,0,1]
	v_pk_fma_f32 v[46:47], v[46:47], v[230:231], v[248:249] op_sel_hi:[1,0,1]
	v_pk_fma_f32 v[44:45], v[44:45], v[230:231], v[246:247] op_sel_hi:[1,0,1]
	v_pk_max_f16 v72, v78, 0
	v_pk_max_f16 v73, v76, 0
	v_pk_max_f16 v74, v77, 0
	v_pk_max_f16 v75, v75, 0
	v_pk_max_f16 v64, v68, 0
	v_pk_max_f16 v65, v69, 0
	v_pk_max_f16 v66, v70, 0
	v_pk_max_f16 v67, v67, 0
	v_cvt_pk_f16_f32 v60, v60, v61
	v_cvt_pk_f16_f32 v61, v62, v63
	v_cvt_pk_f16_f32 v62, v56, v57
	v_cvt_pk_f16_f32 v59, v58, v59
	v_cvt_pk_f16_f32 v52, v52, v53
	v_cvt_pk_f16_f32 v53, v54, v55
	v_cvt_pk_f16_f32 v54, v44, v45
	v_cvt_pk_f16_f32 v47, v46, v47
	ds_write_b128 v175, v[72:75]
	ds_write_b128 v175, v[64:67] offset:64
	v_pk_max_f16 v56, v60, 0
	v_pk_max_f16 v57, v61, 0
	v_pk_max_f16 v58, v62, 0
	v_pk_max_f16 v59, v59, 0
	v_pk_max_f16 v44, v52, 0
	v_pk_max_f16 v45, v53, 0
	v_pk_max_f16 v46, v54, 0
	v_pk_max_f16 v47, v47, 0
	ds_read_b128 v[64:67], v176
	ds_read_b128 v[68:71], v176 offset:1152
	ds_write_b128 v175, v[56:59]
	ds_write_b128 v175, v[44:47] offset:64
	ds_read_b128 v[44:47], v176
	ds_read_b128 v[52:55], v176 offset:1152
	v_add_u32_e32 v72, s56, v120
	v_lshlrev_b32_e32 v73, 1, v72
	v_add_u32_e32 v74, v73, v170
	v_add_u32_e32 v56, s62, v88
	s_waitcnt lgkmcnt(5)
	buffer_store_dwordx4 v[64:67], v74, s[20:23], 0 offen nt
	v_add_u32_e32 v57, v56, v170
	v_pk_fma_f32 v[42:43], v[42:43], v[230:231], v[240:241] op_sel:[0,1,0]
	v_add_u32_e32 v64, v73, v171
	s_waitcnt lgkmcnt(4)
	buffer_store_dwordx4 v[68:71], v64, s[20:23], 0 offen nt
	s_waitcnt lgkmcnt(1)
	buffer_store_dwordx4 v[44:47], v57, s[20:23], 0 offen nt
	v_pk_fma_f32 v[40:41], v[40:41], v[230:231], v[238:239] op_sel:[0,1,0]
	v_pk_fma_f32 v[38:39], v[38:39], v[230:231], v[244:245] op_sel:[0,1,0]
	v_add_u32_e32 v44, v56, v171
	s_waitcnt lgkmcnt(0)
	buffer_store_dwordx4 v[52:55], v44, s[20:23], 0 offen nt
	v_pk_fma_f32 v[44:45], v[50:51], v[230:231], v[236:237] op_sel:[0,1,0]
	v_pk_fma_f32 v[46:47], v[48:49], v[230:231], v[234:235] op_sel:[0,1,0]
	v_pk_fma_f32 v[36:37], v[36:37], v[230:231], v[242:243] op_sel:[0,1,0]
	v_pk_fma_f32 v[30:31], v[30:31], v[230:231], v[248:249] op_sel:[0,1,0]
	v_pk_fma_f32 v[28:29], v[28:29], v[230:231], v[246:247] op_sel:[0,1,0]
	v_cvt_pk_f16_f32 v46, v46, v47
	v_cvt_pk_f16_f32 v44, v44, v45
	v_cvt_pk_f16_f32 v45, v40, v41
	v_cvt_pk_f16_f32 v43, v42, v43
	v_cvt_pk_f16_f32 v36, v36, v37
	v_cvt_pk_f16_f32 v37, v38, v39
	v_cvt_pk_f16_f32 v38, v28, v29
	v_cvt_pk_f16_f32 v31, v30, v31
	v_pk_max_f16 v40, v46, 0
	v_pk_max_f16 v41, v44, 0
	v_pk_max_f16 v42, v45, 0
	v_pk_max_f16 v43, v43, 0
	v_pk_max_f16 v28, v36, 0
	v_pk_max_f16 v29, v37, 0
	v_pk_max_f16 v30, v38, 0
	v_pk_max_f16 v31, v31, 0
	ds_write_b128 v175, v[40:43]
	ds_write_b128 v175, v[28:31] offset:64
	ds_read_b128 v[28:31], v176
	ds_read_b128 v[36:39], v176 offset:1152
	v_add_u32_e32 v40, s63, v72
	v_lshlrev_b32_e32 v41, 1, v40
	v_add_u32_e32 v42, v41, v170
	s_waitcnt lgkmcnt(1)
	buffer_store_dwordx4 v[28:31], v42, s[20:23], 0 offen nt
	v_pk_fma_f32 v[26:27], v[26:27], v[232:233], v[240:241] op_sel_hi:[1,0,1]
	v_pk_fma_f32 v[24:25], v[24:25], v[232:233], v[238:239] op_sel_hi:[1,0,1]
	v_add_u32_e32 v28, v41, v171
	s_waitcnt lgkmcnt(0)
	buffer_store_dwordx4 v[36:39], v28, s[20:23], 0 offen nt
	v_pk_fma_f32 v[28:29], v[34:35], v[232:233], v[236:237] op_sel_hi:[1,0,1]
	v_pk_fma_f32 v[30:31], v[32:33], v[232:233], v[234:235] op_sel_hi:[1,0,1]
	v_pk_fma_f32 v[22:23], v[22:23], v[232:233], v[244:245] op_sel_hi:[1,0,1]
	v_pk_fma_f32 v[20:21], v[20:21], v[232:233], v[242:243] op_sel_hi:[1,0,1]
	v_pk_fma_f32 v[14:15], v[14:15], v[232:233], v[248:249] op_sel_hi:[1,0,1]
	v_pk_fma_f32 v[12:13], v[12:13], v[232:233], v[246:247] op_sel_hi:[1,0,1]
	v_cvt_pk_f16_f32 v30, v30, v31
	v_cvt_pk_f16_f32 v28, v28, v29
	v_cvt_pk_f16_f32 v29, v24, v25
	v_cvt_pk_f16_f32 v27, v26, v27
	v_cvt_pk_f16_f32 v20, v20, v21
	v_cvt_pk_f16_f32 v21, v22, v23
	v_cvt_pk_f16_f32 v22, v12, v13
	v_cvt_pk_f16_f32 v15, v14, v15
	v_pk_max_f16 v24, v30, 0
	v_pk_max_f16 v25, v28, 0
	v_pk_max_f16 v26, v29, 0
	v_pk_max_f16 v27, v27, 0
	v_pk_max_f16 v12, v20, 0
	v_pk_max_f16 v13, v21, 0
	v_pk_max_f16 v14, v22, 0
	v_pk_max_f16 v15, v15, 0
	ds_write_b128 v175, v[24:27]
	ds_write_b128 v175, v[12:15] offset:64
	ds_read_b128 v[12:15], v176
	ds_read_b128 v[20:23], v176 offset:1152
	v_add_u32_e32 v24, s64, v40
	v_lshlrev_b32_e32 v25, 1, v24
	v_add_u32_e32 v26, v25, v170
	s_waitcnt lgkmcnt(1)
	buffer_store_dwordx4 v[12:15], v26, s[20:23], 0 offen nt
	v_pk_fma_f32 v[10:11], v[10:11], v[232:233], v[240:241] op_sel:[0,1,0]
	v_pk_fma_f32 v[8:9], v[8:9], v[232:233], v[238:239] op_sel:[0,1,0]
	v_pk_fma_f32 v[12:13], v[18:19], v[232:233], v[236:237] op_sel:[0,1,0]
	v_pk_fma_f32 v[14:15], v[16:17], v[232:233], v[234:235] op_sel:[0,1,0]
	v_pk_fma_f32 v[6:7], v[6:7], v[232:233], v[244:245] op_sel:[0,1,0]
	v_pk_fma_f32 v[4:5], v[4:5], v[232:233], v[242:243] op_sel:[0,1,0]
	v_pk_fma_f32 v[2:3], v[2:3], v[232:233], v[248:249] op_sel:[0,1,0]
	v_pk_fma_f32 v[0:1], v[0:1], v[232:233], v[246:247] op_sel:[0,1,0]
	v_cvt_pk_f16_f32 v14, v14, v15
	v_cvt_pk_f16_f32 v12, v12, v13
	v_cvt_pk_f16_f32 v13, v8, v9
	v_cvt_pk_f16_f32 v11, v10, v11
	v_cvt_pk_f16_f32 v4, v4, v5
	v_cvt_pk_f16_f32 v5, v6, v7
	v_cvt_pk_f16_f32 v6, v0, v1
	v_cvt_pk_f16_f32 v3, v2, v3
	v_pk_max_f16 v8, v14, 0
	v_pk_max_f16 v9, v12, 0
	v_pk_max_f16 v10, v13, 0
	v_pk_max_f16 v11, v11, 0
	v_pk_max_f16 v0, v4, 0
	v_pk_max_f16 v1, v5, 0
	v_pk_max_f16 v2, v6, 0
	v_pk_max_f16 v3, v3, 0
	ds_write_b128 v175, v[8:11]
	ds_write_b128 v175, v[0:3] offset:64
	ds_read_b128 v[0:3], v176
	ds_read_b128 v[4:7], v176 offset:1152
	v_add_lshl_u32 v8, v24, s64, 1
	v_add_u32_e32 v25, v25, v171
	v_add_u32_e32 v9, v8, v170
	s_waitcnt lgkmcnt(4)
	buffer_store_dwordx4 v[20:23], v25, s[20:23], 0 offen nt
	s_waitcnt lgkmcnt(1)
	buffer_store_dwordx4 v[0:3], v9, s[20:23], 0 offen nt
	s_mov_b32 s68, s67
	s_mov_b32 s70, s69
	v_add_u32_e32 v0, v8, v171
	s_mov_b64 s[30:31], s[0:1]
	s_mov_b64 s[28:29], s[8:9]
	s_mov_b64 vcc, s[6:7]
	s_waitcnt lgkmcnt(0)
	buffer_store_dwordx4 v[4:7], v0, s[20:23], 0 offen nt
	s_cbranch_vccz .LBB9_12
	s_waitcnt vmcnt(0)
	s_cmpk_gt_u32 s36, 0xff
	s_cbranch_scc1 .LBB9_31
	s_barrier

.LBB9_32:
	s_endpgm
	s_endpgm
	s_endpgm
	s_endpgm
	s_endpgm
	s_endpgm
	s_endpgm
	s_endpgm
	s_endpgm
	s_endpgm
	s_endpgm
	s_endpgm
	s_endpgm
	.section	.rodata,"a",@progbits
	.p2align	6, 0x0

.LBB10_27:
	ds_read_b128 v[72:75], v231
	ds_read_b128 v[80:83], v231 offset:1024
	ds_read_b128 v[88:91], v231 offset:2048
	ds_read_b128 v[92:95], v231 offset:3072
	s_add_u32 s40, s38, 0xfff40080
	s_addc_u32 s41, s39, -1
	s_cmp_eq_u32 s87, 44
	s_cselect_b32 s43, s9, s41
	s_cselect_b32 s42, s8, s40
	s_cselect_b32 s41, s1, s86
	s_cselect_b32 s40, s0, s85
	v_lshl_add_u64 v[190:191], s[38:39], 0, v[184:185]
	s_add_i32 m0, s51, 0xc000
	ds_read_b128 v[136:139], v232
	ds_read_b128 v[148:151], v232 offset:1024
	ds_read_b128 v[152:155], v232 offset:2048
	ds_read_b128 v[156:159], v232 offset:3072
	ds_read_b128 v[160:163], v232 offset:4096
	ds_read_b128 v[164:167], v232 offset:5120
	ds_read_b128 v[168:171], v232 offset:6144
	ds_read_b128 v[172:175], v232 offset:7168
	global_load_lds_dwordx4 v[190:191], off
	v_lshl_add_u64 v[190:191], s[38:39], 0, v[186:187]
	s_add_i32 m0, s51, 0xe000
	s_nop 0
	global_load_lds_dwordx4 v[190:191], off
	s_waitcnt lgkmcnt(8)
	s_barrier
	s_waitcnt lgkmcnt(0)
	v_mfma_f32_16x16x32_f16 v[144:147], v[72:75], v[136:139], v[144:147]
	v_mfma_f32_16x16x32_f16 v[140:143], v[88:91], v[136:139], v[140:143]
	v_mfma_f32_16x16x32_f16 v[124:127], v[72:75], v[152:155], v[124:127]
	v_mfma_f32_16x16x32_f16 v[120:123], v[88:91], v[152:155], v[120:123]
	v_mfma_f32_16x16x32_f16 v[108:111], v[72:75], v[160:163], v[108:111]
	v_mfma_f32_16x16x32_f16 v[104:107], v[88:91], v[160:163], v[104:107]
	v_mfma_f32_16x16x32_f16 v[84:87], v[72:75], v[168:171], v[84:87]
	v_mfma_f32_16x16x32_f16 v[76:79], v[88:91], v[168:171], v[76:79]
	v_mfma_f32_16x16x32_f16 v[144:147], v[80:83], v[148:151], v[144:147]
	v_mfma_f32_16x16x32_f16 v[140:143], v[92:95], v[148:151], v[140:143]
	v_mfma_f32_16x16x32_f16 v[124:127], v[80:83], v[156:159], v[124:127]
	v_mfma_f32_16x16x32_f16 v[120:123], v[92:95], v[156:159], v[120:123]
	v_mfma_f32_16x16x32_f16 v[108:111], v[80:83], v[164:167], v[108:111]
	v_mfma_f32_16x16x32_f16 v[104:107], v[92:95], v[164:167], v[104:107]
	v_mfma_f32_16x16x32_f16 v[84:87], v[80:83], v[172:175], v[84:87]
	v_mfma_f32_16x16x32_f16 v[76:79], v[92:95], v[172:175], v[76:79]
	s_barrier
	s_add_i32 s88, s69, s50
	v_lshl_add_u64 v[206:207], s[40:41], 0, v[178:179]
	s_mov_b32 m0, s88
	ds_read_b128 v[190:193], v233
	ds_read_b128 v[194:197], v233 offset:1024
	ds_read_b128 v[198:201], v233 offset:2048
	ds_read_b128 v[202:205], v233 offset:3072
	global_load_lds_dwordx4 v[206:207], off
	v_lshl_add_u64 v[208:209], s[40:41], 0, v[182:183]
	s_add_i32 m0, s88, 0x2000
	s_nop 0
	global_load_lds_dwordx4 v[208:209], off
	s_barrier
	s_waitcnt lgkmcnt(0)
	v_mfma_f32_16x16x32_f16 v[132:135], v[190:193], v[136:139], v[132:135]
	v_mfma_f32_16x16x32_f16 v[128:131], v[198:201], v[136:139], v[128:131]
	v_mfma_f32_16x16x32_f16 v[116:119], v[190:193], v[152:155], v[116:119]
	v_mfma_f32_16x16x32_f16 v[112:115], v[198:201], v[152:155], v[112:115]
	v_mfma_f32_16x16x32_f16 v[100:103], v[190:193], v[160:163], v[100:103]
	v_mfma_f32_16x16x32_f16 v[96:99], v[198:201], v[160:163], v[96:99]
	v_mfma_f32_16x16x32_f16 v[68:71], v[190:193], v[168:171], v[68:71]
	v_mfma_f32_16x16x32_f16 v[64:67], v[198:201], v[168:171], v[64:67]
	v_mfma_f32_16x16x32_f16 v[132:135], v[194:197], v[148:151], v[132:135]
	v_mfma_f32_16x16x32_f16 v[128:131], v[202:205], v[148:151], v[128:131]
	v_mfma_f32_16x16x32_f16 v[116:119], v[194:197], v[156:159], v[116:119]
	v_mfma_f32_16x16x32_f16 v[112:115], v[202:205], v[156:159], v[112:115]
	v_mfma_f32_16x16x32_f16 v[100:103], v[194:197], v[164:167], v[100:103]
	v_mfma_f32_16x16x32_f16 v[96:99], v[202:205], v[164:167], v[96:99]
	v_mfma_f32_16x16x32_f16 v[68:71], v[194:197], v[172:175], v[68:71]
	v_mfma_f32_16x16x32_f16 v[64:67], v[202:205], v[172:175], v[64:67]
	s_barrier
	s_mov_b32 m0, s51
	v_lshl_add_u64 v[210:211], s[42:43], 0, v[176:177]
	ds_read_b128 v[136:139], v232 offset:16384
	ds_read_b128 v[148:151], v232 offset:17408
	ds_read_b128 v[152:155], v232 offset:18432
	ds_read_b128 v[156:159], v232 offset:19456
	ds_read_b128 v[160:163], v232 offset:20480
	ds_read_b128 v[164:167], v232 offset:21504
	ds_read_b128 v[168:171], v232 offset:22528
	ds_read_b128 v[172:175], v232 offset:23552
	global_load_lds_dwordx4 v[210:211], off
	v_lshl_add_u64 v[212:213], s[42:43], 0, v[180:181]
	s_mov_b32 m0, s52
	s_nop 0
	global_load_lds_dwordx4 v[212:213], off
	s_barrier
	s_waitcnt lgkmcnt(0)
	v_mfma_f32_16x16x32_f16 v[60:63], v[72:75], v[136:139], v[60:63]
	v_mfma_f32_16x16x32_f16 v[56:59], v[88:91], v[136:139], v[56:59]
	v_mfma_f32_16x16x32_f16 v[44:47], v[72:75], v[152:155], v[44:47]
	v_mfma_f32_16x16x32_f16 v[40:43], v[88:91], v[152:155], v[40:43]
	v_mfma_f32_16x16x32_f16 v[28:31], v[72:75], v[160:163], v[28:31]
	v_mfma_f32_16x16x32_f16 v[24:27], v[88:91], v[160:163], v[24:27]
	v_mfma_f32_16x16x32_f16 v[12:15], v[72:75], v[168:171], v[12:15]
	v_mfma_f32_16x16x32_f16 v[8:11], v[88:91], v[168:171], v[8:11]
	v_mfma_f32_16x16x32_f16 v[60:63], v[80:83], v[148:151], v[60:63]
	v_mfma_f32_16x16x32_f16 v[56:59], v[92:95], v[148:151], v[56:59]
	v_mfma_f32_16x16x32_f16 v[44:47], v[80:83], v[156:159], v[44:47]
	v_mfma_f32_16x16x32_f16 v[40:43], v[92:95], v[156:159], v[40:43]
	v_mfma_f32_16x16x32_f16 v[28:31], v[80:83], v[164:167], v[28:31]
	v_mfma_f32_16x16x32_f16 v[24:27], v[92:95], v[164:167], v[24:27]
	v_mfma_f32_16x16x32_f16 v[12:15], v[80:83], v[172:175], v[12:15]
	v_mfma_f32_16x16x32_f16 v[8:11], v[92:95], v[172:175], v[8:11]
	s_barrier
	s_add_u32 s88, s40, 0x30000
	s_addc_u32 s89, s41, 0
	s_add_i32 s90, s70, s50
	v_lshl_add_u64 v[72:73], s[88:89], 0, v[178:179]
	s_mov_b32 m0, s90
	s_nop 0
	global_load_lds_dwordx4 v[72:73], off
	v_lshl_add_u64 v[72:73], s[88:89], 0, v[182:183]
	s_add_i32 m0, s90, 0x2000
	s_nop 0
	global_load_lds_dwordx4 v[72:73], off
	s_waitcnt vmcnt(6)
	s_barrier
	v_mfma_f32_16x16x32_f16 v[52:55], v[190:193], v[136:139], v[52:55]
	v_mfma_f32_16x16x32_f16 v[48:51], v[198:201], v[136:139], v[48:51]
	v_mfma_f32_16x16x32_f16 v[36:39], v[190:193], v[152:155], v[36:39]
	v_mfma_f32_16x16x32_f16 v[32:35], v[198:201], v[152:155], v[32:35]
	v_mfma_f32_16x16x32_f16 v[20:23], v[190:193], v[160:163], v[20:23]
	v_mfma_f32_16x16x32_f16 v[16:19], v[198:201], v[160:163], v[16:19]
	v_mfma_f32_16x16x32_f16 v[4:7], v[190:193], v[168:171], v[4:7]
	v_mfma_f32_16x16x32_f16 v[0:3], v[198:201], v[168:171], v[0:3]
	v_mfma_f32_16x16x32_f16 v[52:55], v[194:197], v[148:151], v[52:55]
	v_mfma_f32_16x16x32_f16 v[48:51], v[202:205], v[148:151], v[48:51]
	v_mfma_f32_16x16x32_f16 v[36:39], v[194:197], v[156:159], v[36:39]
	v_mfma_f32_16x16x32_f16 v[32:35], v[202:205], v[156:159], v[32:35]
	v_mfma_f32_16x16x32_f16 v[20:23], v[194:197], v[164:167], v[20:23]
	v_mfma_f32_16x16x32_f16 v[16:19], v[202:205], v[164:167], v[16:19]
	v_mfma_f32_16x16x32_f16 v[4:7], v[194:197], v[172:175], v[4:7]
	v_mfma_f32_16x16x32_f16 v[0:3], v[202:205], v[172:175], v[0:3]
	s_barrier
	s_add_i32 s88, 0, 0x18000
	v_add_u32_e32 v92, s88, v228
	ds_read_b128 v[72:75], v92
	ds_read_b128 v[80:83], v92 offset:1024
	ds_read_b128 v[88:91], v92 offset:2048
	ds_read_b128 v[92:95], v92 offset:3072
	s_add_u32 s42, s42, 0xc0000
	s_addc_u32 s43, s43, 0
	s_mov_b32 m0, s53
	v_lshl_add_u64 v[190:191], s[42:43], 0, v[176:177]
	ds_read_b128 v[136:139], v232 offset:32768
	ds_read_b128 v[148:151], v232 offset:33792
	ds_read_b128 v[152:155], v232 offset:34816
	ds_read_b128 v[156:159], v232 offset:35840
	ds_read_b128 v[160:163], v232 offset:36864
	ds_read_b128 v[164:167], v232 offset:37888
	ds_read_b128 v[168:171], v232 offset:38912
	ds_read_b128 v[172:175], v232 offset:39936
	global_load_lds_dwordx4 v[190:191], off
	v_lshl_add_u64 v[190:191], s[42:43], 0, v[180:181]
	s_mov_b32 m0, s54
	s_nop 0
	global_load_lds_dwordx4 v[190:191], off
	s_waitcnt lgkmcnt(8)
	s_barrier
	s_waitcnt lgkmcnt(0)
	v_mfma_f32_16x16x32_f16 v[144:147], v[72:75], v[136:139], v[144:147]
	v_mfma_f32_16x16x32_f16 v[140:143], v[88:91], v[136:139], v[140:143]
	v_mfma_f32_16x16x32_f16 v[124:127], v[72:75], v[152:155], v[124:127]
	v_mfma_f32_16x16x32_f16 v[120:123], v[88:91], v[152:155], v[120:123]
	v_mfma_f32_16x16x32_f16 v[108:111], v[72:75], v[160:163], v[108:111]
	v_mfma_f32_16x16x32_f16 v[104:107], v[88:91], v[160:163], v[104:107]
	v_mfma_f32_16x16x32_f16 v[84:87], v[72:75], v[168:171], v[84:87]
	v_mfma_f32_16x16x32_f16 v[76:79], v[88:91], v[168:171], v[76:79]
	v_mfma_f32_16x16x32_f16 v[144:147], v[80:83], v[148:151], v[144:147]
	v_mfma_f32_16x16x32_f16 v[140:143], v[92:95], v[148:151], v[140:143]
	v_mfma_f32_16x16x32_f16 v[124:127], v[80:83], v[156:159], v[124:127]
	v_mfma_f32_16x16x32_f16 v[120:123], v[92:95], v[156:159], v[120:123]
	v_mfma_f32_16x16x32_f16 v[108:111], v[80:83], v[164:167], v[108:111]
	v_mfma_f32_16x16x32_f16 v[104:107], v[92:95], v[164:167], v[104:107]
	v_mfma_f32_16x16x32_f16 v[84:87], v[80:83], v[172:175], v[84:87]
	v_mfma_f32_16x16x32_f16 v[76:79], v[92:95], v[172:175], v[76:79]
	s_barrier
	s_add_i32 s42, 0, 0x1c000
	s_add_i32 s43, s88, s50
	v_add_u32_e32 v202, s42, v228
	v_lshl_add_u64 v[206:207], v[206:207], 0, s[36:37]
	s_mov_b32 m0, s43
	ds_read_b128 v[190:193], v202
	ds_read_b128 v[194:197], v202 offset:1024
	ds_read_b128 v[198:201], v202 offset:2048
	ds_read_b128 v[202:205], v202 offset:3072
	global_load_lds_dwordx4 v[206:207], off
	v_lshl_add_u64 v[206:207], v[208:209], 0, s[36:37]
	s_add_i32 m0, s43, 0x2000
	s_nop 0
	global_load_lds_dwordx4 v[206:207], off
	s_barrier
	s_waitcnt lgkmcnt(0)
	v_mfma_f32_16x16x32_f16 v[132:135], v[190:193], v[136:139], v[132:135]
	v_mfma_f32_16x16x32_f16 v[128:131], v[198:201], v[136:139], v[128:131]
	v_mfma_f32_16x16x32_f16 v[116:119], v[190:193], v[152:155], v[116:119]
	v_mfma_f32_16x16x32_f16 v[112:115], v[198:201], v[152:155], v[112:115]
	v_mfma_f32_16x16x32_f16 v[100:103], v[190:193], v[160:163], v[100:103]
	v_mfma_f32_16x16x32_f16 v[96:99], v[198:201], v[160:163], v[96:99]
	v_mfma_f32_16x16x32_f16 v[68:71], v[190:193], v[168:171], v[68:71]
	v_mfma_f32_16x16x32_f16 v[64:67], v[198:201], v[168:171], v[64:67]
	v_mfma_f32_16x16x32_f16 v[132:135], v[194:197], v[148:151], v[132:135]
	v_mfma_f32_16x16x32_f16 v[128:131], v[202:205], v[148:151], v[128:131]
	v_mfma_f32_16x16x32_f16 v[116:119], v[194:197], v[156:159], v[116:119]
	v_mfma_f32_16x16x32_f16 v[112:115], v[202:205], v[156:159], v[112:115]
	v_mfma_f32_16x16x32_f16 v[100:103], v[194:197], v[164:167], v[100:103]
	v_mfma_f32_16x16x32_f16 v[96:99], v[202:205], v[164:167], v[96:99]
	v_mfma_f32_16x16x32_f16 v[68:71], v[194:197], v[172:175], v[68:71]
	v_mfma_f32_16x16x32_f16 v[64:67], v[202:205], v[172:175], v[64:67]
	s_barrier
	s_mov_b32 m0, s58
	v_lshl_add_u64 v[206:207], v[210:211], 0, s[36:37]
	ds_read_b128 v[136:139], v232 offset:49152
	ds_read_b128 v[148:151], v232 offset:50176
	ds_read_b128 v[152:155], v232 offset:51200
	ds_read_b128 v[156:159], v232 offset:52224
	ds_read_b128 v[160:163], v232 offset:53248
	ds_read_b128 v[164:167], v232 offset:54272
	ds_read_b128 v[168:171], v232 offset:55296
	ds_read_b128 v[172:175], v232 offset:56320
	global_load_lds_dwordx4 v[206:207], off
	v_lshl_add_u64 v[206:207], v[212:213], 0, s[36:37]
	s_mov_b32 m0, s59
	s_nop 0
	global_load_lds_dwordx4 v[206:207], off
	s_barrier
	s_waitcnt lgkmcnt(0)
	v_mfma_f32_16x16x32_f16 v[60:63], v[72:75], v[136:139], v[60:63]
	v_mfma_f32_16x16x32_f16 v[56:59], v[88:91], v[136:139], v[56:59]
	v_mfma_f32_16x16x32_f16 v[44:47], v[72:75], v[152:155], v[44:47]
	v_mfma_f32_16x16x32_f16 v[40:43], v[88:91], v[152:155], v[40:43]
	v_mfma_f32_16x16x32_f16 v[28:31], v[72:75], v[160:163], v[28:31]
	v_mfma_f32_16x16x32_f16 v[24:27], v[88:91], v[160:163], v[24:27]
	v_mfma_f32_16x16x32_f16 v[12:15], v[72:75], v[168:171], v[12:15]
	v_mfma_f32_16x16x32_f16 v[8:11], v[88:91], v[168:171], v[8:11]
	v_mfma_f32_16x16x32_f16 v[60:63], v[80:83], v[148:151], v[60:63]
	v_mfma_f32_16x16x32_f16 v[56:59], v[92:95], v[148:151], v[56:59]
	v_mfma_f32_16x16x32_f16 v[44:47], v[80:83], v[156:159], v[44:47]
	v_mfma_f32_16x16x32_f16 v[40:43], v[92:95], v[156:159], v[40:43]
	v_mfma_f32_16x16x32_f16 v[28:31], v[80:83], v[164:167], v[28:31]
	v_mfma_f32_16x16x32_f16 v[24:27], v[92:95], v[164:167], v[24:27]
	v_mfma_f32_16x16x32_f16 v[12:15], v[80:83], v[172:175], v[12:15]
	v_mfma_f32_16x16x32_f16 v[8:11], v[92:95], v[172:175], v[8:11]
	s_barrier
	s_add_u32 s40, s40, 0x30080
	s_addc_u32 s41, s41, 0
	s_add_i32 s42, s42, s50
	v_lshl_add_u64 v[72:73], s[40:41], 0, v[178:179]
	s_mov_b32 m0, s42
	s_nop 0
	global_load_lds_dwordx4 v[72:73], off
	v_lshl_add_u64 v[72:73], s[40:41], 0, v[182:183]
	s_add_i32 m0, s42, 0x2000
	s_nop 0
	global_load_lds_dwordx4 v[72:73], off
	s_waitcnt vmcnt(6)
	s_barrier
	v_mfma_f32_16x16x32_f16 v[52:55], v[190:193], v[136:139], v[52:55]
	v_mfma_f32_16x16x32_f16 v[48:51], v[198:201], v[136:139], v[48:51]
	v_mfma_f32_16x16x32_f16 v[36:39], v[190:193], v[152:155], v[36:39]
	v_mfma_f32_16x16x32_f16 v[32:35], v[198:201], v[152:155], v[32:35]
	v_mfma_f32_16x16x32_f16 v[20:23], v[190:193], v[160:163], v[20:23]
	v_mfma_f32_16x16x32_f16 v[16:19], v[198:201], v[160:163], v[16:19]
	v_mfma_f32_16x16x32_f16 v[4:7], v[190:193], v[168:171], v[4:7]
	v_mfma_f32_16x16x32_f16 v[0:3], v[198:201], v[168:171], v[0:3]
	v_mfma_f32_16x16x32_f16 v[52:55], v[194:197], v[148:151], v[52:55]
	v_mfma_f32_16x16x32_f16 v[48:51], v[202:205], v[148:151], v[48:51]
	v_mfma_f32_16x16x32_f16 v[36:39], v[194:197], v[156:159], v[36:39]
	v_mfma_f32_16x16x32_f16 v[32:35], v[202:205], v[156:159], v[32:35]
	v_mfma_f32_16x16x32_f16 v[20:23], v[194:197], v[164:167], v[20:23]
	v_mfma_f32_16x16x32_f16 v[16:19], v[202:205], v[164:167], v[16:19]
	v_mfma_f32_16x16x32_f16 v[4:7], v[194:197], v[172:175], v[4:7]
	v_mfma_f32_16x16x32_f16 v[0:3], v[202:205], v[172:175], v[0:3]
	s_barrier
	s_add_i32 s87, s87, 2
	s_add_u32 s38, s38, 0x100
	s_addc_u32 s39, s39, 0
	s_add_u32 s85, s85, 0x100
	s_addc_u32 s86, s86, 0
	s_cmp_gt_u32 s87, 45
	s_cbranch_scc0 .LBB10_27
	s_lshl_b32 s92, s84, 8
	s_add_i32 s92, s92, s57
	s_lshl_b32 s93, s83, 8
	s_or_b32 s93, s93, s60
	v_lshlrev_b32_e32 v237, 2, v226
	s_lshl_b32 s96, s93, 2
	s_add_u32 s94, s16, s96
	s_addc_u32 s95, s17, 0
	global_load_dwordx4 v[72:75], v237, s[94:95] offset:0
	global_load_dwordx4 v[80:83], v237, s[94:95] offset:16
	global_load_dwordx4 v[88:91], v237, s[94:95] offset:128
	global_load_dwordx4 v[92:95], v237, s[94:95] offset:144
	s_add_u32 s94, s18, s96
	s_addc_u32 s95, s19, 0
	global_load_dwordx4 v[136:139], v237, s[94:95] offset:0
	global_load_dwordx4 v[148:151], v237, s[94:95] offset:16
	global_load_dwordx4 v[152:155], v237, s[94:95] offset:128
	global_load_dwordx4 v[156:159], v237, s[94:95] offset:144
	s_add_u32 s94, s14, s96
	s_addc_u32 s95, s15, 0
	global_load_dwordx4 v[160:163], v237, s[94:95] offset:0
	global_load_dwordx4 v[164:167], v237, s[94:95] offset:16
	global_load_dwordx4 v[168:171], v237, s[94:95] offset:128
	global_load_dwordx4 v[172:175], v237, s[94:95] offset:144
	v_lshlrev_b32_e32 v190, 3, v227
	s_lshl_b32 s96, s92, 3
	s_add_u32 s94, s12, s96
	s_addc_u32 s95, s13, 0
	global_load_dwordx2 v[238:239], v190, s[94:95] offset:0
	global_load_dwordx2 v[192:193], v190, s[94:95] offset:128
	global_load_dwordx2 v[194:195], v190, s[94:95] offset:256
	global_load_dwordx2 v[196:197], v190, s[94:95] offset:384
	global_load_dwordx2 v[198:199], v190, s[94:95] offset:1024
	global_load_dwordx2 v[200:201], v190, s[94:95] offset:1152
	global_load_dwordx2 v[202:203], v190, s[94:95] offset:1280
	global_load_dwordx2 v[204:205], v190, s[94:95] offset:1408
	v_mul_u32_u24_e32 v191, 0x600, v227
	v_lshl_add_u32 v191, v226, 1, v191
	s_mul_i32 s96, s92, 0x600
	s_lshl_b32 s97, s93, 1
	s_add_u32 s96, s96, s97
	s_add_u32 s98, s10, s96
	s_addc_u32 s99, s11, 0
	s_add_u32 s94, s98, 0x0
	s_addc_u32 s95, s99, 0
	global_load_dwordx4 v[208:211], v191, s[94:95] offset:0 nt
	global_load_dwordx4 v[212:215], v191, s[94:95] offset:64 nt
	s_add_u32 s94, s98, 0x6000
	s_addc_u32 s95, s99, 0
	global_load_dwordx4 v[216:219], v191, s[94:95] offset:0 nt
	global_load_dwordx4 v[220:223], v191, s[94:95] offset:64 nt
	v_add_u32_e32 v224, s92, v229
	v_mul_u32_u24_e32 v224, 0x600, v224
	s_lshl_b32 s97, s93, 1
	v_add3_u32 v224, v224, v230, s97
	s_lshl_b32 s96, s83, 2
	s_lshr_b32 s97, s60, 6
	s_add_u32 s96, s96, s97
	s_lshl_b32 s96, s96, 19
	s_lshl_b32 s97, s92, 3
	s_add_u32 s96, s96, s97
	s_add_u32 s100, s28, s96
	s_addc_u32 s101, s29, 0
	s_waitcnt vmcnt(19)
	v_pk_add_f32 v[72:73], v[72:73], v[136:137]
	v_pk_add_f32 v[74:75], v[74:75], v[138:139]
	s_waitcnt vmcnt(18)
	v_pk_add_f32 v[80:81], v[80:81], v[148:149]
	v_pk_add_f32 v[82:83], v[82:83], v[150:151]
	s_waitcnt vmcnt(17)
	v_pk_add_f32 v[88:89], v[88:89], v[152:153]
	v_pk_add_f32 v[90:91], v[90:91], v[154:155]
	s_waitcnt vmcnt(16)
	v_pk_add_f32 v[92:93], v[92:93], v[156:157]
	v_pk_add_f32 v[94:95], v[94:95], v[158:159]
	v_pk_add_f32 v[144:145], v[144:145], v[72:73]
	v_pk_add_f32 v[146:147], v[146:147], v[74:75]
	v_pk_add_f32 v[124:125], v[124:125], v[72:73]
	v_pk_add_f32 v[126:127], v[126:127], v[74:75]
	v_pk_add_f32 v[108:109], v[108:109], v[72:73]
	v_pk_add_f32 v[110:111], v[110:111], v[74:75]
	v_pk_add_f32 v[84:85], v[84:85], v[72:73]
	v_pk_add_f32 v[86:87], v[86:87], v[74:75]
	v_pk_add_f32 v[60:61], v[60:61], v[72:73]
	v_pk_add_f32 v[62:63], v[62:63], v[74:75]
	v_pk_add_f32 v[44:45], v[44:45], v[72:73]
	v_pk_add_f32 v[46:47], v[46:47], v[74:75]
	v_pk_add_f32 v[28:29], v[28:29], v[72:73]
	v_pk_add_f32 v[30:31], v[30:31], v[74:75]
	v_pk_add_f32 v[12:13], v[12:13], v[72:73]
	v_pk_add_f32 v[14:15], v[14:15], v[74:75]
	v_pk_add_f32 v[140:141], v[140:141], v[80:81]
	v_pk_add_f32 v[142:143], v[142:143], v[82:83]
	v_pk_add_f32 v[120:121], v[120:121], v[80:81]
	v_pk_add_f32 v[122:123], v[122:123], v[82:83]
	v_pk_add_f32 v[104:105], v[104:105], v[80:81]
	v_pk_add_f32 v[106:107], v[106:107], v[82:83]
	v_pk_add_f32 v[76:77], v[76:77], v[80:81]
	v_pk_add_f32 v[78:79], v[78:79], v[82:83]
	v_pk_add_f32 v[56:57], v[56:57], v[80:81]
	v_pk_add_f32 v[58:59], v[58:59], v[82:83]
	v_pk_add_f32 v[40:41], v[40:41], v[80:81]
	v_pk_add_f32 v[42:43], v[42:43], v[82:83]
	v_pk_add_f32 v[24:25], v[24:25], v[80:81]
	v_pk_add_f32 v[26:27], v[26:27], v[82:83]
	v_pk_add_f32 v[8:9], v[8:9], v[80:81]
	v_pk_add_f32 v[10:11], v[10:11], v[82:83]
	v_pk_add_f32 v[132:133], v[132:133], v[88:89]
	v_pk_add_f32 v[134:135], v[134:135], v[90:91]
	v_pk_add_f32 v[116:117], v[116:117], v[88:89]
	v_pk_add_f32 v[118:119], v[118:119], v[90:91]
	v_pk_add_f32 v[100:101], v[100:101], v[88:89]
	v_pk_add_f32 v[102:103], v[102:103], v[90:91]
	v_pk_add_f32 v[68:69], v[68:69], v[88:89]
	v_pk_add_f32 v[70:71], v[70:71], v[90:91]
	v_pk_add_f32 v[52:53], v[52:53], v[88:89]
	v_pk_add_f32 v[54:55], v[54:55], v[90:91]
	v_pk_add_f32 v[36:37], v[36:37], v[88:89]
	v_pk_add_f32 v[38:39], v[38:39], v[90:91]
	v_pk_add_f32 v[20:21], v[20:21], v[88:89]
	v_pk_add_f32 v[22:23], v[22:23], v[90:91]
	v_pk_add_f32 v[4:5], v[4:5], v[88:89]
	v_pk_add_f32 v[6:7], v[6:7], v[90:91]
	v_pk_add_f32 v[128:129], v[128:129], v[92:93]
	v_pk_add_f32 v[130:131], v[130:131], v[94:95]
	v_pk_add_f32 v[112:113], v[112:113], v[92:93]
	v_pk_add_f32 v[114:115], v[114:115], v[94:95]
	v_pk_add_f32 v[96:97], v[96:97], v[92:93]
	v_pk_add_f32 v[98:99], v[98:99], v[94:95]
	v_pk_add_f32 v[64:65], v[64:65], v[92:93]
	v_pk_add_f32 v[66:67], v[66:67], v[94:95]
	v_pk_add_f32 v[48:49], v[48:49], v[92:93]
	v_pk_add_f32 v[50:51], v[50:51], v[94:95]
	v_pk_add_f32 v[32:33], v[32:33], v[92:93]
	v_pk_add_f32 v[34:35], v[34:35], v[94:95]
	v_pk_add_f32 v[16:17], v[16:17], v[92:93]
	v_pk_add_f32 v[18:19], v[18:19], v[94:95]
	v_pk_add_f32 v[0:1], v[0:1], v[92:93]
	v_pk_add_f32 v[2:3], v[2:3], v[94:95]
	s_add_u32 s94, s98, 0xc000
	s_addc_u32 s95, s99, 0
	global_load_dwordx4 v[240:243], v191, s[94:95] offset:0 nt
	global_load_dwordx4 v[244:247], v191, s[94:95] offset:64 nt
	s_add_u32 s94, s98, 0x12000
	s_addc_u32 s95, s99, 0
	global_load_dwordx4 v[248:251], v191, s[94:95] offset:0 nt
	global_load_dwordx4 v[252:255], v191, s[94:95] offset:64 nt
	s_add_u32 s94, s98, 0x30000
	s_addc_u32 s95, s99, 0
	global_load_dwordx4 v[136:139], v191, s[94:95] offset:0 nt
	global_load_dwordx4 v[148:151], v191, s[94:95] offset:64 nt
	s_add_u32 s94, s98, 0x36000
	s_addc_u32 s95, s99, 0
	global_load_dwordx4 v[152:155], v191, s[94:95] offset:0 nt
	global_load_dwordx4 v[156:159], v191, s[94:95] offset:64 nt
	s_waitcnt vmcnt(19)
	s_waitcnt vmcnt(11)
	v_cvt_f32_f16_e32 v72, v208
	v_cvt_f32_f16_sdwa v73, v208 dst_sel:DWORD dst_unused:UNUSED_PAD src0_sel:WORD_1
	v_cvt_f32_f16_e32 v74, v209
	v_cvt_f32_f16_sdwa v75, v209 dst_sel:DWORD dst_unused:UNUSED_PAD src0_sel:WORD_1
	v_cvt_f32_f16_e32 v80, v210
	v_cvt_f32_f16_sdwa v81, v210 dst_sel:DWORD dst_unused:UNUSED_PAD src0_sel:WORD_1
	v_cvt_f32_f16_e32 v82, v211
	v_cvt_f32_f16_sdwa v83, v211 dst_sel:DWORD dst_unused:UNUSED_PAD src0_sel:WORD_1
	v_sub_f32_e32 v72, v72, v238
	v_sub_f32_e32 v73, v73, v238
	v_sub_f32_e32 v74, v74, v238
	v_sub_f32_e32 v75, v75, v238
	v_sub_f32_e32 v80, v80, v238
	v_sub_f32_e32 v81, v81, v238
	v_sub_f32_e32 v82, v82, v238
	v_sub_f32_e32 v83, v83, v238
	v_pk_mul_f32 v[72:73], v[238:239], v[72:73] op_sel:[1,0]
	v_pk_mul_f32 v[74:75], v[238:239], v[74:75] op_sel:[1,0]
	v_pk_mul_f32 v[80:81], v[238:239], v[80:81] op_sel:[1,0]
	v_pk_mul_f32 v[82:83], v[238:239], v[82:83] op_sel:[1,0]
	v_pk_fma_f32 v[144:145], v[72:73], v[160:161], v[144:145]
	v_pk_fma_f32 v[146:147], v[74:75], v[162:163], v[146:147]
	v_pk_fma_f32 v[140:141], v[80:81], v[164:165], v[140:141]
	v_pk_fma_f32 v[142:143], v[82:83], v[166:167], v[142:143]
	v_cvt_pk_f16_f32 v144, v144, v145
	v_cvt_pk_f16_f32 v145, v146, v147
	v_cvt_pk_f16_f32 v146, v140, v141
	v_cvt_pk_f16_f32 v147, v142, v143
	ds_write_b128 v235, v[144:147]
	v_fma_mix_f32 v206, v144, 1.0, 0 op_sel_hi:[1,0,0]
	v_fma_mix_f32 v207, v144, v144, 0 op_sel_hi:[1,1,0]
	v_fma_mix_f32 v206, v144, 1.0, v206 op_sel:[1,0,0] op_sel_hi:[1,0,0]
	v_fma_mix_f32 v207, v144, v144, v207 op_sel:[1,1,0] op_sel_hi:[1,1,0]
	v_fma_mix_f32 v206, v145, 1.0, v206 op_sel_hi:[1,0,0]
	v_fma_mix_f32 v207, v145, v145, v207 op_sel_hi:[1,1,0]
	v_fma_mix_f32 v206, v145, 1.0, v206 op_sel:[1,0,0] op_sel_hi:[1,0,0]
	v_fma_mix_f32 v207, v145, v145, v207 op_sel:[1,1,0] op_sel_hi:[1,1,0]
	v_fma_mix_f32 v206, v146, 1.0, v206 op_sel_hi:[1,0,0]
	v_fma_mix_f32 v207, v146, v146, v207 op_sel_hi:[1,1,0]
	v_fma_mix_f32 v206, v146, 1.0, v206 op_sel:[1,0,0] op_sel_hi:[1,0,0]
	v_fma_mix_f32 v207, v146, v146, v207 op_sel:[1,1,0] op_sel_hi:[1,1,0]
	v_fma_mix_f32 v206, v147, 1.0, v206 op_sel_hi:[1,0,0]
	v_fma_mix_f32 v207, v147, v147, v207 op_sel_hi:[1,1,0]
	v_fma_mix_f32 v206, v147, 1.0, v206 op_sel:[1,0,0] op_sel_hi:[1,0,0]
	v_fma_mix_f32 v207, v147, v147, v207 op_sel:[1,1,0] op_sel_hi:[1,1,0]
	s_waitcnt vmcnt(10)
	v_cvt_f32_f16_e32 v72, v212
	v_cvt_f32_f16_sdwa v73, v212 dst_sel:DWORD dst_unused:UNUSED_PAD src0_sel:WORD_1
	v_cvt_f32_f16_e32 v74, v213
	v_cvt_f32_f16_sdwa v75, v213 dst_sel:DWORD dst_unused:UNUSED_PAD src0_sel:WORD_1
	v_cvt_f32_f16_e32 v80, v214
	v_cvt_f32_f16_sdwa v81, v214 dst_sel:DWORD dst_unused:UNUSED_PAD src0_sel:WORD_1
	v_cvt_f32_f16_e32 v82, v215
	v_cvt_f32_f16_sdwa v83, v215 dst_sel:DWORD dst_unused:UNUSED_PAD src0_sel:WORD_1
	v_sub_f32_e32 v72, v72, v238
	v_sub_f32_e32 v73, v73, v238
	v_sub_f32_e32 v74, v74, v238
	v_sub_f32_e32 v75, v75, v238
	v_sub_f32_e32 v80, v80, v238
	v_sub_f32_e32 v81, v81, v238
	v_sub_f32_e32 v82, v82, v238
	v_sub_f32_e32 v83, v83, v238
	v_pk_mul_f32 v[72:73], v[238:239], v[72:73] op_sel:[1,0]
	v_pk_mul_f32 v[74:75], v[238:239], v[74:75] op_sel:[1,0]
	v_pk_mul_f32 v[80:81], v[238:239], v[80:81] op_sel:[1,0]
	v_pk_mul_f32 v[82:83], v[238:239], v[82:83] op_sel:[1,0]
	v_pk_fma_f32 v[132:133], v[72:73], v[168:169], v[132:133]
	v_pk_fma_f32 v[134:135], v[74:75], v[170:171], v[134:135]
	v_pk_fma_f32 v[128:129], v[80:81], v[172:173], v[128:129]
	v_pk_fma_f32 v[130:131], v[82:83], v[174:175], v[130:131]
	v_cvt_pk_f16_f32 v132, v132, v133
	v_cvt_pk_f16_f32 v133, v134, v135
	v_cvt_pk_f16_f32 v134, v128, v129
	v_cvt_pk_f16_f32 v135, v130, v131
	ds_write_b128 v235, v[132:135] offset:64
	v_fma_mix_f32 v206, v132, 1.0, v206 op_sel_hi:[1,0,0]
	v_fma_mix_f32 v207, v132, v132, v207 op_sel_hi:[1,1,0]
	v_fma_mix_f32 v206, v132, 1.0, v206 op_sel:[1,0,0] op_sel_hi:[1,0,0]
	v_fma_mix_f32 v207, v132, v132, v207 op_sel:[1,1,0] op_sel_hi:[1,1,0]
	v_fma_mix_f32 v206, v133, 1.0, v206 op_sel_hi:[1,0,0]
	v_fma_mix_f32 v207, v133, v133, v207 op_sel_hi:[1,1,0]
	v_fma_mix_f32 v206, v133, 1.0, v206 op_sel:[1,0,0] op_sel_hi:[1,0,0]
	v_fma_mix_f32 v207, v133, v133, v207 op_sel:[1,1,0] op_sel_hi:[1,1,0]
	v_fma_mix_f32 v206, v134, 1.0, v206 op_sel_hi:[1,0,0]
	v_fma_mix_f32 v207, v134, v134, v207 op_sel_hi:[1,1,0]
	v_fma_mix_f32 v206, v134, 1.0, v206 op_sel:[1,0,0] op_sel_hi:[1,0,0]
	v_fma_mix_f32 v207, v134, v134, v207 op_sel:[1,1,0] op_sel_hi:[1,1,0]
	v_fma_mix_f32 v206, v135, 1.0, v206 op_sel_hi:[1,0,0]
	v_fma_mix_f32 v207, v135, v135, v207 op_sel_hi:[1,1,0]
	v_fma_mix_f32 v206, v135, 1.0, v206 op_sel:[1,0,0] op_sel_hi:[1,0,0]
	v_fma_mix_f32 v207, v135, v135, v207 op_sel:[1,1,0] op_sel_hi:[1,1,0]
	ds_read_b128 v[88:91], v236
	ds_read_b128 v[92:95], v236 offset:1152
	s_waitcnt vmcnt(9)
	v_cvt_f32_f16_e32 v72, v216
	v_cvt_f32_f16_sdwa v73, v216 dst_sel:DWORD dst_unused:UNUSED_PAD src0_sel:WORD_1
	v_cvt_f32_f16_e32 v74, v217
	v_cvt_f32_f16_sdwa v75, v217 dst_sel:DWORD dst_unused:UNUSED_PAD src0_sel:WORD_1
	v_cvt_f32_f16_e32 v80, v218
	v_cvt_f32_f16_sdwa v81, v218 dst_sel:DWORD dst_unused:UNUSED_PAD src0_sel:WORD_1
	v_cvt_f32_f16_e32 v82, v219
	v_cvt_f32_f16_sdwa v83, v219 dst_sel:DWORD dst_unused:UNUSED_PAD src0_sel:WORD_1
	v_sub_f32_e32 v72, v72, v192
	v_sub_f32_e32 v73, v73, v192
	v_sub_f32_e32 v74, v74, v192
	v_sub_f32_e32 v75, v75, v192
	v_sub_f32_e32 v80, v80, v192
	v_sub_f32_e32 v81, v81, v192
	v_sub_f32_e32 v82, v82, v192
	v_sub_f32_e32 v83, v83, v192
	v_pk_mul_f32 v[72:73], v[192:193], v[72:73] op_sel:[1,0]
	v_pk_mul_f32 v[74:75], v[192:193], v[74:75] op_sel:[1,0]
	v_pk_mul_f32 v[80:81], v[192:193], v[80:81] op_sel:[1,0]
	v_pk_mul_f32 v[82:83], v[192:193], v[82:83] op_sel:[1,0]
	v_pk_fma_f32 v[124:125], v[72:73], v[160:161], v[124:125]
	v_pk_fma_f32 v[126:127], v[74:75], v[162:163], v[126:127]
	v_pk_fma_f32 v[120:121], v[80:81], v[164:165], v[120:121]
	v_pk_fma_f32 v[122:123], v[82:83], v[166:167], v[122:123]
	v_cvt_pk_f16_f32 v124, v124, v125
	v_cvt_pk_f16_f32 v125, v126, v127
	v_cvt_pk_f16_f32 v126, v120, v121
	v_cvt_pk_f16_f32 v127, v122, v123
	s_waitcnt lgkmcnt(0)
	buffer_store_dwordx4 v[88:91], v224, s[24:27], 0 offen nt
	v_add_u32_e32 v82, 0x3000, v224
	buffer_store_dwordx4 v[92:95], v82, s[24:27], 0 offen nt
	ds_write_b128 v235, v[124:127]
	v_fma_mix_f32 v140, v124, 1.0, 0 op_sel_hi:[1,0,0]
	v_fma_mix_f32 v141, v124, v124, 0 op_sel_hi:[1,1,0]
	v_fma_mix_f32 v140, v124, 1.0, v140 op_sel:[1,0,0] op_sel_hi:[1,0,0]
	v_fma_mix_f32 v141, v124, v124, v141 op_sel:[1,1,0] op_sel_hi:[1,1,0]
	v_fma_mix_f32 v140, v125, 1.0, v140 op_sel_hi:[1,0,0]
	v_fma_mix_f32 v141, v125, v125, v141 op_sel_hi:[1,1,0]
	v_fma_mix_f32 v140, v125, 1.0, v140 op_sel:[1,0,0] op_sel_hi:[1,0,0]
	v_fma_mix_f32 v141, v125, v125, v141 op_sel:[1,1,0] op_sel_hi:[1,1,0]
	v_fma_mix_f32 v140, v126, 1.0, v140 op_sel_hi:[1,0,0]
	v_fma_mix_f32 v141, v126, v126, v141 op_sel_hi:[1,1,0]
	v_fma_mix_f32 v140, v126, 1.0, v140 op_sel:[1,0,0] op_sel_hi:[1,0,0]
	v_fma_mix_f32 v141, v126, v126, v141 op_sel:[1,1,0] op_sel_hi:[1,1,0]
	v_fma_mix_f32 v140, v127, 1.0, v140 op_sel_hi:[1,0,0]
	v_fma_mix_f32 v141, v127, v127, v141 op_sel_hi:[1,1,0]
	v_fma_mix_f32 v140, v127, 1.0, v140 op_sel:[1,0,0] op_sel_hi:[1,0,0]
	v_fma_mix_f32 v141, v127, v127, v141 op_sel:[1,1,0] op_sel_hi:[1,1,0]
	s_waitcnt vmcnt(10)
	v_cvt_f32_f16_e32 v72, v220
	v_cvt_f32_f16_sdwa v73, v220 dst_sel:DWORD dst_unused:UNUSED_PAD src0_sel:WORD_1
	v_cvt_f32_f16_e32 v74, v221
	v_cvt_f32_f16_sdwa v75, v221 dst_sel:DWORD dst_unused:UNUSED_PAD src0_sel:WORD_1
	v_cvt_f32_f16_e32 v80, v222
	v_cvt_f32_f16_sdwa v81, v222 dst_sel:DWORD dst_unused:UNUSED_PAD src0_sel:WORD_1
	v_cvt_f32_f16_e32 v82, v223
	v_cvt_f32_f16_sdwa v83, v223 dst_sel:DWORD dst_unused:UNUSED_PAD src0_sel:WORD_1
	v_sub_f32_e32 v72, v72, v192
	v_sub_f32_e32 v73, v73, v192
	v_sub_f32_e32 v74, v74, v192
	v_sub_f32_e32 v75, v75, v192
	v_sub_f32_e32 v80, v80, v192
	v_sub_f32_e32 v81, v81, v192
	v_sub_f32_e32 v82, v82, v192
	v_sub_f32_e32 v83, v83, v192
	v_pk_mul_f32 v[72:73], v[192:193], v[72:73] op_sel:[1,0]
	v_pk_mul_f32 v[74:75], v[192:193], v[74:75] op_sel:[1,0]
	v_pk_mul_f32 v[80:81], v[192:193], v[80:81] op_sel:[1,0]
	v_pk_mul_f32 v[82:83], v[192:193], v[82:83] op_sel:[1,0]
	v_pk_fma_f32 v[116:117], v[72:73], v[168:169], v[116:117]
	v_pk_fma_f32 v[118:119], v[74:75], v[170:171], v[118:119]
	v_pk_fma_f32 v[112:113], v[80:81], v[172:173], v[112:113]
	v_pk_fma_f32 v[114:115], v[82:83], v[174:175], v[114:115]
	v_cvt_pk_f16_f32 v116, v116, v117
	v_cvt_pk_f16_f32 v117, v118, v119
	v_cvt_pk_f16_f32 v118, v112, v113
	v_cvt_pk_f16_f32 v119, v114, v115
	ds_write_b128 v235, v[116:119] offset:64
	v_fma_mix_f32 v140, v116, 1.0, v140 op_sel_hi:[1,0,0]
	v_fma_mix_f32 v141, v116, v116, v141 op_sel_hi:[1,1,0]
	v_fma_mix_f32 v140, v116, 1.0, v140 op_sel:[1,0,0] op_sel_hi:[1,0,0]
	v_fma_mix_f32 v141, v116, v116, v141 op_sel:[1,1,0] op_sel_hi:[1,1,0]
	v_fma_mix_f32 v140, v117, 1.0, v140 op_sel_hi:[1,0,0]
	v_fma_mix_f32 v141, v117, v117, v141 op_sel_hi:[1,1,0]
	v_fma_mix_f32 v140, v117, 1.0, v140 op_sel:[1,0,0] op_sel_hi:[1,0,0]
	v_fma_mix_f32 v141, v117, v117, v141 op_sel:[1,1,0] op_sel_hi:[1,1,0]
	v_fma_mix_f32 v140, v118, 1.0, v140 op_sel_hi:[1,0,0]
	v_fma_mix_f32 v141, v118, v118, v141 op_sel_hi:[1,1,0]
	v_fma_mix_f32 v140, v118, 1.0, v140 op_sel:[1,0,0] op_sel_hi:[1,0,0]
	v_fma_mix_f32 v141, v118, v118, v141 op_sel:[1,1,0] op_sel_hi:[1,1,0]
	v_fma_mix_f32 v140, v119, 1.0, v140 op_sel_hi:[1,0,0]
	v_fma_mix_f32 v141, v119, v119, v141 op_sel_hi:[1,1,0]
	v_fma_mix_f32 v140, v119, 1.0, v140 op_sel:[1,0,0] op_sel_hi:[1,0,0]
	v_fma_mix_f32 v141, v119, v119, v141 op_sel:[1,1,0] op_sel_hi:[1,1,0]
	ds_read_b128 v[208:211], v236
	ds_read_b128 v[128:131], v236 offset:1152
	s_add_u32 s94, s98, 0x3c000
	s_addc_u32 s95, s99, 0
	global_load_dwordx4 v[212:215], v191, s[94:95] offset:0 nt
	global_load_dwordx4 v[144:147], v191, s[94:95] offset:64 nt
	s_add_u32 s94, s98, 0x42000
	s_addc_u32 s95, s99, 0
	global_load_dwordx4 v[132:135], v191, s[94:95] offset:0 nt
	global_load_dwordx4 v[88:91], v191, s[94:95] offset:64 nt
	s_waitcnt vmcnt(13)
	v_cvt_f32_f16_e32 v72, v240
	v_cvt_f32_f16_sdwa v73, v240 dst_sel:DWORD dst_unused:UNUSED_PAD src0_sel:WORD_1
	v_cvt_f32_f16_e32 v74, v241
	v_cvt_f32_f16_sdwa v75, v241 dst_sel:DWORD dst_unused:UNUSED_PAD src0_sel:WORD_1
	v_cvt_f32_f16_e32 v80, v242
	v_cvt_f32_f16_sdwa v81, v242 dst_sel:DWORD dst_unused:UNUSED_PAD src0_sel:WORD_1
	v_cvt_f32_f16_e32 v82, v243
	v_cvt_f32_f16_sdwa v83, v243 dst_sel:DWORD dst_unused:UNUSED_PAD src0_sel:WORD_1
	v_sub_f32_e32 v72, v72, v194
	v_sub_f32_e32 v73, v73, v194
	v_sub_f32_e32 v74, v74, v194
	v_sub_f32_e32 v75, v75, v194
	v_sub_f32_e32 v80, v80, v194
	v_sub_f32_e32 v81, v81, v194
	v_sub_f32_e32 v82, v82, v194
	v_sub_f32_e32 v83, v83, v194
	v_pk_mul_f32 v[72:73], v[194:195], v[72:73] op_sel:[1,0]
	v_pk_mul_f32 v[74:75], v[194:195], v[74:75] op_sel:[1,0]
	v_pk_mul_f32 v[80:81], v[194:195], v[80:81] op_sel:[1,0]
	v_pk_mul_f32 v[82:83], v[194:195], v[82:83] op_sel:[1,0]
	v_pk_fma_f32 v[108:109], v[72:73], v[160:161], v[108:109]
	v_pk_fma_f32 v[110:111], v[74:75], v[162:163], v[110:111]
	v_pk_fma_f32 v[104:105], v[80:81], v[164:165], v[104:105]
	v_pk_fma_f32 v[106:107], v[82:83], v[166:167], v[106:107]
	v_cvt_pk_f16_f32 v108, v108, v109
	v_cvt_pk_f16_f32 v109, v110, v111
	v_cvt_pk_f16_f32 v110, v104, v105
	v_cvt_pk_f16_f32 v111, v106, v107
	s_waitcnt lgkmcnt(0)
	v_add_u32_e32 v83, 0x6000, v224
	buffer_store_dwordx4 v[208:211], v83, s[24:27], 0 offen nt
	v_add_u32_e32 v82, 0x9000, v224
	buffer_store_dwordx4 v[128:131], v82, s[24:27], 0 offen nt
	ds_write_b128 v235, v[108:111]
	v_fma_mix_f32 v142, v108, 1.0, 0 op_sel_hi:[1,0,0]
	v_fma_mix_f32 v143, v108, v108, 0 op_sel_hi:[1,1,0]
	v_fma_mix_f32 v142, v108, 1.0, v142 op_sel:[1,0,0] op_sel_hi:[1,0,0]
	v_fma_mix_f32 v143, v108, v108, v143 op_sel:[1,1,0] op_sel_hi:[1,1,0]
	v_fma_mix_f32 v142, v109, 1.0, v142 op_sel_hi:[1,0,0]
	v_fma_mix_f32 v143, v109, v109, v143 op_sel_hi:[1,1,0]
	v_fma_mix_f32 v142, v109, 1.0, v142 op_sel:[1,0,0] op_sel_hi:[1,0,0]
	v_fma_mix_f32 v143, v109, v109, v143 op_sel:[1,1,0] op_sel_hi:[1,1,0]
	v_fma_mix_f32 v142, v110, 1.0, v142 op_sel_hi:[1,0,0]
	v_fma_mix_f32 v143, v110, v110, v143 op_sel_hi:[1,1,0]
	v_fma_mix_f32 v142, v110, 1.0, v142 op_sel:[1,0,0] op_sel_hi:[1,0,0]
	v_fma_mix_f32 v143, v110, v110, v143 op_sel:[1,1,0] op_sel_hi:[1,1,0]
	v_fma_mix_f32 v142, v111, 1.0, v142 op_sel_hi:[1,0,0]
	v_fma_mix_f32 v143, v111, v111, v143 op_sel_hi:[1,1,0]
	v_fma_mix_f32 v142, v111, 1.0, v142 op_sel:[1,0,0] op_sel_hi:[1,0,0]
	v_fma_mix_f32 v143, v111, v111, v143 op_sel:[1,1,0] op_sel_hi:[1,1,0]
	s_waitcnt vmcnt(14)
	v_cvt_f32_f16_e32 v72, v244
	v_cvt_f32_f16_sdwa v73, v244 dst_sel:DWORD dst_unused:UNUSED_PAD src0_sel:WORD_1
	v_cvt_f32_f16_e32 v74, v245
	v_cvt_f32_f16_sdwa v75, v245 dst_sel:DWORD dst_unused:UNUSED_PAD src0_sel:WORD_1
	v_cvt_f32_f16_e32 v80, v246
	v_cvt_f32_f16_sdwa v81, v246 dst_sel:DWORD dst_unused:UNUSED_PAD src0_sel:WORD_1
	v_cvt_f32_f16_e32 v82, v247
	v_cvt_f32_f16_sdwa v83, v247 dst_sel:DWORD dst_unused:UNUSED_PAD src0_sel:WORD_1
	v_sub_f32_e32 v72, v72, v194
	v_sub_f32_e32 v73, v73, v194
	v_sub_f32_e32 v74, v74, v194
	v_sub_f32_e32 v75, v75, v194
	v_sub_f32_e32 v80, v80, v194
	v_sub_f32_e32 v81, v81, v194
	v_sub_f32_e32 v82, v82, v194
	v_sub_f32_e32 v83, v83, v194
	v_pk_mul_f32 v[72:73], v[194:195], v[72:73] op_sel:[1,0]
	v_pk_mul_f32 v[74:75], v[194:195], v[74:75] op_sel:[1,0]
	v_pk_mul_f32 v[80:81], v[194:195], v[80:81] op_sel:[1,0]
	v_pk_mul_f32 v[82:83], v[194:195], v[82:83] op_sel:[1,0]
	v_pk_fma_f32 v[100:101], v[72:73], v[168:169], v[100:101]
	v_pk_fma_f32 v[102:103], v[74:75], v[170:171], v[102:103]
	v_pk_fma_f32 v[96:97], v[80:81], v[172:173], v[96:97]
	v_pk_fma_f32 v[98:99], v[82:83], v[174:175], v[98:99]
	v_cvt_pk_f16_f32 v100, v100, v101
	v_cvt_pk_f16_f32 v101, v102, v103
	v_cvt_pk_f16_f32 v102, v96, v97
	v_cvt_pk_f16_f32 v103, v98, v99
	ds_write_b128 v235, v[100:103] offset:64
	v_fma_mix_f32 v142, v100, 1.0, v142 op_sel_hi:[1,0,0]
	v_fma_mix_f32 v143, v100, v100, v143 op_sel_hi:[1,1,0]
	v_fma_mix_f32 v142, v100, 1.0, v142 op_sel:[1,0,0] op_sel_hi:[1,0,0]
	v_fma_mix_f32 v143, v100, v100, v143 op_sel:[1,1,0] op_sel_hi:[1,1,0]
	v_fma_mix_f32 v142, v101, 1.0, v142 op_sel_hi:[1,0,0]
	v_fma_mix_f32 v143, v101, v101, v143 op_sel_hi:[1,1,0]
	v_fma_mix_f32 v142, v101, 1.0, v142 op_sel:[1,0,0] op_sel_hi:[1,0,0]
	v_fma_mix_f32 v143, v101, v101, v143 op_sel:[1,1,0] op_sel_hi:[1,1,0]
	v_fma_mix_f32 v142, v102, 1.0, v142 op_sel_hi:[1,0,0]
	v_fma_mix_f32 v143, v102, v102, v143 op_sel_hi:[1,1,0]
	v_fma_mix_f32 v142, v102, 1.0, v142 op_sel:[1,0,0] op_sel_hi:[1,0,0]
	v_fma_mix_f32 v143, v102, v102, v143 op_sel:[1,1,0] op_sel_hi:[1,1,0]
	v_fma_mix_f32 v142, v103, 1.0, v142 op_sel_hi:[1,0,0]
	v_fma_mix_f32 v143, v103, v103, v143 op_sel_hi:[1,1,0]
	v_fma_mix_f32 v142, v103, 1.0, v142 op_sel:[1,0,0] op_sel_hi:[1,0,0]
	v_fma_mix_f32 v143, v103, v103, v143 op_sel:[1,1,0] op_sel_hi:[1,1,0]
	ds_read_b128 v[92:95], v236
	ds_read_b128 v[120:123], v236 offset:1152
	s_waitcnt vmcnt(13)
	v_cvt_f32_f16_e32 v72, v248
	v_cvt_f32_f16_sdwa v73, v248 dst_sel:DWORD dst_unused:UNUSED_PAD src0_sel:WORD_1
	v_cvt_f32_f16_e32 v74, v249
	v_cvt_f32_f16_sdwa v75, v249 dst_sel:DWORD dst_unused:UNUSED_PAD src0_sel:WORD_1
	v_cvt_f32_f16_e32 v80, v250
	v_cvt_f32_f16_sdwa v81, v250 dst_sel:DWORD dst_unused:UNUSED_PAD src0_sel:WORD_1
	v_cvt_f32_f16_e32 v82, v251
	v_cvt_f32_f16_sdwa v83, v251 dst_sel:DWORD dst_unused:UNUSED_PAD src0_sel:WORD_1
	v_sub_f32_e32 v72, v72, v196
	v_sub_f32_e32 v73, v73, v196
	v_sub_f32_e32 v74, v74, v196
	v_sub_f32_e32 v75, v75, v196
	v_sub_f32_e32 v80, v80, v196
	v_sub_f32_e32 v81, v81, v196
	v_sub_f32_e32 v82, v82, v196
	v_sub_f32_e32 v83, v83, v196
	v_pk_mul_f32 v[72:73], v[196:197], v[72:73] op_sel:[1,0]
	v_pk_mul_f32 v[74:75], v[196:197], v[74:75] op_sel:[1,0]
	v_pk_mul_f32 v[80:81], v[196:197], v[80:81] op_sel:[1,0]
	v_pk_mul_f32 v[82:83], v[196:197], v[82:83] op_sel:[1,0]
	v_pk_fma_f32 v[84:85], v[72:73], v[160:161], v[84:85]
	v_pk_fma_f32 v[86:87], v[74:75], v[162:163], v[86:87]
	v_pk_fma_f32 v[76:77], v[80:81], v[164:165], v[76:77]
	v_pk_fma_f32 v[78:79], v[82:83], v[166:167], v[78:79]
	v_cvt_pk_f16_f32 v84, v84, v85
	v_cvt_pk_f16_f32 v85, v86, v87
	v_cvt_pk_f16_f32 v86, v76, v77
	v_cvt_pk_f16_f32 v87, v78, v79
	s_waitcnt lgkmcnt(0)
	v_add_u32_e32 v83, 0xc000, v224
	buffer_store_dwordx4 v[92:95], v83, s[24:27], 0 offen nt
	v_add_u32_e32 v82, 0xf000, v224
	buffer_store_dwordx4 v[120:123], v82, s[24:27], 0 offen nt
	ds_write_b128 v235, v[84:87]
	v_fma_mix_f32 v216, v84, 1.0, 0 op_sel_hi:[1,0,0]
	v_fma_mix_f32 v217, v84, v84, 0 op_sel_hi:[1,1,0]
	v_fma_mix_f32 v216, v84, 1.0, v216 op_sel:[1,0,0] op_sel_hi:[1,0,0]
	v_fma_mix_f32 v217, v84, v84, v217 op_sel:[1,1,0] op_sel_hi:[1,1,0]
	v_fma_mix_f32 v216, v85, 1.0, v216 op_sel_hi:[1,0,0]
	v_fma_mix_f32 v217, v85, v85, v217 op_sel_hi:[1,1,0]
	v_fma_mix_f32 v216, v85, 1.0, v216 op_sel:[1,0,0] op_sel_hi:[1,0,0]
	v_fma_mix_f32 v217, v85, v85, v217 op_sel:[1,1,0] op_sel_hi:[1,1,0]
	v_fma_mix_f32 v216, v86, 1.0, v216 op_sel_hi:[1,0,0]
	v_fma_mix_f32 v217, v86, v86, v217 op_sel_hi:[1,1,0]
	v_fma_mix_f32 v216, v86, 1.0, v216 op_sel:[1,0,0] op_sel_hi:[1,0,0]
	v_fma_mix_f32 v217, v86, v86, v217 op_sel:[1,1,0] op_sel_hi:[1,1,0]
	v_fma_mix_f32 v216, v87, 1.0, v216 op_sel_hi:[1,0,0]
	v_fma_mix_f32 v217, v87, v87, v217 op_sel_hi:[1,1,0]
	v_fma_mix_f32 v216, v87, 1.0, v216 op_sel:[1,0,0] op_sel_hi:[1,0,0]
	v_fma_mix_f32 v217, v87, v87, v217 op_sel:[1,1,0] op_sel_hi:[1,1,0]
	s_waitcnt vmcnt(14)
	v_cvt_f32_f16_e32 v72, v252
	v_cvt_f32_f16_sdwa v73, v252 dst_sel:DWORD dst_unused:UNUSED_PAD src0_sel:WORD_1
	v_cvt_f32_f16_e32 v74, v253
	v_cvt_f32_f16_sdwa v75, v253 dst_sel:DWORD dst_unused:UNUSED_PAD src0_sel:WORD_1
	v_cvt_f32_f16_e32 v80, v254
	v_cvt_f32_f16_sdwa v81, v254 dst_sel:DWORD dst_unused:UNUSED_PAD src0_sel:WORD_1
	v_cvt_f32_f16_e32 v82, v255
	v_cvt_f32_f16_sdwa v83, v255 dst_sel:DWORD dst_unused:UNUSED_PAD src0_sel:WORD_1
	v_sub_f32_e32 v72, v72, v196
	v_sub_f32_e32 v73, v73, v196
	v_sub_f32_e32 v74, v74, v196
	v_sub_f32_e32 v75, v75, v196
	v_sub_f32_e32 v80, v80, v196
	v_sub_f32_e32 v81, v81, v196
	v_sub_f32_e32 v82, v82, v196
	v_sub_f32_e32 v83, v83, v196
	v_pk_mul_f32 v[72:73], v[196:197], v[72:73] op_sel:[1,0]
	v_pk_mul_f32 v[74:75], v[196:197], v[74:75] op_sel:[1,0]
	v_pk_mul_f32 v[80:81], v[196:197], v[80:81] op_sel:[1,0]
	v_pk_mul_f32 v[82:83], v[196:197], v[82:83] op_sel:[1,0]
	v_pk_fma_f32 v[68:69], v[72:73], v[168:169], v[68:69]
	v_pk_fma_f32 v[70:71], v[74:75], v[170:171], v[70:71]
	v_pk_fma_f32 v[64:65], v[80:81], v[172:173], v[64:65]
	v_pk_fma_f32 v[66:67], v[82:83], v[174:175], v[66:67]
	v_cvt_pk_f16_f32 v68, v68, v69
	v_cvt_pk_f16_f32 v69, v70, v71
	v_cvt_pk_f16_f32 v70, v64, v65
	v_cvt_pk_f16_f32 v71, v66, v67
	ds_write_b128 v235, v[68:71] offset:64
	v_fma_mix_f32 v216, v68, 1.0, v216 op_sel_hi:[1,0,0]
	v_fma_mix_f32 v217, v68, v68, v217 op_sel_hi:[1,1,0]
	v_fma_mix_f32 v216, v68, 1.0, v216 op_sel:[1,0,0] op_sel_hi:[1,0,0]
	v_fma_mix_f32 v217, v68, v68, v217 op_sel:[1,1,0] op_sel_hi:[1,1,0]
	v_fma_mix_f32 v216, v69, 1.0, v216 op_sel_hi:[1,0,0]
	v_fma_mix_f32 v217, v69, v69, v217 op_sel_hi:[1,1,0]
	v_fma_mix_f32 v216, v69, 1.0, v216 op_sel:[1,0,0] op_sel_hi:[1,0,0]
	v_fma_mix_f32 v217, v69, v69, v217 op_sel:[1,1,0] op_sel_hi:[1,1,0]
	v_fma_mix_f32 v216, v70, 1.0, v216 op_sel_hi:[1,0,0]
	v_fma_mix_f32 v217, v70, v70, v217 op_sel_hi:[1,1,0]
	v_fma_mix_f32 v216, v70, 1.0, v216 op_sel:[1,0,0] op_sel_hi:[1,0,0]
	v_fma_mix_f32 v217, v70, v70, v217 op_sel:[1,1,0] op_sel_hi:[1,1,0]
	v_fma_mix_f32 v216, v71, 1.0, v216 op_sel_hi:[1,0,0]
	v_fma_mix_f32 v217, v71, v71, v217 op_sel_hi:[1,1,0]
	v_fma_mix_f32 v216, v71, 1.0, v216 op_sel:[1,0,0] op_sel_hi:[1,0,0]
	v_fma_mix_f32 v217, v71, v71, v217 op_sel:[1,1,0] op_sel_hi:[1,1,0]
	ds_read_b128 v[112:115], v236
	ds_read_b128 v[220:223], v236 offset:1152
	s_waitcnt vmcnt(13)
	v_cvt_f32_f16_e32 v72, v136
	v_cvt_f32_f16_sdwa v73, v136 dst_sel:DWORD dst_unused:UNUSED_PAD src0_sel:WORD_1
	v_cvt_f32_f16_e32 v74, v137
	v_cvt_f32_f16_sdwa v75, v137 dst_sel:DWORD dst_unused:UNUSED_PAD src0_sel:WORD_1
	v_cvt_f32_f16_e32 v80, v138
	v_cvt_f32_f16_sdwa v81, v138 dst_sel:DWORD dst_unused:UNUSED_PAD src0_sel:WORD_1
	v_cvt_f32_f16_e32 v82, v139
	v_cvt_f32_f16_sdwa v83, v139 dst_sel:DWORD dst_unused:UNUSED_PAD src0_sel:WORD_1
	v_sub_f32_e32 v72, v72, v198
	v_sub_f32_e32 v73, v73, v198
	v_sub_f32_e32 v74, v74, v198
	v_sub_f32_e32 v75, v75, v198
	v_sub_f32_e32 v80, v80, v198
	v_sub_f32_e32 v81, v81, v198
	v_sub_f32_e32 v82, v82, v198
	v_sub_f32_e32 v83, v83, v198
	v_pk_mul_f32 v[72:73], v[198:199], v[72:73] op_sel:[1,0]
	v_pk_mul_f32 v[74:75], v[198:199], v[74:75] op_sel:[1,0]
	v_pk_mul_f32 v[80:81], v[198:199], v[80:81] op_sel:[1,0]
	v_pk_mul_f32 v[82:83], v[198:199], v[82:83] op_sel:[1,0]
	v_pk_fma_f32 v[60:61], v[72:73], v[160:161], v[60:61]
	v_pk_fma_f32 v[62:63], v[74:75], v[162:163], v[62:63]
	v_pk_fma_f32 v[56:57], v[80:81], v[164:165], v[56:57]
	v_pk_fma_f32 v[58:59], v[82:83], v[166:167], v[58:59]
	v_cvt_pk_f16_f32 v60, v60, v61
	v_cvt_pk_f16_f32 v61, v62, v63
	v_cvt_pk_f16_f32 v62, v56, v57
	v_cvt_pk_f16_f32 v63, v58, v59
	s_waitcnt lgkmcnt(0)
	v_add_u32_e32 v83, 0x12000, v224
	buffer_store_dwordx4 v[112:115], v83, s[24:27], 0 offen nt
	v_add_u32_e32 v82, 0x15000, v224
	buffer_store_dwordx4 v[220:223], v82, s[24:27], 0 offen nt
	ds_write_b128 v235, v[60:63]
	v_fma_mix_f32 v218, v60, 1.0, 0 op_sel_hi:[1,0,0]
	v_fma_mix_f32 v219, v60, v60, 0 op_sel_hi:[1,1,0]
	v_fma_mix_f32 v218, v60, 1.0, v218 op_sel:[1,0,0] op_sel_hi:[1,0,0]
	v_fma_mix_f32 v219, v60, v60, v219 op_sel:[1,1,0] op_sel_hi:[1,1,0]
	v_fma_mix_f32 v218, v61, 1.0, v218 op_sel_hi:[1,0,0]
	v_fma_mix_f32 v219, v61, v61, v219 op_sel_hi:[1,1,0]
	v_fma_mix_f32 v218, v61, 1.0, v218 op_sel:[1,0,0] op_sel_hi:[1,0,0]
	v_fma_mix_f32 v219, v61, v61, v219 op_sel:[1,1,0] op_sel_hi:[1,1,0]
	v_fma_mix_f32 v218, v62, 1.0, v218 op_sel_hi:[1,0,0]
	v_fma_mix_f32 v219, v62, v62, v219 op_sel_hi:[1,1,0]
	v_fma_mix_f32 v218, v62, 1.0, v218 op_sel:[1,0,0] op_sel_hi:[1,0,0]
	v_fma_mix_f32 v219, v62, v62, v219 op_sel:[1,1,0] op_sel_hi:[1,1,0]
	v_fma_mix_f32 v218, v63, 1.0, v218 op_sel_hi:[1,0,0]
	v_fma_mix_f32 v219, v63, v63, v219 op_sel_hi:[1,1,0]
	v_fma_mix_f32 v218, v63, 1.0, v218 op_sel:[1,0,0] op_sel_hi:[1,0,0]
	v_fma_mix_f32 v219, v63, v63, v219 op_sel:[1,1,0] op_sel_hi:[1,1,0]
	s_waitcnt vmcnt(14)
	v_cvt_f32_f16_e32 v72, v148
	v_cvt_f32_f16_sdwa v73, v148 dst_sel:DWORD dst_unused:UNUSED_PAD src0_sel:WORD_1
	v_cvt_f32_f16_e32 v74, v149
	v_cvt_f32_f16_sdwa v75, v149 dst_sel:DWORD dst_unused:UNUSED_PAD src0_sel:WORD_1
	v_cvt_f32_f16_e32 v80, v150
	v_cvt_f32_f16_sdwa v81, v150 dst_sel:DWORD dst_unused:UNUSED_PAD src0_sel:WORD_1
	v_cvt_f32_f16_e32 v82, v151
	v_cvt_f32_f16_sdwa v83, v151 dst_sel:DWORD dst_unused:UNUSED_PAD src0_sel:WORD_1
	v_sub_f32_e32 v72, v72, v198
	v_sub_f32_e32 v73, v73, v198
	v_sub_f32_e32 v74, v74, v198
	v_sub_f32_e32 v75, v75, v198
	v_sub_f32_e32 v80, v80, v198
	v_sub_f32_e32 v81, v81, v198
	v_sub_f32_e32 v82, v82, v198
	v_sub_f32_e32 v83, v83, v198
	v_pk_mul_f32 v[72:73], v[198:199], v[72:73] op_sel:[1,0]
	v_pk_mul_f32 v[74:75], v[198:199], v[74:75] op_sel:[1,0]
	v_pk_mul_f32 v[80:81], v[198:199], v[80:81] op_sel:[1,0]
	v_pk_mul_f32 v[82:83], v[198:199], v[82:83] op_sel:[1,0]
	v_pk_fma_f32 v[52:53], v[72:73], v[168:169], v[52:53]
	v_pk_fma_f32 v[54:55], v[74:75], v[170:171], v[54:55]
	v_pk_fma_f32 v[48:49], v[80:81], v[172:173], v[48:49]
	v_pk_fma_f32 v[50:51], v[82:83], v[174:175], v[50:51]
	v_cvt_pk_f16_f32 v52, v52, v53
	v_cvt_pk_f16_f32 v53, v54, v55
	v_cvt_pk_f16_f32 v54, v48, v49
	v_cvt_pk_f16_f32 v55, v50, v51
	ds_write_b128 v235, v[52:55] offset:64
	v_fma_mix_f32 v218, v52, 1.0, v218 op_sel_hi:[1,0,0]
	v_fma_mix_f32 v219, v52, v52, v219 op_sel_hi:[1,1,0]
	v_fma_mix_f32 v218, v52, 1.0, v218 op_sel:[1,0,0] op_sel_hi:[1,0,0]
	v_fma_mix_f32 v219, v52, v52, v219 op_sel:[1,1,0] op_sel_hi:[1,1,0]
	v_fma_mix_f32 v218, v53, 1.0, v218 op_sel_hi:[1,0,0]
	v_fma_mix_f32 v219, v53, v53, v219 op_sel_hi:[1,1,0]
	v_fma_mix_f32 v218, v53, 1.0, v218 op_sel:[1,0,0] op_sel_hi:[1,0,0]
	v_fma_mix_f32 v219, v53, v53, v219 op_sel:[1,1,0] op_sel_hi:[1,1,0]
	v_fma_mix_f32 v218, v54, 1.0, v218 op_sel_hi:[1,0,0]
	v_fma_mix_f32 v219, v54, v54, v219 op_sel_hi:[1,1,0]
	v_fma_mix_f32 v218, v54, 1.0, v218 op_sel:[1,0,0] op_sel_hi:[1,0,0]
	v_fma_mix_f32 v219, v54, v54, v219 op_sel:[1,1,0] op_sel_hi:[1,1,0]
	v_fma_mix_f32 v218, v55, 1.0, v218 op_sel_hi:[1,0,0]
	v_fma_mix_f32 v219, v55, v55, v219 op_sel_hi:[1,1,0]
	v_fma_mix_f32 v218, v55, 1.0, v218 op_sel:[1,0,0] op_sel_hi:[1,0,0]
	v_fma_mix_f32 v219, v55, v55, v219 op_sel:[1,1,0] op_sel_hi:[1,1,0]
	ds_read_b128 v[124:127], v236
	ds_read_b128 v[116:119], v236 offset:1152
	s_waitcnt vmcnt(13)
	v_cvt_f32_f16_e32 v72, v152
	v_cvt_f32_f16_sdwa v73, v152 dst_sel:DWORD dst_unused:UNUSED_PAD src0_sel:WORD_1
	v_cvt_f32_f16_e32 v74, v153
	v_cvt_f32_f16_sdwa v75, v153 dst_sel:DWORD dst_unused:UNUSED_PAD src0_sel:WORD_1
	v_cvt_f32_f16_e32 v80, v154
	v_cvt_f32_f16_sdwa v81, v154 dst_sel:DWORD dst_unused:UNUSED_PAD src0_sel:WORD_1
	v_cvt_f32_f16_e32 v82, v155
	v_cvt_f32_f16_sdwa v83, v155 dst_sel:DWORD dst_unused:UNUSED_PAD src0_sel:WORD_1
	v_sub_f32_e32 v72, v72, v200
	v_sub_f32_e32 v73, v73, v200
	v_sub_f32_e32 v74, v74, v200
	v_sub_f32_e32 v75, v75, v200
	v_sub_f32_e32 v80, v80, v200
	v_sub_f32_e32 v81, v81, v200
	v_sub_f32_e32 v82, v82, v200
	v_sub_f32_e32 v83, v83, v200
	v_pk_mul_f32 v[72:73], v[200:201], v[72:73] op_sel:[1,0]
	v_pk_mul_f32 v[74:75], v[200:201], v[74:75] op_sel:[1,0]
	v_pk_mul_f32 v[80:81], v[200:201], v[80:81] op_sel:[1,0]
	v_pk_mul_f32 v[82:83], v[200:201], v[82:83] op_sel:[1,0]
	v_pk_fma_f32 v[44:45], v[72:73], v[160:161], v[44:45]
	v_pk_fma_f32 v[46:47], v[74:75], v[162:163], v[46:47]
	v_pk_fma_f32 v[40:41], v[80:81], v[164:165], v[40:41]
	v_pk_fma_f32 v[42:43], v[82:83], v[166:167], v[42:43]
	v_cvt_pk_f16_f32 v44, v44, v45
	v_cvt_pk_f16_f32 v45, v46, v47
	v_cvt_pk_f16_f32 v46, v40, v41
	v_cvt_pk_f16_f32 v47, v42, v43
	s_waitcnt lgkmcnt(0)
	v_add_u32_e32 v83, 0x30000, v224
	buffer_store_dwordx4 v[124:127], v83, s[24:27], 0 offen nt
	v_add_u32_e32 v82, 0x33000, v224
	buffer_store_dwordx4 v[116:119], v82, s[24:27], 0 offen nt
	ds_write_b128 v235, v[44:47]
	v_fma_mix_f32 v208, v44, 1.0, 0 op_sel_hi:[1,0,0]
	v_fma_mix_f32 v209, v44, v44, 0 op_sel_hi:[1,1,0]
	v_fma_mix_f32 v208, v44, 1.0, v208 op_sel:[1,0,0] op_sel_hi:[1,0,0]
	v_fma_mix_f32 v209, v44, v44, v209 op_sel:[1,1,0] op_sel_hi:[1,1,0]
	v_fma_mix_f32 v208, v45, 1.0, v208 op_sel_hi:[1,0,0]
	v_fma_mix_f32 v209, v45, v45, v209 op_sel_hi:[1,1,0]
	v_fma_mix_f32 v208, v45, 1.0, v208 op_sel:[1,0,0] op_sel_hi:[1,0,0]
	v_fma_mix_f32 v209, v45, v45, v209 op_sel:[1,1,0] op_sel_hi:[1,1,0]
	v_fma_mix_f32 v208, v46, 1.0, v208 op_sel_hi:[1,0,0]
	v_fma_mix_f32 v209, v46, v46, v209 op_sel_hi:[1,1,0]
	v_fma_mix_f32 v208, v46, 1.0, v208 op_sel:[1,0,0] op_sel_hi:[1,0,0]
	v_fma_mix_f32 v209, v46, v46, v209 op_sel:[1,1,0] op_sel_hi:[1,1,0]
	v_fma_mix_f32 v208, v47, 1.0, v208 op_sel_hi:[1,0,0]
	v_fma_mix_f32 v209, v47, v47, v209 op_sel_hi:[1,1,0]
	v_fma_mix_f32 v208, v47, 1.0, v208 op_sel:[1,0,0] op_sel_hi:[1,0,0]
	v_fma_mix_f32 v209, v47, v47, v209 op_sel:[1,1,0] op_sel_hi:[1,1,0]
	s_waitcnt vmcnt(14)
	v_cvt_f32_f16_e32 v72, v156
	v_cvt_f32_f16_sdwa v73, v156 dst_sel:DWORD dst_unused:UNUSED_PAD src0_sel:WORD_1
	v_cvt_f32_f16_e32 v74, v157
	v_cvt_f32_f16_sdwa v75, v157 dst_sel:DWORD dst_unused:UNUSED_PAD src0_sel:WORD_1
	v_cvt_f32_f16_e32 v80, v158
	v_cvt_f32_f16_sdwa v81, v158 dst_sel:DWORD dst_unused:UNUSED_PAD src0_sel:WORD_1
	v_cvt_f32_f16_e32 v82, v159
	v_cvt_f32_f16_sdwa v83, v159 dst_sel:DWORD dst_unused:UNUSED_PAD src0_sel:WORD_1
	v_sub_f32_e32 v72, v72, v200
	v_sub_f32_e32 v73, v73, v200
	v_sub_f32_e32 v74, v74, v200
	v_sub_f32_e32 v75, v75, v200
	v_sub_f32_e32 v80, v80, v200
	v_sub_f32_e32 v81, v81, v200
	v_sub_f32_e32 v82, v82, v200
	v_sub_f32_e32 v83, v83, v200
	v_pk_mul_f32 v[72:73], v[200:201], v[72:73] op_sel:[1,0]
	v_pk_mul_f32 v[74:75], v[200:201], v[74:75] op_sel:[1,0]
	v_pk_mul_f32 v[80:81], v[200:201], v[80:81] op_sel:[1,0]
	v_pk_mul_f32 v[82:83], v[200:201], v[82:83] op_sel:[1,0]
	v_pk_fma_f32 v[36:37], v[72:73], v[168:169], v[36:37]
	v_pk_fma_f32 v[38:39], v[74:75], v[170:171], v[38:39]
	v_pk_fma_f32 v[32:33], v[80:81], v[172:173], v[32:33]
	v_pk_fma_f32 v[34:35], v[82:83], v[174:175], v[34:35]
	v_cvt_pk_f16_f32 v36, v36, v37
	v_cvt_pk_f16_f32 v37, v38, v39
	v_cvt_pk_f16_f32 v38, v32, v33
	v_cvt_pk_f16_f32 v39, v34, v35
	ds_write_b128 v235, v[36:39] offset:64
	v_fma_mix_f32 v208, v36, 1.0, v208 op_sel_hi:[1,0,0]
	v_fma_mix_f32 v209, v36, v36, v209 op_sel_hi:[1,1,0]
	v_fma_mix_f32 v208, v36, 1.0, v208 op_sel:[1,0,0] op_sel_hi:[1,0,0]
	v_fma_mix_f32 v209, v36, v36, v209 op_sel:[1,1,0] op_sel_hi:[1,1,0]
	v_fma_mix_f32 v208, v37, 1.0, v208 op_sel_hi:[1,0,0]
	v_fma_mix_f32 v209, v37, v37, v209 op_sel_hi:[1,1,0]
	v_fma_mix_f32 v208, v37, 1.0, v208 op_sel:[1,0,0] op_sel_hi:[1,0,0]
	v_fma_mix_f32 v209, v37, v37, v209 op_sel:[1,1,0] op_sel_hi:[1,1,0]
	v_fma_mix_f32 v208, v38, 1.0, v208 op_sel_hi:[1,0,0]
	v_fma_mix_f32 v209, v38, v38, v209 op_sel_hi:[1,1,0]
	v_fma_mix_f32 v208, v38, 1.0, v208 op_sel:[1,0,0] op_sel_hi:[1,0,0]
	v_fma_mix_f32 v209, v38, v38, v209 op_sel:[1,1,0] op_sel_hi:[1,1,0]
	v_fma_mix_f32 v208, v39, 1.0, v208 op_sel_hi:[1,0,0]
	v_fma_mix_f32 v209, v39, v39, v209 op_sel_hi:[1,1,0]
	v_fma_mix_f32 v208, v39, 1.0, v208 op_sel:[1,0,0] op_sel_hi:[1,0,0]
	v_fma_mix_f32 v209, v39, v39, v209 op_sel:[1,1,0] op_sel_hi:[1,1,0]
	ds_read_b128 v[128:131], v236
	ds_read_b128 v[104:107], v236 offset:1152
	s_waitcnt vmcnt(11)
	v_cvt_f32_f16_e32 v72, v212
	v_cvt_f32_f16_sdwa v73, v212 dst_sel:DWORD dst_unused:UNUSED_PAD src0_sel:WORD_1
	v_cvt_f32_f16_e32 v74, v213
	v_cvt_f32_f16_sdwa v75, v213 dst_sel:DWORD dst_unused:UNUSED_PAD src0_sel:WORD_1
	v_cvt_f32_f16_e32 v80, v214
	v_cvt_f32_f16_sdwa v81, v214 dst_sel:DWORD dst_unused:UNUSED_PAD src0_sel:WORD_1
	v_cvt_f32_f16_e32 v82, v215
	v_cvt_f32_f16_sdwa v83, v215 dst_sel:DWORD dst_unused:UNUSED_PAD src0_sel:WORD_1
	v_sub_f32_e32 v72, v72, v202
	v_sub_f32_e32 v73, v73, v202
	v_sub_f32_e32 v74, v74, v202
	v_sub_f32_e32 v75, v75, v202
	v_sub_f32_e32 v80, v80, v202
	v_sub_f32_e32 v81, v81, v202
	v_sub_f32_e32 v82, v82, v202
	v_sub_f32_e32 v83, v83, v202
	v_pk_mul_f32 v[72:73], v[202:203], v[72:73] op_sel:[1,0]
	v_pk_mul_f32 v[74:75], v[202:203], v[74:75] op_sel:[1,0]
	v_pk_mul_f32 v[80:81], v[202:203], v[80:81] op_sel:[1,0]
	v_pk_mul_f32 v[82:83], v[202:203], v[82:83] op_sel:[1,0]
	v_pk_fma_f32 v[28:29], v[72:73], v[160:161], v[28:29]
	v_pk_fma_f32 v[30:31], v[74:75], v[162:163], v[30:31]
	v_pk_fma_f32 v[24:25], v[80:81], v[164:165], v[24:25]
	v_pk_fma_f32 v[26:27], v[82:83], v[166:167], v[26:27]
	v_cvt_pk_f16_f32 v28, v28, v29
	v_cvt_pk_f16_f32 v29, v30, v31
	v_cvt_pk_f16_f32 v30, v24, v25
	v_cvt_pk_f16_f32 v31, v26, v27
	s_waitcnt lgkmcnt(0)
	v_add_u32_e32 v83, 0x36000, v224
	buffer_store_dwordx4 v[128:131], v83, s[24:27], 0 offen nt
	v_add_u32_e32 v82, 0x39000, v224
	buffer_store_dwordx4 v[104:107], v82, s[24:27], 0 offen nt
	ds_write_b128 v235, v[28:31]
	v_fma_mix_f32 v210, v28, 1.0, 0 op_sel_hi:[1,0,0]
	v_fma_mix_f32 v211, v28, v28, 0 op_sel_hi:[1,1,0]
	v_fma_mix_f32 v210, v28, 1.0, v210 op_sel:[1,0,0] op_sel_hi:[1,0,0]
	v_fma_mix_f32 v211, v28, v28, v211 op_sel:[1,1,0] op_sel_hi:[1,1,0]
	v_fma_mix_f32 v210, v29, 1.0, v210 op_sel_hi:[1,0,0]
	v_fma_mix_f32 v211, v29, v29, v211 op_sel_hi:[1,1,0]
	v_fma_mix_f32 v210, v29, 1.0, v210 op_sel:[1,0,0] op_sel_hi:[1,0,0]
	v_fma_mix_f32 v211, v29, v29, v211 op_sel:[1,1,0] op_sel_hi:[1,1,0]
	v_fma_mix_f32 v210, v30, 1.0, v210 op_sel_hi:[1,0,0]
	v_fma_mix_f32 v211, v30, v30, v211 op_sel_hi:[1,1,0]
	v_fma_mix_f32 v210, v30, 1.0, v210 op_sel:[1,0,0] op_sel_hi:[1,0,0]
	v_fma_mix_f32 v211, v30, v30, v211 op_sel:[1,1,0] op_sel_hi:[1,1,0]
	v_fma_mix_f32 v210, v31, 1.0, v210 op_sel_hi:[1,0,0]
	v_fma_mix_f32 v211, v31, v31, v211 op_sel_hi:[1,1,0]
	v_fma_mix_f32 v210, v31, 1.0, v210 op_sel:[1,0,0] op_sel_hi:[1,0,0]
	v_fma_mix_f32 v211, v31, v31, v211 op_sel:[1,1,0] op_sel_hi:[1,1,0]
	s_waitcnt vmcnt(12)
	v_cvt_f32_f16_e32 v72, v144
	v_cvt_f32_f16_sdwa v73, v144 dst_sel:DWORD dst_unused:UNUSED_PAD src0_sel:WORD_1
	v_cvt_f32_f16_e32 v74, v145
	v_cvt_f32_f16_sdwa v75, v145 dst_sel:DWORD dst_unused:UNUSED_PAD src0_sel:WORD_1
	v_cvt_f32_f16_e32 v80, v146
	v_cvt_f32_f16_sdwa v81, v146 dst_sel:DWORD dst_unused:UNUSED_PAD src0_sel:WORD_1
	v_cvt_f32_f16_e32 v82, v147
	v_cvt_f32_f16_sdwa v83, v147 dst_sel:DWORD dst_unused:UNUSED_PAD src0_sel:WORD_1
	v_sub_f32_e32 v72, v72, v202
	v_sub_f32_e32 v73, v73, v202
	v_sub_f32_e32 v74, v74, v202
	v_sub_f32_e32 v75, v75, v202
	v_sub_f32_e32 v80, v80, v202
	v_sub_f32_e32 v81, v81, v202
	v_sub_f32_e32 v82, v82, v202
	v_sub_f32_e32 v83, v83, v202
	v_pk_mul_f32 v[72:73], v[202:203], v[72:73] op_sel:[1,0]
	v_pk_mul_f32 v[74:75], v[202:203], v[74:75] op_sel:[1,0]
	v_pk_mul_f32 v[80:81], v[202:203], v[80:81] op_sel:[1,0]
	v_pk_mul_f32 v[82:83], v[202:203], v[82:83] op_sel:[1,0]
	v_pk_fma_f32 v[20:21], v[72:73], v[168:169], v[20:21]
	v_pk_fma_f32 v[22:23], v[74:75], v[170:171], v[22:23]
	v_pk_fma_f32 v[16:17], v[80:81], v[172:173], v[16:17]
	v_pk_fma_f32 v[18:19], v[82:83], v[174:175], v[18:19]
	v_cvt_pk_f16_f32 v20, v20, v21
	v_cvt_pk_f16_f32 v21, v22, v23
	v_cvt_pk_f16_f32 v22, v16, v17
	v_cvt_pk_f16_f32 v23, v18, v19
	ds_write_b128 v235, v[20:23] offset:64
	v_fma_mix_f32 v210, v20, 1.0, v210 op_sel_hi:[1,0,0]
	v_fma_mix_f32 v211, v20, v20, v211 op_sel_hi:[1,1,0]
	v_fma_mix_f32 v210, v20, 1.0, v210 op_sel:[1,0,0] op_sel_hi:[1,0,0]
	v_fma_mix_f32 v211, v20, v20, v211 op_sel:[1,1,0] op_sel_hi:[1,1,0]
	v_fma_mix_f32 v210, v21, 1.0, v210 op_sel_hi:[1,0,0]
	v_fma_mix_f32 v211, v21, v21, v211 op_sel_hi:[1,1,0]
	v_fma_mix_f32 v210, v21, 1.0, v210 op_sel:[1,0,0] op_sel_hi:[1,0,0]
	v_fma_mix_f32 v211, v21, v21, v211 op_sel:[1,1,0] op_sel_hi:[1,1,0]
	v_fma_mix_f32 v210, v22, 1.0, v210 op_sel_hi:[1,0,0]
	v_fma_mix_f32 v211, v22, v22, v211 op_sel_hi:[1,1,0]
	v_fma_mix_f32 v210, v22, 1.0, v210 op_sel:[1,0,0] op_sel_hi:[1,0,0]
	v_fma_mix_f32 v211, v22, v22, v211 op_sel:[1,1,0] op_sel_hi:[1,1,0]
	v_fma_mix_f32 v210, v23, 1.0, v210 op_sel_hi:[1,0,0]
	v_fma_mix_f32 v211, v23, v23, v211 op_sel_hi:[1,1,0]
	v_fma_mix_f32 v210, v23, 1.0, v210 op_sel:[1,0,0] op_sel_hi:[1,0,0]
	v_fma_mix_f32 v211, v23, v23, v211 op_sel:[1,1,0] op_sel_hi:[1,1,0]
	ds_read_b128 v[240:243], v236
	ds_read_b128 v[96:99], v236 offset:1152
	s_waitcnt vmcnt(11)
	v_cvt_f32_f16_e32 v72, v132
	v_cvt_f32_f16_sdwa v73, v132 dst_sel:DWORD dst_unused:UNUSED_PAD src0_sel:WORD_1
	v_cvt_f32_f16_e32 v74, v133
	v_cvt_f32_f16_sdwa v75, v133 dst_sel:DWORD dst_unused:UNUSED_PAD src0_sel:WORD_1
	v_cvt_f32_f16_e32 v80, v134
	v_cvt_f32_f16_sdwa v81, v134 dst_sel:DWORD dst_unused:UNUSED_PAD src0_sel:WORD_1
	v_cvt_f32_f16_e32 v82, v135
	v_cvt_f32_f16_sdwa v83, v135 dst_sel:DWORD dst_unused:UNUSED_PAD src0_sel:WORD_1
	v_sub_f32_e32 v72, v72, v204
	v_sub_f32_e32 v73, v73, v204
	v_sub_f32_e32 v74, v74, v204
	v_sub_f32_e32 v75, v75, v204
	v_sub_f32_e32 v80, v80, v204
	v_sub_f32_e32 v81, v81, v204
	v_sub_f32_e32 v82, v82, v204
	v_sub_f32_e32 v83, v83, v204
	v_pk_mul_f32 v[72:73], v[204:205], v[72:73] op_sel:[1,0]
	v_pk_mul_f32 v[74:75], v[204:205], v[74:75] op_sel:[1,0]
	v_pk_mul_f32 v[80:81], v[204:205], v[80:81] op_sel:[1,0]
	v_pk_mul_f32 v[82:83], v[204:205], v[82:83] op_sel:[1,0]
	v_pk_fma_f32 v[12:13], v[72:73], v[160:161], v[12:13]
	v_pk_fma_f32 v[14:15], v[74:75], v[162:163], v[14:15]
	v_pk_fma_f32 v[8:9], v[80:81], v[164:165], v[8:9]
	v_pk_fma_f32 v[10:11], v[82:83], v[166:167], v[10:11]
	v_cvt_pk_f16_f32 v12, v12, v13
	v_cvt_pk_f16_f32 v13, v14, v15
	v_cvt_pk_f16_f32 v14, v8, v9
	v_cvt_pk_f16_f32 v15, v10, v11
	s_waitcnt lgkmcnt(0)
	v_add_u32_e32 v83, 0x3c000, v224
	buffer_store_dwordx4 v[240:243], v83, s[24:27], 0 offen nt
	v_add_u32_e32 v82, 0x3f000, v224
	buffer_store_dwordx4 v[96:99], v82, s[24:27], 0 offen nt
	ds_write_b128 v235, v[12:15]
	v_fma_mix_f32 v244, v12, 1.0, 0 op_sel_hi:[1,0,0]
	v_fma_mix_f32 v245, v12, v12, 0 op_sel_hi:[1,1,0]
	v_fma_mix_f32 v244, v12, 1.0, v244 op_sel:[1,0,0] op_sel_hi:[1,0,0]
	v_fma_mix_f32 v245, v12, v12, v245 op_sel:[1,1,0] op_sel_hi:[1,1,0]
	v_fma_mix_f32 v244, v13, 1.0, v244 op_sel_hi:[1,0,0]
	v_fma_mix_f32 v245, v13, v13, v245 op_sel_hi:[1,1,0]
	v_fma_mix_f32 v244, v13, 1.0, v244 op_sel:[1,0,0] op_sel_hi:[1,0,0]
	v_fma_mix_f32 v245, v13, v13, v245 op_sel:[1,1,0] op_sel_hi:[1,1,0]
	v_fma_mix_f32 v244, v14, 1.0, v244 op_sel_hi:[1,0,0]
	v_fma_mix_f32 v245, v14, v14, v245 op_sel_hi:[1,1,0]
	v_fma_mix_f32 v244, v14, 1.0, v244 op_sel:[1,0,0] op_sel_hi:[1,0,0]
	v_fma_mix_f32 v245, v14, v14, v245 op_sel:[1,1,0] op_sel_hi:[1,1,0]
	v_fma_mix_f32 v244, v15, 1.0, v244 op_sel_hi:[1,0,0]
	v_fma_mix_f32 v245, v15, v15, v245 op_sel_hi:[1,1,0]
	v_fma_mix_f32 v244, v15, 1.0, v244 op_sel:[1,0,0] op_sel_hi:[1,0,0]
	v_fma_mix_f32 v245, v15, v15, v245 op_sel:[1,1,0] op_sel_hi:[1,1,0]
	s_waitcnt vmcnt(12)
	v_cvt_f32_f16_e32 v72, v88
	v_cvt_f32_f16_sdwa v73, v88 dst_sel:DWORD dst_unused:UNUSED_PAD src0_sel:WORD_1
	v_cvt_f32_f16_e32 v74, v89
	v_cvt_f32_f16_sdwa v75, v89 dst_sel:DWORD dst_unused:UNUSED_PAD src0_sel:WORD_1
	v_cvt_f32_f16_e32 v80, v90
	v_cvt_f32_f16_sdwa v81, v90 dst_sel:DWORD dst_unused:UNUSED_PAD src0_sel:WORD_1
	v_cvt_f32_f16_e32 v82, v91
	v_cvt_f32_f16_sdwa v83, v91 dst_sel:DWORD dst_unused:UNUSED_PAD src0_sel:WORD_1
	v_sub_f32_e32 v72, v72, v204
	v_sub_f32_e32 v73, v73, v204
	v_sub_f32_e32 v74, v74, v204
	v_sub_f32_e32 v75, v75, v204
	v_sub_f32_e32 v80, v80, v204
	v_sub_f32_e32 v81, v81, v204
	v_sub_f32_e32 v82, v82, v204
	v_sub_f32_e32 v83, v83, v204
	v_pk_mul_f32 v[72:73], v[204:205], v[72:73] op_sel:[1,0]
	v_pk_mul_f32 v[74:75], v[204:205], v[74:75] op_sel:[1,0]
	v_pk_mul_f32 v[80:81], v[204:205], v[80:81] op_sel:[1,0]
	v_pk_mul_f32 v[82:83], v[204:205], v[82:83] op_sel:[1,0]
	v_pk_fma_f32 v[4:5], v[72:73], v[168:169], v[4:5]
	v_pk_fma_f32 v[6:7], v[74:75], v[170:171], v[6:7]
	v_pk_fma_f32 v[0:1], v[80:81], v[172:173], v[0:1]
	v_pk_fma_f32 v[2:3], v[82:83], v[174:175], v[2:3]
	v_cvt_pk_f16_f32 v4, v4, v5
	v_cvt_pk_f16_f32 v5, v6, v7
	v_cvt_pk_f16_f32 v6, v0, v1
	v_cvt_pk_f16_f32 v7, v2, v3
	ds_write_b128 v235, v[4:7] offset:64
	v_fma_mix_f32 v244, v4, 1.0, v244 op_sel_hi:[1,0,0]
	v_fma_mix_f32 v245, v4, v4, v245 op_sel_hi:[1,1,0]
	v_fma_mix_f32 v244, v4, 1.0, v244 op_sel:[1,0,0] op_sel_hi:[1,0,0]
	v_fma_mix_f32 v245, v4, v4, v245 op_sel:[1,1,0] op_sel_hi:[1,1,0]
	v_fma_mix_f32 v244, v5, 1.0, v244 op_sel_hi:[1,0,0]
	v_fma_mix_f32 v245, v5, v5, v245 op_sel_hi:[1,1,0]
	v_fma_mix_f32 v244, v5, 1.0, v244 op_sel:[1,0,0] op_sel_hi:[1,0,0]
	v_fma_mix_f32 v245, v5, v5, v245 op_sel:[1,1,0] op_sel_hi:[1,1,0]
	v_fma_mix_f32 v244, v6, 1.0, v244 op_sel_hi:[1,0,0]
	v_fma_mix_f32 v245, v6, v6, v245 op_sel_hi:[1,1,0]
	v_fma_mix_f32 v244, v6, 1.0, v244 op_sel:[1,0,0] op_sel_hi:[1,0,0]
	v_fma_mix_f32 v245, v6, v6, v245 op_sel:[1,1,0] op_sel_hi:[1,1,0]
	v_fma_mix_f32 v244, v7, 1.0, v244 op_sel_hi:[1,0,0]
	v_fma_mix_f32 v245, v7, v7, v245 op_sel_hi:[1,1,0]
	v_fma_mix_f32 v244, v7, 1.0, v244 op_sel:[1,0,0] op_sel_hi:[1,0,0]
	v_fma_mix_f32 v245, v7, v7, v245 op_sel:[1,1,0] op_sel_hi:[1,1,0]
	ds_read_b128 v[108:111], v236
	ds_read_b128 v[100:103], v236 offset:1152
	s_waitcnt lgkmcnt(0)
	v_add_u32_e32 v83, 0x42000, v224
	buffer_store_dwordx4 v[108:111], v83, s[24:27], 0 offen nt
	v_add_u32_e32 v82, 0x45000, v224
	buffer_store_dwordx4 v[100:103], v82, s[24:27], 0 offen nt
	v_xor_b32_e32 v225, 16, v234
	v_lshlrev_b32_e32 v225, 2, v225
	v_xor_b32_e32 v246, 32, v234
	v_lshlrev_b32_e32 v246, 2, v246
	ds_bpermute_b32 v92, v225, v206
	ds_bpermute_b32 v93, v225, v207
	ds_bpermute_b32 v94, v225, v140
	ds_bpermute_b32 v95, v225, v141
	ds_bpermute_b32 v120, v225, v142
	ds_bpermute_b32 v121, v225, v143
	ds_bpermute_b32 v122, v225, v216
	ds_bpermute_b32 v123, v225, v217
	s_waitcnt lgkmcnt(0)
	v_pk_add_f32 v[206:207], v[206:207], v[92:93]
	v_pk_add_f32 v[140:141], v[140:141], v[94:95]
	v_pk_add_f32 v[142:143], v[142:143], v[120:121]
	v_pk_add_f32 v[216:217], v[216:217], v[122:123]
	ds_bpermute_b32 v92, v225, v218
	ds_bpermute_b32 v93, v225, v219
	ds_bpermute_b32 v94, v225, v208
	ds_bpermute_b32 v95, v225, v209
	ds_bpermute_b32 v120, v225, v210
	ds_bpermute_b32 v121, v225, v211
	ds_bpermute_b32 v122, v225, v244
	ds_bpermute_b32 v123, v225, v245
	s_waitcnt lgkmcnt(0)
	v_pk_add_f32 v[218:219], v[218:219], v[92:93]
	v_pk_add_f32 v[208:209], v[208:209], v[94:95]
	v_pk_add_f32 v[210:211], v[210:211], v[120:121]
	v_pk_add_f32 v[244:245], v[244:245], v[122:123]
	ds_bpermute_b32 v92, v246, v206
	ds_bpermute_b32 v93, v246, v207
	ds_bpermute_b32 v94, v246, v140
	ds_bpermute_b32 v95, v246, v141
	ds_bpermute_b32 v120, v246, v142
	ds_bpermute_b32 v121, v246, v143
	ds_bpermute_b32 v122, v246, v216
	ds_bpermute_b32 v123, v246, v217
	s_waitcnt lgkmcnt(0)
	v_pk_add_f32 v[206:207], v[206:207], v[92:93]
	v_pk_add_f32 v[140:141], v[140:141], v[94:95]
	v_pk_add_f32 v[142:143], v[142:143], v[120:121]
	v_pk_add_f32 v[216:217], v[216:217], v[122:123]
	ds_bpermute_b32 v92, v246, v218
	ds_bpermute_b32 v93, v246, v219
	ds_bpermute_b32 v94, v246, v208
	ds_bpermute_b32 v95, v246, v209
	ds_bpermute_b32 v120, v246, v210
	ds_bpermute_b32 v121, v246, v211
	ds_bpermute_b32 v122, v246, v244
	ds_bpermute_b32 v123, v246, v245
	s_waitcnt lgkmcnt(0)
	v_pk_add_f32 v[218:219], v[218:219], v[92:93]
	v_pk_add_f32 v[208:209], v[208:209], v[94:95]
	v_pk_add_f32 v[210:211], v[210:211], v[120:121]
	v_pk_add_f32 v[244:245], v[244:245], v[122:123]
	s_mov_b64 exec, 0xffff
	global_store_dwordx2 v190, v[206:207], s[100:101] offset:0
	global_store_dwordx2 v190, v[140:141], s[100:101] offset:128
	global_store_dwordx2 v190, v[142:143], s[100:101] offset:256
	global_store_dwordx2 v190, v[216:217], s[100:101] offset:384
	global_store_dwordx2 v190, v[218:219], s[100:101] offset:1024
	global_store_dwordx2 v190, v[208:209], s[100:101] offset:1152
	global_store_dwordx2 v190, v[210:211], s[100:101] offset:1280
	global_store_dwordx2 v190, v[244:245], s[100:101] offset:1408
	s_mov_b64 exec, -1
	s_mov_b32 s83, s81
	s_mov_b32 s84, s82
	s_mov_b64 s[40:41], s[0:1]
	s_mov_b64 s[38:39], s[8:9]
	s_mov_b64 vcc, s[6:7]
	s_cbranch_vccz .LBB10_12
	s_waitcnt vmcnt(0)
	s_cmpk_gt_u32 s44, 0xff
	s_cbranch_scc1 .LBB10_31
	s_barrier
